# GEMM unit boundary: epilogue waits vmcnt(#stores) for tile DMAs, next unit's first two K-loop vmcnt waits skipped in trip 0 (all 4 GEMM phases)
# speedup vs baseline: 1.0066x; 1.0066x over previous
; template <class Epi, bool GATHER, bool EXPERT, bool FP8>
; DI void gemm_phase(LAS unsigned char* lds, const Gemm g, const StaticOrder& S, const Epi& E) {
;     ...
; #pragma unroll
;         for (int a = 0; a < 2; ++a)
; #pragma unroll
;             for (int b = 0; b < 2; ++b)
; #pragma unroll
;                 for (int m = 0; m < 4; ++m)
; #pragma unroll
;                     for (int n = 0; n < 2; ++n) acc[a][b][m][n] = (f32x4){0.f, 0.f, 0.f, 0.f};
;         cur = nxt; cA = nA; cB = nB; ++ui;
.LBB0_114:
	s_ashr_i32 s41, s40, 31
	s_lshl_b64 s[0:1], s[40:41], 20
	s_add_u32 s5, s49, s0
	s_addc_u32 s15, s50, s1
	s_and_b64 s[0:1], s[2:3], exec
	s_cselect_b32 s42, s5, s6
	s_cselect_b32 s43, s15, s7
	s_ashr_i32 s39, s38, 31
	s_lshl_b64 s[0:1], s[38:39], 20
	s_add_u32 s5, s51, s0
	s_addc_u32 s15, s52, s1
	s_and_b64 s[0:1], s[2:3], exec
	s_cselect_b32 s44, s5, s8
	s_cselect_b32 s45, s15, s9
	s_add_u32 s5, s8, 0x100
	.p2align 8
	s_addc_u32 s15, s9, 0
	s_add_u32 s6, s6, 0x80
	v_mov_b32_e32 v2, 0
	s_addc_u32 s7, s7, 0
	s_mov_b32 s18, -2
	v_mov_b32_e32 v3, v2
	v_mov_b32_e32 v4, v2
	v_mov_b32_e32 v5, v2
	v_mov_b32_e32 v6, v2
	v_mov_b32_e32 v7, v2
	v_mov_b32_e32 v8, v2
	v_mov_b32_e32 v9, v2
	v_mov_b32_e32 v10, v2
	v_mov_b32_e32 v11, v2
	v_mov_b32_e32 v12, v2
	v_mov_b32_e32 v13, v2
	v_mov_b32_e32 v18, v2
	v_mov_b32_e32 v19, v2
	v_mov_b32_e32 v20, v2
	v_mov_b32_e32 v21, v2
	v_mov_b32_e32 v26, v2
	v_mov_b32_e32 v27, v2
	v_mov_b32_e32 v28, v2
	v_mov_b32_e32 v29, v2
	s_waitcnt vmcnt(0)
	v_mov_b32_e32 v34, v2
	v_mov_b32_e32 v35, v2
	v_mov_b32_e32 v36, v2
	v_mov_b32_e32 v37, v2
	v_mov_b32_e32 v42, v2
	v_mov_b32_e32 v43, v2
	v_mov_b32_e32 v44, v2
	v_mov_b32_e32 v45, v2
	v_mov_b32_e32 v50, v2
	v_mov_b32_e32 v51, v2
	v_mov_b32_e32 v52, v2
	v_mov_b32_e32 v53, v2
	v_mov_b32_e32 v14, v2
	v_mov_b32_e32 v15, v2
	v_mov_b32_e32 v16, v2
	v_mov_b32_e32 v17, v2
	v_mov_b32_e32 v22, v2
	v_mov_b32_e32 v23, v2
	v_mov_b32_e32 v24, v2
	v_mov_b32_e32 v25, v2
	v_mov_b32_e32 v30, v2
	v_mov_b32_e32 v31, v2
	v_mov_b32_e32 v32, v2
	v_mov_b32_e32 v33, v2
	v_mov_b32_e32 v38, v2
	v_mov_b32_e32 v39, v2
	v_mov_b32_e32 v40, v2
	v_mov_b32_e32 v41, v2
	v_mov_b32_e32 v46, v2
	v_mov_b32_e32 v47, v2
	v_mov_b32_e32 v48, v2
	v_mov_b32_e32 v49, v2
	v_mov_b32_e32 v54, v2
	v_mov_b32_e32 v55, v2
	v_mov_b32_e32 v56, v2
	v_mov_b32_e32 v57, v2
	v_mov_b32_e32 v58, v2
	v_mov_b32_e32 v59, v2
	v_mov_b32_e32 v60, v2
	v_mov_b32_e32 v61, v2
	v_mov_b32_e32 v62, v2
	v_mov_b32_e32 v63, v2
	v_mov_b32_e32 v64, v2
	v_mov_b32_e32 v65, v2
	v_mov_b32_e32 v66, v2
	v_mov_b32_e32 v67, v2
	v_mov_b32_e32 v68, v2
	v_mov_b32_e32 v69, v2
	v_mov_b32_e32 v70, v2
	v_mov_b32_e32 v71, v2
	v_mov_b32_e32 v72, v2
	v_mov_b32_e32 v73, v2
	v_mov_b32_e32 v74, v2
	v_mov_b32_e32 v75, v2
	v_mov_b32_e32 v76, v2
	v_mov_b32_e32 v77, v2
	v_mov_b32_e32 v82, v2
	v_mov_b32_e32 v83, v2
	v_mov_b32_e32 v84, v2
	v_mov_b32_e32 v85, v2
	v_mov_b32_e32 v90, v2
	v_mov_b32_e32 v91, v2
	v_mov_b32_e32 v92, v2
	v_mov_b32_e32 v93, v2
	v_mov_b32_e32 v98, v2
	v_mov_b32_e32 v99, v2
	v_mov_b32_e32 v100, v2
	v_mov_b32_e32 v101, v2
	v_mov_b32_e32 v106, v2
	v_mov_b32_e32 v107, v2
	v_mov_b32_e32 v108, v2
	v_mov_b32_e32 v109, v2
	v_mov_b32_e32 v114, v2
	v_mov_b32_e32 v115, v2
	v_mov_b32_e32 v116, v2
	v_mov_b32_e32 v117, v2
	v_mov_b32_e32 v78, v2
	v_mov_b32_e32 v79, v2
	v_mov_b32_e32 v80, v2
	v_mov_b32_e32 v81, v2
	v_mov_b32_e32 v86, v2
	v_mov_b32_e32 v87, v2
	v_mov_b32_e32 v88, v2
	v_mov_b32_e32 v89, v2
	v_mov_b32_e32 v94, v2
	v_mov_b32_e32 v95, v2
	v_mov_b32_e32 v96, v2
	v_mov_b32_e32 v97, v2
	v_mov_b32_e32 v102, v2
	v_mov_b32_e32 v103, v2
	v_mov_b32_e32 v104, v2
	v_mov_b32_e32 v105, v2
	v_mov_b32_e32 v110, v2
	v_mov_b32_e32 v111, v2
	v_mov_b32_e32 v112, v2
	v_mov_b32_e32 v113, v2
	v_mov_b32_e32 v118, v2
	v_mov_b32_e32 v119, v2
	v_mov_b32_e32 v120, v2
	v_mov_b32_e32 v121, v2
	v_mov_b32_e32 v122, v2
	v_mov_b32_e32 v123, v2
	v_mov_b32_e32 v124, v2
	v_mov_b32_e32 v125, v2
	v_mov_b32_e32 v126, v2
	v_mov_b32_e32 v127, v2
	v_mov_b32_e32 v128, v2
	v_mov_b32_e32 v129, v2
	s_cmp_gt_u32 s48, 1
	s_cselect_b32 s32, -2, 1
.LBB0_115:
	ds_read_b128 v[130:133], v231
	ds_read_b128 v[134:137], v231 offset:1024
	ds_read_b128 v[138:141], v231 offset:2048
	ds_read_b128 v[142:145], v231 offset:3072
	ds_read_b128 v[146:149], v232
	ds_read_b128 v[150:153], v232 offset:1024
	ds_read_b128 v[154:157], v232 offset:2048
	ds_read_b128 v[158:161], v232 offset:3072
	s_add_u32 s0, s6, 0x80
	s_addc_u32 s1, s7, 0
	s_cmp_eq_u32 s18, 28
	s_cselect_b32 s9, s43, s1
	s_cselect_b32 s8, s42, s0
	s_cselect_b32 s1, s45, s15
	s_cselect_b32 s0, s44, s5
	v_mov_b32_e32 v186, v227
	ds_read_b128 v[162:165], v233
	ds_read_b128 v[166:169], v233 offset:1024
	ds_read_b128 v[170:173], v233 offset:2048
	ds_read_b128 v[174:177], v233 offset:3072
	ds_read_b128 v[178:181], v233 offset:4096
	ds_read_b128 v[182:185], v233 offset:5120
	ds_read_b128 v[192:195], v233 offset:6144
	ds_read_b128 v[196:199], v233 offset:7168
	s_add_i32 m0, s37, 0xc000
	s_nop 0
	global_load_lds_dwordx4 v186, s[6:7]
	v_mov_b32_e32 v186, v229
	s_add_i32 m0, s37, 0xe000
	s_nop 0
	global_load_lds_dwordx4 v186, s[6:7]
	s_cmp_eq_u32 s18, s32
	s_cbranch_scc1 .Lskipw_p1_0
	s_waitcnt vmcnt(8)
.Lskipw_p1_0:
	s_waitcnt lgkmcnt(0)
	s_barrier
	s_setprio 1
	s_waitcnt lgkmcnt(0)
	v_mfma_f32_16x16x32_bf16 v[126:129], v[130:133], v[162:165], v[126:129]
	v_mfma_f32_16x16x32_bf16 v[122:125], v[138:141], v[162:165], v[122:125]
	v_mfma_f32_16x16x32_bf16 v[118:121], v[130:133], v[170:173], v[118:121]
	v_mfma_f32_16x16x32_bf16 v[110:113], v[138:141], v[170:173], v[110:113]
	v_mfma_f32_16x16x32_bf16 v[102:105], v[130:133], v[178:181], v[102:105]
	v_mfma_f32_16x16x32_bf16 v[94:97], v[138:141], v[178:181], v[94:97]
	v_mfma_f32_16x16x32_bf16 v[86:89], v[130:133], v[192:195], v[86:89]
	v_mfma_f32_16x16x32_bf16 v[78:81], v[138:141], v[192:195], v[78:81]
	v_mfma_f32_16x16x32_bf16 v[126:129], v[134:137], v[166:169], v[126:129]
	v_mfma_f32_16x16x32_bf16 v[122:125], v[142:145], v[166:169], v[122:125]
	v_mfma_f32_16x16x32_bf16 v[118:121], v[134:137], v[174:177], v[118:121]
	v_mfma_f32_16x16x32_bf16 v[110:113], v[142:145], v[174:177], v[110:113]
	v_mfma_f32_16x16x32_bf16 v[102:105], v[134:137], v[182:185], v[102:105]
	v_mfma_f32_16x16x32_bf16 v[94:97], v[142:145], v[182:185], v[94:97]
	v_mfma_f32_16x16x32_bf16 v[86:89], v[134:137], v[196:199], v[86:89]
	v_mfma_f32_16x16x32_bf16 v[78:81], v[142:145], v[196:199], v[78:81]
	s_setprio 0
	s_setprio 1
	v_mfma_f32_16x16x32_bf16 v[114:117], v[146:149], v[162:165], v[114:117]
	v_mfma_f32_16x16x32_bf16 v[106:109], v[154:157], v[162:165], v[106:109]
	v_mfma_f32_16x16x32_bf16 v[98:101], v[146:149], v[170:173], v[98:101]
	v_mfma_f32_16x16x32_bf16 v[90:93], v[154:157], v[170:173], v[90:93]
	v_mfma_f32_16x16x32_bf16 v[82:85], v[146:149], v[178:181], v[82:85]
	v_mfma_f32_16x16x32_bf16 v[74:77], v[154:157], v[178:181], v[74:77]
	v_mfma_f32_16x16x32_bf16 v[70:73], v[146:149], v[192:195], v[70:73]
	v_mfma_f32_16x16x32_bf16 v[66:69], v[154:157], v[192:195], v[66:69]
	v_mfma_f32_16x16x32_bf16 v[114:117], v[150:153], v[166:169], v[114:117]
	v_mfma_f32_16x16x32_bf16 v[106:109], v[158:161], v[166:169], v[106:109]
	v_mfma_f32_16x16x32_bf16 v[98:101], v[150:153], v[174:177], v[98:101]
	v_mfma_f32_16x16x32_bf16 v[90:93], v[158:161], v[174:177], v[90:93]
	v_mfma_f32_16x16x32_bf16 v[82:85], v[150:153], v[182:185], v[82:85]
	v_mfma_f32_16x16x32_bf16 v[74:77], v[158:161], v[182:185], v[74:77]
	v_mfma_f32_16x16x32_bf16 v[70:73], v[150:153], v[196:199], v[70:73]
	v_mfma_f32_16x16x32_bf16 v[66:69], v[158:161], v[196:199], v[66:69]
	s_setprio 0
	s_barrier
	v_mov_b32_e32 v186, v1
	s_add_i32 s33, s75, s53
	ds_read_b128 v[162:165], v233 offset:16384
	ds_read_b128 v[166:169], v233 offset:17408
	ds_read_b128 v[170:173], v233 offset:18432
	ds_read_b128 v[174:177], v233 offset:19456
	ds_read_b128 v[178:181], v233 offset:20480
	ds_read_b128 v[182:185], v233 offset:21504
	ds_read_b128 v[192:195], v233 offset:22528
	ds_read_b128 v[196:199], v233 offset:23552
	s_mov_b32 m0, s33
	s_nop 0
	global_load_lds_dwordx4 v186, s[0:1]
	v_mov_b32_e32 v186, v225
	s_add_i32 m0, s33, 0x2000
	s_add_u32 s46, s0, 0x80000
	global_load_lds_dwordx4 v186, s[0:1]
	s_addc_u32 s47, s1, 0
	v_mov_b32_e32 v186, v1
	s_add_i32 s33, s76, s53
	s_mov_b32 m0, s33
	s_nop 0
	global_load_lds_dwordx4 v186, s[46:47]
	v_mov_b32_e32 v186, v225
	s_add_i32 m0, s33, 0x2000
	s_nop 0
	global_load_lds_dwordx4 v186, s[46:47]
	v_mov_b32_e32 v186, v226
	s_mov_b32 m0, s37
	s_nop 0
	global_load_lds_dwordx4 v186, s[8:9]
	v_mov_b32_e32 v186, v228
	s_mov_b32 m0, s54
	s_nop 0
	global_load_lds_dwordx4 v186, s[8:9]
	s_cmp_eq_u32 s18, s32
	s_cbranch_scc1 .Lskipw_p1_1
	s_waitcnt vmcnt(8)
.Lskipw_p1_1:
	s_waitcnt lgkmcnt(0)
	s_barrier
	s_setprio 1
	s_waitcnt lgkmcnt(0)
	v_mfma_f32_16x16x32_bf16 v[62:65], v[130:133], v[162:165], v[62:65]
	v_mfma_f32_16x16x32_bf16 v[58:61], v[138:141], v[162:165], v[58:61]
	v_mfma_f32_16x16x32_bf16 v[54:57], v[130:133], v[170:173], v[54:57]
	v_mfma_f32_16x16x32_bf16 v[46:49], v[138:141], v[170:173], v[46:49]
	v_mfma_f32_16x16x32_bf16 v[38:41], v[130:133], v[178:181], v[38:41]
	v_mfma_f32_16x16x32_bf16 v[30:33], v[138:141], v[178:181], v[30:33]
	v_mfma_f32_16x16x32_bf16 v[22:25], v[130:133], v[192:195], v[22:25]
	v_mfma_f32_16x16x32_bf16 v[14:17], v[138:141], v[192:195], v[14:17]
	v_mfma_f32_16x16x32_bf16 v[62:65], v[134:137], v[166:169], v[62:65]
	v_mfma_f32_16x16x32_bf16 v[58:61], v[142:145], v[166:169], v[58:61]
	v_mfma_f32_16x16x32_bf16 v[54:57], v[134:137], v[174:177], v[54:57]
	v_mfma_f32_16x16x32_bf16 v[46:49], v[142:145], v[174:177], v[46:49]
	v_mfma_f32_16x16x32_bf16 v[38:41], v[134:137], v[182:185], v[38:41]
	v_mfma_f32_16x16x32_bf16 v[30:33], v[142:145], v[182:185], v[30:33]
	v_mfma_f32_16x16x32_bf16 v[22:25], v[134:137], v[196:199], v[22:25]
	v_mfma_f32_16x16x32_bf16 v[14:17], v[142:145], v[196:199], v[14:17]
	s_setprio 0
	s_setprio 1
	v_mfma_f32_16x16x32_bf16 v[50:53], v[146:149], v[162:165], v[50:53]
	v_mfma_f32_16x16x32_bf16 v[42:45], v[154:157], v[162:165], v[42:45]
	v_mfma_f32_16x16x32_bf16 v[34:37], v[146:149], v[170:173], v[34:37]
	v_mfma_f32_16x16x32_bf16 v[26:29], v[154:157], v[170:173], v[26:29]
	v_mfma_f32_16x16x32_bf16 v[18:21], v[146:149], v[178:181], v[18:21]
	v_mfma_f32_16x16x32_bf16 v[10:13], v[154:157], v[178:181], v[10:13]
	v_mfma_f32_16x16x32_bf16 v[6:9], v[146:149], v[192:195], v[6:9]
	v_mfma_f32_16x16x32_bf16 v[2:5], v[154:157], v[192:195], v[2:5]
	v_mfma_f32_16x16x32_bf16 v[50:53], v[150:153], v[166:169], v[50:53]
	v_mfma_f32_16x16x32_bf16 v[42:45], v[158:161], v[166:169], v[42:45]
	v_mfma_f32_16x16x32_bf16 v[34:37], v[150:153], v[174:177], v[34:37]
	v_mfma_f32_16x16x32_bf16 v[26:29], v[158:161], v[174:177], v[26:29]
	v_mfma_f32_16x16x32_bf16 v[18:21], v[150:153], v[182:185], v[18:21]
	v_mfma_f32_16x16x32_bf16 v[10:13], v[158:161], v[182:185], v[10:13]
	v_mfma_f32_16x16x32_bf16 v[6:9], v[150:153], v[196:199], v[6:9]
	v_mfma_f32_16x16x32_bf16 v[2:5], v[158:161], v[196:199], v[2:5]
	s_setprio 0
	s_barrier
	s_add_i32 s33, 0, 0x18000
	s_add_i32 s39, 0, 0x1c000
	v_add_u32_e32 v142, s33, v230
	v_add_u32_e32 v158, s39, v230
	ds_read_b128 v[130:133], v142
	ds_read_b128 v[134:137], v142 offset:1024
	ds_read_b128 v[138:141], v142 offset:2048
	ds_read_b128 v[142:145], v142 offset:3072
	ds_read_b128 v[146:149], v158
	ds_read_b128 v[150:153], v158 offset:1024
	ds_read_b128 v[154:157], v158 offset:2048
	ds_read_b128 v[158:161], v158 offset:3072
	v_mov_b32_e32 v186, v227
	s_mov_b32 m0, s55
	ds_read_b128 v[162:165], v233 offset:32768
	ds_read_b128 v[166:169], v233 offset:33792
	ds_read_b128 v[170:173], v233 offset:34816
	ds_read_b128 v[174:177], v233 offset:35840
	ds_read_b128 v[178:181], v233 offset:36864
	ds_read_b128 v[182:185], v233 offset:37888
	ds_read_b128 v[192:195], v233 offset:38912
	ds_read_b128 v[196:199], v233 offset:39936
	s_nop 0
	global_load_lds_dwordx4 v186, s[8:9]
	v_mov_b32_e32 v186, v229
	s_mov_b32 m0, s56
	s_nop 0
	global_load_lds_dwordx4 v186, s[8:9]
	s_waitcnt vmcnt(8)
	s_waitcnt lgkmcnt(0)
	s_barrier
	s_setprio 1
	s_waitcnt lgkmcnt(0)
	v_mfma_f32_16x16x32_bf16 v[126:129], v[130:133], v[162:165], v[126:129]
	v_mfma_f32_16x16x32_bf16 v[122:125], v[138:141], v[162:165], v[122:125]
	v_mfma_f32_16x16x32_bf16 v[118:121], v[130:133], v[170:173], v[118:121]
	v_mfma_f32_16x16x32_bf16 v[110:113], v[138:141], v[170:173], v[110:113]
	v_mfma_f32_16x16x32_bf16 v[102:105], v[130:133], v[178:181], v[102:105]
	v_mfma_f32_16x16x32_bf16 v[94:97], v[138:141], v[178:181], v[94:97]
	v_mfma_f32_16x16x32_bf16 v[86:89], v[130:133], v[192:195], v[86:89]
	v_mfma_f32_16x16x32_bf16 v[78:81], v[138:141], v[192:195], v[78:81]
	v_mfma_f32_16x16x32_bf16 v[126:129], v[134:137], v[166:169], v[126:129]
	v_mfma_f32_16x16x32_bf16 v[122:125], v[142:145], v[166:169], v[122:125]
	v_mfma_f32_16x16x32_bf16 v[118:121], v[134:137], v[174:177], v[118:121]
	v_mfma_f32_16x16x32_bf16 v[110:113], v[142:145], v[174:177], v[110:113]
	v_mfma_f32_16x16x32_bf16 v[102:105], v[134:137], v[182:185], v[102:105]
	v_mfma_f32_16x16x32_bf16 v[94:97], v[142:145], v[182:185], v[94:97]
	v_mfma_f32_16x16x32_bf16 v[86:89], v[134:137], v[196:199], v[86:89]
	v_mfma_f32_16x16x32_bf16 v[78:81], v[142:145], v[196:199], v[78:81]
	s_setprio 0
	s_setprio 1
	v_mfma_f32_16x16x32_bf16 v[114:117], v[146:149], v[162:165], v[114:117]
	v_mfma_f32_16x16x32_bf16 v[106:109], v[154:157], v[162:165], v[106:109]
	v_mfma_f32_16x16x32_bf16 v[98:101], v[146:149], v[170:173], v[98:101]
	v_mfma_f32_16x16x32_bf16 v[90:93], v[154:157], v[170:173], v[90:93]
	v_mfma_f32_16x16x32_bf16 v[82:85], v[146:149], v[178:181], v[82:85]
	v_mfma_f32_16x16x32_bf16 v[74:77], v[154:157], v[178:181], v[74:77]
	v_mfma_f32_16x16x32_bf16 v[70:73], v[146:149], v[192:195], v[70:73]
	v_mfma_f32_16x16x32_bf16 v[66:69], v[154:157], v[192:195], v[66:69]
	v_mfma_f32_16x16x32_bf16 v[114:117], v[150:153], v[166:169], v[114:117]
	v_mfma_f32_16x16x32_bf16 v[106:109], v[158:161], v[166:169], v[106:109]
	v_mfma_f32_16x16x32_bf16 v[98:101], v[150:153], v[174:177], v[98:101]
	v_mfma_f32_16x16x32_bf16 v[90:93], v[158:161], v[174:177], v[90:93]
	v_mfma_f32_16x16x32_bf16 v[82:85], v[150:153], v[182:185], v[82:85]
	v_mfma_f32_16x16x32_bf16 v[74:77], v[158:161], v[182:185], v[74:77]
	v_mfma_f32_16x16x32_bf16 v[70:73], v[150:153], v[196:199], v[70:73]
	v_mfma_f32_16x16x32_bf16 v[66:69], v[158:161], v[196:199], v[66:69]
	s_setprio 0
	s_barrier
; #define PG8_BAR __builtin_amdgcn_s_barrier()
; template <class Epi, bool GATHER, bool EXPERT, bool FP8>
; DI void gemm_phase(LAS unsigned char* lds, const Gemm g, const StaticOrder& S, const Epi& E) {
;     ...
;         for (int t = 0; t < nt; t += 2) {
;             const bool last = (t == nt - 2);
;             const char* a1 = cA + (size_t)(t + 1) * kstep;
;             const char* a2 = last ? nA : cA + (size_t)(t + 2) * kstep; const char* b2 = last ? nB : cB + (size_t)(t + 2) * kstep;
;             const char* a3 = a2 + kstep; const char* b3 = b2 + kstep;
;             unsigned o00 = coffA[0][0], o01 = coffA[0][1], o10 = coffA[1][0], o11 = coffA[1][1];
;             if (GATHER && last && has_next) {
;                 o00 = sp[0] * (unsigned)(K * 2) + (unsigned)C0x2; o01 = sp[512] * (unsigned)(K * 2) + (unsigned)C1x2;
;                 o10 = sp[1024] * (unsigned)(K * 2) + (unsigned)C0x2; o11 = sp[1536] * (unsigned)(K * 2) + (unsigned)C1x2; }
;             PG8_TRIP(a1, a2, b2, a3, b3, o00, o01, o10, o11);
;             if (last) { coffA[0][0] = o00; coffA[0][1] = o01; coffA[1][0] = o10; coffA[1][1] = o11; }
;         }
;         if (wr == 0) PG8_BAR;
	v_mov_b32_e32 v186, v1
	ds_read_b128 v[162:165], v233 offset:49152
	ds_read_b128 v[166:169], v233 offset:50176
	ds_read_b128 v[170:173], v233 offset:51200
	ds_read_b128 v[174:177], v233 offset:52224
	ds_read_b128 v[178:181], v233 offset:53248
	ds_read_b128 v[182:185], v233 offset:54272
	ds_read_b128 v[192:195], v233 offset:55296
	ds_read_b128 v[196:199], v233 offset:56320
	s_add_i32 s33, s33, s53
	v_lshl_add_u64 v[200:201], s[0:1], 0, v[186:187]
	v_lshl_add_u64 v[200:201], v[200:201], 0, s[24:25]
	s_mov_b32 m0, s33
	v_mov_b32_e32 v186, v225
	global_load_lds_dwordx4 v[200:201], off
	s_add_i32 m0, s33, 0x2000
	s_nop 0
	v_lshl_add_u64 v[200:201], s[0:1], 0, v[186:187]
	s_add_u32 s0, s0, 0x80080
	v_lshl_add_u64 v[200:201], v[200:201], 0, s[24:25]
	s_addc_u32 s1, s1, 0
	v_mov_b32_e32 v186, v1
	s_add_i32 s33, s39, s53
	global_load_lds_dwordx4 v[200:201], off
	s_mov_b32 m0, s33
	s_nop 0
	global_load_lds_dwordx4 v186, s[0:1]
	v_mov_b32_e32 v186, v225
	s_add_i32 m0, s33, 0x2000
	s_nop 0
	global_load_lds_dwordx4 v186, s[0:1]
	v_mov_b32_e32 v186, v226
	s_mov_b32 m0, s62
	v_lshl_add_u64 v[200:201], s[8:9], 0, v[186:187]
	v_lshl_add_u64 v[200:201], v[200:201], 0, s[24:25]
	v_mov_b32_e32 v186, v228
	global_load_lds_dwordx4 v[200:201], off
	s_mov_b32 m0, s63
	v_lshl_add_u64 v[200:201], s[8:9], 0, v[186:187]
	v_lshl_add_u64 v[200:201], v[200:201], 0, s[24:25]
	global_load_lds_dwordx4 v[200:201], off
	s_waitcnt vmcnt(8)
	s_waitcnt lgkmcnt(0)
	s_barrier
	s_setprio 1
	s_waitcnt lgkmcnt(0)
	v_mfma_f32_16x16x32_bf16 v[62:65], v[130:133], v[162:165], v[62:65]
	v_mfma_f32_16x16x32_bf16 v[58:61], v[138:141], v[162:165], v[58:61]
	v_mfma_f32_16x16x32_bf16 v[54:57], v[130:133], v[170:173], v[54:57]
	v_mfma_f32_16x16x32_bf16 v[46:49], v[138:141], v[170:173], v[46:49]
	v_mfma_f32_16x16x32_bf16 v[38:41], v[130:133], v[178:181], v[38:41]
	v_mfma_f32_16x16x32_bf16 v[30:33], v[138:141], v[178:181], v[30:33]
	v_mfma_f32_16x16x32_bf16 v[22:25], v[130:133], v[192:195], v[22:25]
	v_mfma_f32_16x16x32_bf16 v[14:17], v[138:141], v[192:195], v[14:17]
	v_mfma_f32_16x16x32_bf16 v[62:65], v[134:137], v[166:169], v[62:65]
	v_mfma_f32_16x16x32_bf16 v[58:61], v[142:145], v[166:169], v[58:61]
	v_mfma_f32_16x16x32_bf16 v[54:57], v[134:137], v[174:177], v[54:57]
	v_mfma_f32_16x16x32_bf16 v[46:49], v[142:145], v[174:177], v[46:49]
	v_mfma_f32_16x16x32_bf16 v[38:41], v[134:137], v[182:185], v[38:41]
	v_mfma_f32_16x16x32_bf16 v[30:33], v[142:145], v[182:185], v[30:33]
	v_mfma_f32_16x16x32_bf16 v[22:25], v[134:137], v[196:199], v[22:25]
	v_mfma_f32_16x16x32_bf16 v[14:17], v[142:145], v[196:199], v[14:17]
	s_setprio 0
	s_setprio 1
	v_mfma_f32_16x16x32_bf16 v[50:53], v[146:149], v[162:165], v[50:53]
	v_mfma_f32_16x16x32_bf16 v[42:45], v[154:157], v[162:165], v[42:45]
	v_mfma_f32_16x16x32_bf16 v[34:37], v[146:149], v[170:173], v[34:37]
	v_mfma_f32_16x16x32_bf16 v[26:29], v[154:157], v[170:173], v[26:29]
	v_mfma_f32_16x16x32_bf16 v[18:21], v[146:149], v[178:181], v[18:21]
	v_mfma_f32_16x16x32_bf16 v[10:13], v[154:157], v[178:181], v[10:13]
	v_mfma_f32_16x16x32_bf16 v[6:9], v[146:149], v[192:195], v[6:9]
	v_mfma_f32_16x16x32_bf16 v[2:5], v[154:157], v[192:195], v[2:5]
	v_mfma_f32_16x16x32_bf16 v[50:53], v[150:153], v[166:169], v[50:53]
	v_mfma_f32_16x16x32_bf16 v[42:45], v[158:161], v[166:169], v[42:45]
	v_mfma_f32_16x16x32_bf16 v[34:37], v[150:153], v[174:177], v[34:37]
	v_mfma_f32_16x16x32_bf16 v[26:29], v[158:161], v[174:177], v[26:29]
	v_mfma_f32_16x16x32_bf16 v[18:21], v[150:153], v[182:185], v[18:21]
	v_mfma_f32_16x16x32_bf16 v[10:13], v[158:161], v[182:185], v[10:13]
	v_mfma_f32_16x16x32_bf16 v[6:9], v[150:153], v[196:199], v[6:9]
	v_mfma_f32_16x16x32_bf16 v[2:5], v[158:161], v[196:199], v[2:5]
	s_setprio 0
	s_barrier
	s_add_i32 s18, s18, 2
	s_add_u32 s5, s5, 0x100
	s_addc_u32 s15, s15, 0
	s_add_u32 s6, s6, 0x100
	s_addc_u32 s7, s7, 0
	s_cmp_gt_u32 s18, 29
	s_cbranch_scc0 .LBB0_115
	s_and_b64 vcc, exec, s[26:27]
	s_cbranch_vccz .LBB0_118
	s_barrier

; DI unsigned cvtpk(float lo, float hi) { f32x2 v = {lo, hi}; bf16x2_t b = __builtin_convertvector(v, bf16x2_t); return __builtin_bit_cast(unsigned, b); }
;     DI void operator()(const f32x4 (&acc)[2][2][4][2], const Unit& u, int wr, int wc, int fr, int fq, const LAS unsigned char* st) const {
;         const int row0 = u.pm * BM + wr * 64 + fr, col0 = u.pn * BM + wc * 32 + 8 * fq;
;         if (u.pn >= 8) {
; #pragma unroll
;             for (int ai = 0; ai < 2; ++ai)
; #pragma unroll
;                 for (int m = 0; m < 4; ++m) { const int row = row0 + ai * HALF + m * 16; bf16* rowp = O + (size_t)row * ldc + col0;
;                     if (u.pn < 12) rowp = HM + 2 * HM_PLANE + ((size_t)((row >> 14) * 8 + ((2 * u.pn) & 7)) * SEQ + (row & (SEQ - 1))) * 128 + wc * 32 + 8 * fq;
; #pragma unroll
;                     for (int bj = 0; bj < 2; ++bj) { const f32x4 v0 = acc[ai][bj][m][0], v1 = acc[ai][bj][m][1];
;                         u32x4 w; w.x = cvtpk(v0[0], v0[1]); w.y = cvtpk(v0[2], v0[3]); w.z = cvtpk(v1[0], v1[1]); w.w = cvtpk(v1[2], v1[3]);
;                         *(u32x4*)(rowp + (u.pn < 12 ? (size_t)bj * SEQ * 128 : (size_t)bj * HALF)) = w; } }
.LBB0_214:
	s_lshl_b32 s0, s36, 8
	s_or_b32 s0, s0, s61
	v_add_u32_e32 v130, s0, v192
	s_lshl_b32 s0, s36, 1
	s_and_b32 s8, s0, 6
	s_ashr_i32 s0, s33, 11
	s_and_b32 s0, s0, -8
	s_or_b32 s0, s8, s0
	s_ashr_i32 s1, s0, 31
	s_lshl_b64 s[0:1], s[0:1], 22
	s_add_u32 s4, s34, s0
	s_addc_u32 s5, s35, s1
	s_lshl_b32 s72, s61, 1
	v_lshlrev_b32_e32 v136, 8, v242
	s_cmp_lt_u32 s36, 12
	v_and_b32_e32 v186, 0x3fcf00, v136
	v_ashrrev_i32_e32 v131, 31, v130
	v_ashrrev_i32_e32 v193, 31, v192
	v_mov_b64_e32 v[132:133], s[20:21]
	v_lshl_add_u64 v[136:137], s[4:5], 0, v[186:187]
	s_cselect_b64 vcc, -1, 0
	v_mad_i64_i32 v[134:135], s[0:1], v242, s87, v[132:133]
	v_lshlrev_b64 v[130:131], 1, v[130:131]
	v_lshl_add_u64 v[136:137], v[136:137], 0, s[72:73]
	v_lshlrev_b64 v[138:139], 1, v[192:193]
	s_and_b64 s[0:1], vcc, exec
	v_lshl_add_u64 v[134:135], v[134:135], 0, v[130:131]
	v_lshl_add_u64 v[136:137], v[136:137], 0, v[138:139]
	s_mov_b32 s0, 0x400000
	v_cndmask_b32_e32 v135, v135, v137, vcc
	s_cselect_b32 s0, s0, 0x100
	s_mov_b32 s1, s73
	v_cndmask_b32_e32 v134, v134, v136, vcc
	v_cvt_pk_bf16_f32 v114, v114, v115
	v_cvt_pk_bf16_f32 v115, v116, v117
	v_cvt_pk_bf16_f32 v116, v106, v107
	v_cvt_pk_bf16_f32 v117, v108, v109
	v_lshl_add_u64 v[106:107], v[134:135], 0, s[0:1]
	v_or_b32_e32 v108, 16, v242
	global_store_dwordx4 v[106:107], v[114:117], off
	v_mad_i64_i32 v[106:107], s[6:7], v108, s87, v[132:133]
	v_lshlrev_b32_e32 v108, 8, v108
	v_and_b32_e32 v186, 0x3fdf00, v108
	v_lshl_add_u64 v[108:109], s[4:5], 0, v[186:187]
	v_lshl_add_u64 v[108:109], v[108:109], 0, s[72:73]
	v_lshl_add_u64 v[106:107], v[106:107], 0, v[130:131]
	v_lshl_add_u64 v[108:109], v[108:109], 0, v[138:139]
	v_cndmask_b32_e32 v115, v107, v109, vcc
	v_cndmask_b32_e32 v114, v106, v108, vcc
	v_cvt_pk_bf16_f32 v126, v126, v127
	v_cvt_pk_bf16_f32 v127, v128, v129
	v_cvt_pk_bf16_f32 v128, v122, v123
	v_cvt_pk_bf16_f32 v129, v124, v125
	v_cvt_pk_bf16_f32 v98, v98, v99
	v_cvt_pk_bf16_f32 v99, v100, v101
	v_cvt_pk_bf16_f32 v100, v90, v91
	v_cvt_pk_bf16_f32 v101, v92, v93
	v_lshl_add_u64 v[90:91], v[114:115], 0, s[0:1]
	v_or_b32_e32 v92, 32, v242
	global_store_dwordx4 v[134:135], v[126:129], off
	global_store_dwordx4 v[90:91], v[98:101], off
	v_mad_i64_i32 v[90:91], s[6:7], v92, s87, v[132:133]
	v_lshlrev_b32_e32 v92, 8, v92
	v_and_b32_e32 v186, 0x3fef00, v92
	v_lshl_add_u64 v[92:93], s[4:5], 0, v[186:187]
	v_lshl_add_u64 v[92:93], v[92:93], 0, s[72:73]
	v_lshl_add_u64 v[90:91], v[90:91], 0, v[130:131]
	v_lshl_add_u64 v[92:93], v[92:93], 0, v[138:139]
	v_cndmask_b32_e32 v99, v91, v93, vcc
	v_cndmask_b32_e32 v98, v90, v92, vcc
	v_cvt_pk_bf16_f32 v106, v118, v119
	v_cvt_pk_bf16_f32 v107, v120, v121
	v_cvt_pk_bf16_f32 v108, v110, v111
	v_cvt_pk_bf16_f32 v109, v112, v113
	v_cvt_pk_bf16_f32 v82, v82, v83
	v_cvt_pk_bf16_f32 v83, v84, v85
	v_cvt_pk_bf16_f32 v84, v74, v75
	v_cvt_pk_bf16_f32 v85, v76, v77
	v_lshl_add_u64 v[74:75], v[98:99], 0, s[0:1]
	v_or_b32_e32 v76, 48, v242
	global_store_dwordx4 v[114:115], v[106:109], off
	global_store_dwordx4 v[74:75], v[82:85], off
	v_mad_i64_i32 v[74:75], s[6:7], v76, s87, v[132:133]
	v_lshlrev_b32_e32 v76, 8, v76
	v_and_b32_e32 v186, 0x3fff00, v76
	v_lshl_add_u64 v[76:77], s[4:5], 0, v[186:187]
	v_lshl_add_u64 v[76:77], v[76:77], 0, s[72:73]
	v_lshl_add_u64 v[74:75], v[74:75], 0, v[130:131]
	v_lshl_add_u64 v[76:77], v[76:77], 0, v[138:139]
	v_cndmask_b32_e32 v83, v75, v77, vcc
	v_cndmask_b32_e32 v82, v74, v76, vcc
	v_cvt_pk_bf16_f32 v90, v102, v103
	v_cvt_pk_bf16_f32 v91, v104, v105
	v_cvt_pk_bf16_f32 v92, v94, v95
	v_cvt_pk_bf16_f32 v93, v96, v97
	v_cvt_pk_bf16_f32 v70, v70, v71
	v_cvt_pk_bf16_f32 v71, v72, v73
	v_cvt_pk_bf16_f32 v72, v66, v67
	v_cvt_pk_bf16_f32 v73, v68, v69
	v_lshl_add_u64 v[66:67], v[82:83], 0, s[0:1]
	global_store_dwordx4 v[98:99], v[90:93], off
; DI unsigned cvtpk(float lo, float hi) { f32x2 v = {lo, hi}; bf16x2_t b = __builtin_convertvector(v, bf16x2_t); return __builtin_bit_cast(unsigned, b); }
;     DI void operator()(const f32x4 (&acc)[2][2][4][2], const Unit& u, int wr, int wc, int fr, int fq, const LAS unsigned char* st) const {
;     ...
;         if (u.pn >= 8) {
; #pragma unroll
;             for (int ai = 0; ai < 2; ++ai)
; #pragma unroll
;                 for (int m = 0; m < 4; ++m) { const int row = row0 + ai * HALF + m * 16; bf16* rowp = O + (size_t)row * ldc + col0;
;                     if (u.pn < 12) rowp = HM + 2 * HM_PLANE + ((size_t)((row >> 14) * 8 + ((2 * u.pn) & 7)) * SEQ + (row & (SEQ - 1))) * 128 + wc * 32 + 8 * fq;
; #pragma unroll
;                     for (int bj = 0; bj < 2; ++bj) { const f32x4 v0 = acc[ai][bj][m][0], v1 = acc[ai][bj][m][1];
;                         u32x4 w; w.x = cvtpk(v0[0], v0[1]); w.y = cvtpk(v0[2], v0[3]); w.z = cvtpk(v1[0], v1[1]); w.w = cvtpk(v1[2], v1[3]);
;                         *(u32x4*)(rowp + (u.pn < 12 ? (size_t)bj * SEQ * 128 : (size_t)bj * HALF)) = w; } }
;             return;
	global_store_dwordx4 v[66:67], v[70:73], off
	v_cvt_pk_bf16_f32 v74, v86, v87
	v_cvt_pk_bf16_f32 v75, v88, v89
	v_add_u32_e32 v70, 0x80, v242
	v_ashrrev_i32_e32 v66, 11, v70
	v_and_or_b32 v66, v66, -8, s8
	v_ashrrev_i32_e32 v67, 31, v66
	v_lshlrev_b64 v[66:67], 22, v[66:67]
	v_mad_i64_i32 v[68:69], s[4:5], v70, s87, v[132:133]
	v_lshlrev_b32_e32 v70, 8, v70
	v_lshl_add_u64 v[66:67], s[34:35], 0, v[66:67]
	v_and_b32_e32 v186, 0x3fcf00, v70
	v_lshl_add_u64 v[70:71], v[66:67], 0, v[186:187]
	v_lshl_add_u64 v[70:71], v[70:71], 0, s[72:73]
	v_lshl_add_u64 v[68:69], v[68:69], 0, v[130:131]
	v_lshl_add_u64 v[70:71], v[70:71], 0, v[138:139]
	v_cndmask_b32_e32 v69, v69, v71, vcc
	v_cndmask_b32_e32 v68, v68, v70, vcc
	v_cvt_pk_bf16_f32 v76, v78, v79
	v_cvt_pk_bf16_f32 v77, v80, v81
	v_cvt_pk_bf16_f32 v50, v50, v51
	v_cvt_pk_bf16_f32 v51, v52, v53
	v_cvt_pk_bf16_f32 v52, v42, v43
	v_cvt_pk_bf16_f32 v53, v44, v45
	v_lshl_add_u64 v[42:43], v[68:69], 0, s[0:1]
	v_add_u32_e32 v44, 0x90, v242
	global_store_dwordx4 v[82:83], v[74:77], off
	global_store_dwordx4 v[42:43], v[50:53], off
	v_mad_i64_i32 v[42:43], s[4:5], v44, s87, v[132:133]
	v_lshlrev_b32_e32 v44, 8, v44
	v_and_b32_e32 v186, 0x3fdf00, v44
	v_lshl_add_u64 v[44:45], v[66:67], 0, v[186:187]
	v_lshl_add_u64 v[44:45], v[44:45], 0, s[72:73]
	v_lshl_add_u64 v[42:43], v[42:43], 0, v[130:131]
	v_lshl_add_u64 v[44:45], v[44:45], 0, v[138:139]
	v_cndmask_b32_e32 v51, v43, v45, vcc
	v_cndmask_b32_e32 v50, v42, v44, vcc
	v_cvt_pk_bf16_f32 v62, v62, v63
	v_cvt_pk_bf16_f32 v63, v64, v65
	v_cvt_pk_bf16_f32 v64, v58, v59
	v_cvt_pk_bf16_f32 v65, v60, v61
	v_cvt_pk_bf16_f32 v34, v34, v35
	v_cvt_pk_bf16_f32 v35, v36, v37
	v_cvt_pk_bf16_f32 v36, v26, v27
	v_cvt_pk_bf16_f32 v37, v28, v29
	v_lshl_add_u64 v[26:27], v[50:51], 0, s[0:1]
	v_add_u32_e32 v28, 0xa0, v242
	global_store_dwordx4 v[68:69], v[62:65], off
	global_store_dwordx4 v[26:27], v[34:37], off
	v_mad_i64_i32 v[26:27], s[4:5], v28, s87, v[132:133]
	v_lshlrev_b32_e32 v28, 8, v28
	v_and_b32_e32 v186, 0x3fef00, v28
	v_lshl_add_u64 v[28:29], v[66:67], 0, v[186:187]
	v_lshl_add_u64 v[28:29], v[28:29], 0, s[72:73]
	v_lshl_add_u64 v[26:27], v[26:27], 0, v[130:131]
	v_lshl_add_u64 v[28:29], v[28:29], 0, v[138:139]
	v_cndmask_b32_e32 v35, v27, v29, vcc
	v_cndmask_b32_e32 v34, v26, v28, vcc
	v_cvt_pk_bf16_f32 v42, v54, v55
	v_cvt_pk_bf16_f32 v43, v56, v57
	v_cvt_pk_bf16_f32 v44, v46, v47
	v_cvt_pk_bf16_f32 v45, v48, v49
	v_cvt_pk_bf16_f32 v18, v18, v19
	v_cvt_pk_bf16_f32 v19, v20, v21
	v_cvt_pk_bf16_f32 v20, v10, v11
	v_cvt_pk_bf16_f32 v21, v12, v13
	v_lshl_add_u64 v[10:11], v[34:35], 0, s[0:1]
	v_add_u32_e32 v12, 0xb0, v242
	global_store_dwordx4 v[50:51], v[42:45], off
	global_store_dwordx4 v[10:11], v[18:21], off
	v_mad_i64_i32 v[10:11], s[4:5], v12, s87, v[132:133]
	v_lshlrev_b32_e32 v12, 8, v12
	v_and_b32_e32 v186, 0x3fff00, v12
	v_lshl_add_u64 v[12:13], v[66:67], 0, v[186:187]
	v_lshl_add_u64 v[12:13], v[12:13], 0, s[72:73]
	v_lshl_add_u64 v[10:11], v[10:11], 0, v[130:131]
	v_lshl_add_u64 v[12:13], v[12:13], 0, v[138:139]
	v_cndmask_b32_e32 v19, v11, v13, vcc
	v_cndmask_b32_e32 v18, v10, v12, vcc
	v_cvt_pk_bf16_f32 v26, v38, v39
	v_cvt_pk_bf16_f32 v27, v40, v41
	v_cvt_pk_bf16_f32 v28, v30, v31
	v_cvt_pk_bf16_f32 v29, v32, v33
	v_cvt_pk_bf16_f32 v10, v22, v23
	v_cvt_pk_bf16_f32 v11, v24, v25
	v_cvt_pk_bf16_f32 v12, v14, v15
	v_cvt_pk_bf16_f32 v13, v16, v17
	v_cvt_pk_bf16_f32 v6, v6, v7
	v_cvt_pk_bf16_f32 v7, v8, v9
	v_cvt_pk_bf16_f32 v8, v2, v3
	v_cvt_pk_bf16_f32 v9, v4, v5
	v_lshl_add_u64 v[2:3], v[18:19], 0, s[0:1]
	global_store_dwordx4 v[34:35], v[26:29], off
	global_store_dwordx4 v[18:19], v[10:13], off
	global_store_dwordx4 v[2:3], v[6:9], off
	s_waitcnt vmcnt(16)
	s_andn2_b64 vcc, exec, s[2:3]
	s_mov_b64 s[0:1], -1
	s_cbranch_vccnz .LBB0_111

; template <class Epi, bool GATHER, bool EXPERT, bool FP8>
; DI void gemm_phase(LAS unsigned char* lds, const Gemm g, const StaticOrder& S, const Epi& E) {
;     ...
; #pragma unroll
;         for (int a = 0; a < 2; ++a)
; #pragma unroll
;             for (int b = 0; b < 2; ++b)
; #pragma unroll
;                 for (int m = 0; m < 4; ++m)
; #pragma unroll
;                     for (int n = 0; n < 2; ++n) acc[a][b][m][n] = (f32x4){0.f, 0.f, 0.f, 0.f};
;         cur = nxt; cA = nA; cB = nB; ++ui;
.LBB0_792:
	s_ashr_i32 s23, s22, 31
	s_lshl_b64 s[0:1], s[22:23], 20
	s_add_u32 s21, s37, s0
	s_addc_u32 s23, s38, s1
	s_and_b64 s[0:1], s[60:61], exec
	s_cselect_b32 s24, s21, s30
	s_cselect_b32 s25, s23, s31
	s_ashr_i32 s21, s20, 31
	s_lshl_b64 s[0:1], s[20:21], 20
	s_add_u32 s21, s33, s0
	s_addc_u32 s23, s39, s1
	s_and_b64 s[0:1], s[60:61], exec
	s_cselect_b32 s26, s21, s34
	s_cselect_b32 s27, s23, s35
	s_add_u32 s21, s34, 0x100
	.p2align 8
	s_addc_u32 s23, s35, 0
	s_add_u32 s30, s30, 0x80
	v_mov_b32_e32 v2, 0
	s_addc_u32 s31, s31, 0
	s_mov_b32 s55, -2
	v_mov_b32_e32 v3, v2
	v_mov_b32_e32 v4, v2
	v_mov_b32_e32 v5, v2
	v_mov_b32_e32 v6, v2
	v_mov_b32_e32 v7, v2
	v_mov_b32_e32 v8, v2
	v_mov_b32_e32 v9, v2
	v_mov_b32_e32 v14, v2
	v_mov_b32_e32 v15, v2
	v_mov_b32_e32 v16, v2
	v_mov_b32_e32 v17, v2
	v_mov_b32_e32 v18, v2
	v_mov_b32_e32 v19, v2
	v_mov_b32_e32 v20, v2
	v_mov_b32_e32 v21, v2
	v_mov_b32_e32 v26, v2
	v_mov_b32_e32 v27, v2
	v_mov_b32_e32 v28, v2
	v_mov_b32_e32 v29, v2
	v_mov_b32_e32 v30, v2
	v_mov_b32_e32 v31, v2
	v_mov_b32_e32 v32, v2
	v_mov_b32_e32 v33, v2
	v_mov_b32_e32 v38, v2
	v_mov_b32_e32 v39, v2
	v_mov_b32_e32 v40, v2
	v_mov_b32_e32 v41, v2
	v_mov_b32_e32 v46, v2
	v_mov_b32_e32 v47, v2
	v_mov_b32_e32 v48, v2
	v_mov_b32_e32 v49, v2
	v_mov_b32_e32 v10, v2
	v_mov_b32_e32 v11, v2
	v_mov_b32_e32 v12, v2
	v_mov_b32_e32 v13, v2
	v_mov_b32_e32 v22, v2
	v_mov_b32_e32 v23, v2
	v_mov_b32_e32 v24, v2
	v_mov_b32_e32 v25, v2
	v_mov_b32_e32 v34, v2
	v_mov_b32_e32 v35, v2
	v_mov_b32_e32 v36, v2
	v_mov_b32_e32 v37, v2
	v_mov_b32_e32 v42, v2
	v_mov_b32_e32 v43, v2
	v_mov_b32_e32 v44, v2
	v_mov_b32_e32 v45, v2
	v_mov_b32_e32 v50, v2
	v_mov_b32_e32 v51, v2
	v_mov_b32_e32 v52, v2
	v_mov_b32_e32 v53, v2
	v_mov_b32_e32 v54, v2
	v_mov_b32_e32 v55, v2
	v_mov_b32_e32 v56, v2
	v_mov_b32_e32 v57, v2
	v_mov_b32_e32 v58, v2
	v_mov_b32_e32 v59, v2
	v_mov_b32_e32 v60, v2
	v_mov_b32_e32 v61, v2
	v_mov_b32_e32 v62, v2
	v_mov_b32_e32 v63, v2
	v_mov_b32_e32 v64, v2
	v_mov_b32_e32 v65, v2
	v_mov_b32_e32 v66, v2
	v_mov_b32_e32 v67, v2
	v_mov_b32_e32 v68, v2
	v_mov_b32_e32 v69, v2
	v_mov_b32_e32 v70, v2
	v_mov_b32_e32 v71, v2
	v_mov_b32_e32 v72, v2
	v_mov_b32_e32 v73, v2
	v_mov_b32_e32 v78, v2
	v_mov_b32_e32 v79, v2
	v_mov_b32_e32 v80, v2
	v_mov_b32_e32 v81, v2
	v_mov_b32_e32 v86, v2
	v_mov_b32_e32 v87, v2
	v_mov_b32_e32 v88, v2
	v_mov_b32_e32 v89, v2
	v_mov_b32_e32 v94, v2
	v_mov_b32_e32 v95, v2
	v_mov_b32_e32 v96, v2
	v_mov_b32_e32 v97, v2
	v_mov_b32_e32 v98, v2
	v_mov_b32_e32 v99, v2
	v_mov_b32_e32 v100, v2
	v_mov_b32_e32 v101, v2
	v_mov_b32_e32 v102, v2
	v_mov_b32_e32 v103, v2
	v_mov_b32_e32 v104, v2
	v_mov_b32_e32 v105, v2
	v_mov_b32_e32 v106, v2
	v_mov_b32_e32 v107, v2
	v_mov_b32_e32 v108, v2
	v_mov_b32_e32 v109, v2
	v_mov_b32_e32 v74, v2
	v_mov_b32_e32 v75, v2
	v_mov_b32_e32 v76, v2
	v_mov_b32_e32 v77, v2
	v_mov_b32_e32 v82, v2
	v_mov_b32_e32 v83, v2
	v_mov_b32_e32 v84, v2
	v_mov_b32_e32 v85, v2
	v_mov_b32_e32 v90, v2
	v_mov_b32_e32 v91, v2
	v_mov_b32_e32 v92, v2
	v_mov_b32_e32 v93, v2
	v_mov_b32_e32 v110, v2
	v_mov_b32_e32 v111, v2
	v_mov_b32_e32 v112, v2
	v_mov_b32_e32 v113, v2
	v_mov_b32_e32 v114, v2
	v_mov_b32_e32 v115, v2
	v_mov_b32_e32 v116, v2
	v_mov_b32_e32 v117, v2
	v_mov_b32_e32 v118, v2
	v_mov_b32_e32 v119, v2
	v_mov_b32_e32 v120, v2
	v_mov_b32_e32 v121, v2
	v_mov_b32_e32 v122, v2
	v_mov_b32_e32 v123, v2
	v_mov_b32_e32 v124, v2
	v_mov_b32_e32 v125, v2
	v_mov_b32_e32 v126, v2
	v_mov_b32_e32 v127, v2
	v_mov_b32_e32 v128, v2
	v_mov_b32_e32 v129, v2
	s_cmp_gt_u32 s44, 1
	s_cselect_b32 s32, -2, 1
.LBB0_793:
	ds_read_b128 v[136:139], v148
	ds_read_b128 v[152:155], v148 offset:1024
	ds_read_b128 v[156:159], v148 offset:2048
	ds_read_b128 v[160:163], v148 offset:3072
	ds_read_b128 v[164:167], v149
	ds_read_b128 v[168:171], v149 offset:1024
	ds_read_b128 v[172:175], v149 offset:2048
	ds_read_b128 v[176:179], v149 offset:3072
	s_add_u32 s0, s30, 0x80
	s_addc_u32 s1, s31, 0
	s_cmp_eq_u32 s55, 28
	s_cselect_b32 s35, s25, s1
	s_cselect_b32 s34, s24, s0
	s_cselect_b32 s1, s27, s23
	s_cselect_b32 s0, s26, s21
	v_mov_b32_e32 v130, v144
	ds_read_b128 v[180:183], v150
	ds_read_b128 v[184:187], v150 offset:1024
	ds_read_b128 v[188:191], v150 offset:2048
	ds_read_b128 v[192:195], v150 offset:3072
	ds_read_b128 v[196:199], v150 offset:4096
	ds_read_b128 v[200:203], v150 offset:5120
	ds_read_b128 v[204:207], v150 offset:6144
	ds_read_b128 v[208:211], v150 offset:7168
	s_add_i32 m0, s29, 0xc000
	s_nop 0
	global_load_lds_dwordx4 v130, s[30:31]
	v_mov_b32_e32 v130, v146
	s_add_i32 m0, s29, 0xe000
	s_nop 0
	global_load_lds_dwordx4 v130, s[30:31]
	s_cmp_eq_u32 s55, s32
	s_cbranch_scc1 .Lskipw_p6_0
	s_waitcnt vmcnt(8)
.Lskipw_p6_0:
	s_waitcnt lgkmcnt(0)
	s_barrier
	s_setprio 1
	s_waitcnt lgkmcnt(0)
	v_mfma_f32_16x16x32_bf16 v[126:129], v[136:139], v[180:183], v[126:129]
	v_mfma_f32_16x16x32_bf16 v[122:125], v[156:159], v[180:183], v[122:125]
	v_mfma_f32_16x16x32_bf16 v[118:121], v[136:139], v[188:191], v[118:121]
	v_mfma_f32_16x16x32_bf16 v[114:117], v[156:159], v[188:191], v[114:117]
	v_mfma_f32_16x16x32_bf16 v[110:113], v[136:139], v[196:199], v[110:113]
	v_mfma_f32_16x16x32_bf16 v[90:93], v[156:159], v[196:199], v[90:93]
	v_mfma_f32_16x16x32_bf16 v[82:85], v[136:139], v[204:207], v[82:85]
	v_mfma_f32_16x16x32_bf16 v[74:77], v[156:159], v[204:207], v[74:77]
	v_mfma_f32_16x16x32_bf16 v[126:129], v[152:155], v[184:187], v[126:129]
	v_mfma_f32_16x16x32_bf16 v[122:125], v[160:163], v[184:187], v[122:125]
	v_mfma_f32_16x16x32_bf16 v[118:121], v[152:155], v[192:195], v[118:121]
	v_mfma_f32_16x16x32_bf16 v[114:117], v[160:163], v[192:195], v[114:117]
	v_mfma_f32_16x16x32_bf16 v[110:113], v[152:155], v[200:203], v[110:113]
	v_mfma_f32_16x16x32_bf16 v[90:93], v[160:163], v[200:203], v[90:93]
	v_mfma_f32_16x16x32_bf16 v[82:85], v[152:155], v[208:211], v[82:85]
	v_mfma_f32_16x16x32_bf16 v[74:77], v[160:163], v[208:211], v[74:77]
	s_setprio 0
	s_setprio 1
	v_mfma_f32_16x16x32_bf16 v[106:109], v[164:167], v[180:183], v[106:109]
	v_mfma_f32_16x16x32_bf16 v[102:105], v[172:175], v[180:183], v[102:105]
	v_mfma_f32_16x16x32_bf16 v[98:101], v[164:167], v[188:191], v[98:101]
	v_mfma_f32_16x16x32_bf16 v[94:97], v[172:175], v[188:191], v[94:97]
	v_mfma_f32_16x16x32_bf16 v[86:89], v[164:167], v[196:199], v[86:89]
	v_mfma_f32_16x16x32_bf16 v[78:81], v[172:175], v[196:199], v[78:81]
	v_mfma_f32_16x16x32_bf16 v[70:73], v[164:167], v[204:207], v[70:73]
	v_mfma_f32_16x16x32_bf16 v[66:69], v[172:175], v[204:207], v[66:69]
	v_mfma_f32_16x16x32_bf16 v[106:109], v[168:171], v[184:187], v[106:109]
	v_mfma_f32_16x16x32_bf16 v[102:105], v[176:179], v[184:187], v[102:105]
	v_mfma_f32_16x16x32_bf16 v[98:101], v[168:171], v[192:195], v[98:101]
	v_mfma_f32_16x16x32_bf16 v[94:97], v[176:179], v[192:195], v[94:97]
	v_mfma_f32_16x16x32_bf16 v[86:89], v[168:171], v[200:203], v[86:89]
	v_mfma_f32_16x16x32_bf16 v[78:81], v[176:179], v[200:203], v[78:81]
	v_mfma_f32_16x16x32_bf16 v[70:73], v[168:171], v[208:211], v[70:73]
	v_mfma_f32_16x16x32_bf16 v[66:69], v[176:179], v[208:211], v[66:69]
	s_setprio 0
	s_barrier
	v_mov_b32_e32 v130, v1
	s_add_i32 s56, s50, s40
	ds_read_b128 v[180:183], v150 offset:16384
	ds_read_b128 v[184:187], v150 offset:17408
	ds_read_b128 v[188:191], v150 offset:18432
	ds_read_b128 v[192:195], v150 offset:19456
	ds_read_b128 v[196:199], v150 offset:20480
	ds_read_b128 v[200:203], v150 offset:21504
	ds_read_b128 v[204:207], v150 offset:22528
	ds_read_b128 v[208:211], v150 offset:23552
	s_mov_b32 m0, s56
	s_nop 0
	global_load_lds_dwordx4 v130, s[0:1]
	v_mov_b32_e32 v130, v142
	s_add_i32 m0, s56, 0x2000
	s_add_u32 s56, s0, 0x80000
	global_load_lds_dwordx4 v130, s[0:1]
	s_addc_u32 s57, s1, 0
	v_mov_b32_e32 v130, v1
	s_add_i32 s58, s51, s40
	s_mov_b32 m0, s58
	s_nop 0
	global_load_lds_dwordx4 v130, s[56:57]
	v_mov_b32_e32 v130, v142
	s_add_i32 m0, s58, 0x2000
	s_nop 0
	global_load_lds_dwordx4 v130, s[56:57]
	v_mov_b32_e32 v130, v143
	s_mov_b32 m0, s29
	s_nop 0
	global_load_lds_dwordx4 v130, s[34:35]
	v_mov_b32_e32 v130, v145
	s_mov_b32 m0, s41
	s_nop 0
	global_load_lds_dwordx4 v130, s[34:35]
	s_cmp_eq_u32 s55, s32
	s_cbranch_scc1 .Lskipw_p6_1
	s_waitcnt vmcnt(8)
.Lskipw_p6_1:
	s_waitcnt lgkmcnt(0)
	s_barrier
	s_setprio 1
	s_waitcnt lgkmcnt(0)
	v_mfma_f32_16x16x32_bf16 v[62:65], v[136:139], v[180:183], v[62:65]
	v_mfma_f32_16x16x32_bf16 v[58:61], v[156:159], v[180:183], v[58:61]
	v_mfma_f32_16x16x32_bf16 v[54:57], v[136:139], v[188:191], v[54:57]
	v_mfma_f32_16x16x32_bf16 v[50:53], v[156:159], v[188:191], v[50:53]
	v_mfma_f32_16x16x32_bf16 v[42:45], v[136:139], v[196:199], v[42:45]
	v_mfma_f32_16x16x32_bf16 v[34:37], v[156:159], v[196:199], v[34:37]
	v_mfma_f32_16x16x32_bf16 v[22:25], v[136:139], v[204:207], v[22:25]
	v_mfma_f32_16x16x32_bf16 v[10:13], v[156:159], v[204:207], v[10:13]
	v_mfma_f32_16x16x32_bf16 v[62:65], v[152:155], v[184:187], v[62:65]
	v_mfma_f32_16x16x32_bf16 v[58:61], v[160:163], v[184:187], v[58:61]
	v_mfma_f32_16x16x32_bf16 v[54:57], v[152:155], v[192:195], v[54:57]
	v_mfma_f32_16x16x32_bf16 v[50:53], v[160:163], v[192:195], v[50:53]
	v_mfma_f32_16x16x32_bf16 v[42:45], v[152:155], v[200:203], v[42:45]
	v_mfma_f32_16x16x32_bf16 v[34:37], v[160:163], v[200:203], v[34:37]
	v_mfma_f32_16x16x32_bf16 v[22:25], v[152:155], v[208:211], v[22:25]
	v_mfma_f32_16x16x32_bf16 v[10:13], v[160:163], v[208:211], v[10:13]
	s_setprio 0
	s_setprio 1
	v_mfma_f32_16x16x32_bf16 v[46:49], v[164:167], v[180:183], v[46:49]
	v_mfma_f32_16x16x32_bf16 v[38:41], v[172:175], v[180:183], v[38:41]
	v_mfma_f32_16x16x32_bf16 v[30:33], v[164:167], v[188:191], v[30:33]
	v_mfma_f32_16x16x32_bf16 v[26:29], v[172:175], v[188:191], v[26:29]
	v_mfma_f32_16x16x32_bf16 v[18:21], v[164:167], v[196:199], v[18:21]
	v_mfma_f32_16x16x32_bf16 v[14:17], v[172:175], v[196:199], v[14:17]
	v_mfma_f32_16x16x32_bf16 v[6:9], v[164:167], v[204:207], v[6:9]
	v_mfma_f32_16x16x32_bf16 v[2:5], v[172:175], v[204:207], v[2:5]
	v_mfma_f32_16x16x32_bf16 v[46:49], v[168:171], v[184:187], v[46:49]
	v_mfma_f32_16x16x32_bf16 v[38:41], v[176:179], v[184:187], v[38:41]
	v_mfma_f32_16x16x32_bf16 v[30:33], v[168:171], v[192:195], v[30:33]
	v_mfma_f32_16x16x32_bf16 v[26:29], v[176:179], v[192:195], v[26:29]
	v_mfma_f32_16x16x32_bf16 v[18:21], v[168:171], v[200:203], v[18:21]
	v_mfma_f32_16x16x32_bf16 v[14:17], v[176:179], v[200:203], v[14:17]
	v_mfma_f32_16x16x32_bf16 v[6:9], v[168:171], v[208:211], v[6:9]
	v_mfma_f32_16x16x32_bf16 v[2:5], v[176:179], v[208:211], v[2:5]
	s_setprio 0
	s_barrier
	s_add_i32 s56, 0, 0x18000
	v_add_u32_e32 v130, s56, v147
	s_add_i32 s57, 0, 0x1c000
	ds_read_b128 v[136:139], v130
	ds_read_b128 v[152:155], v130 offset:1024
	ds_read_b128 v[156:159], v130 offset:2048
	ds_read_b128 v[160:163], v130 offset:3072
	v_add_u32_e32 v130, s57, v147
	ds_read_b128 v[164:167], v130
	ds_read_b128 v[168:171], v130 offset:1024
	ds_read_b128 v[172:175], v130 offset:2048
	ds_read_b128 v[176:179], v130 offset:3072
	v_mov_b32_e32 v130, v144
	s_mov_b32 m0, s42
	ds_read_b128 v[180:183], v150 offset:32768
	ds_read_b128 v[184:187], v150 offset:33792
	ds_read_b128 v[188:191], v150 offset:34816
	ds_read_b128 v[192:195], v150 offset:35840
	ds_read_b128 v[196:199], v150 offset:36864
	ds_read_b128 v[200:203], v150 offset:37888
	ds_read_b128 v[204:207], v150 offset:38912
	ds_read_b128 v[208:211], v150 offset:39936
	s_nop 0
	global_load_lds_dwordx4 v130, s[34:35]
	v_mov_b32_e32 v130, v146
	s_mov_b32 m0, s43
	s_nop 0
	global_load_lds_dwordx4 v130, s[34:35]
	s_waitcnt vmcnt(8)
	s_waitcnt lgkmcnt(0)
	s_barrier
	s_setprio 1
	s_waitcnt lgkmcnt(0)
	v_mfma_f32_16x16x32_bf16 v[126:129], v[136:139], v[180:183], v[126:129]
	v_mfma_f32_16x16x32_bf16 v[122:125], v[156:159], v[180:183], v[122:125]
	v_mfma_f32_16x16x32_bf16 v[118:121], v[136:139], v[188:191], v[118:121]
	v_mfma_f32_16x16x32_bf16 v[114:117], v[156:159], v[188:191], v[114:117]
	v_mfma_f32_16x16x32_bf16 v[110:113], v[136:139], v[196:199], v[110:113]
	v_mfma_f32_16x16x32_bf16 v[90:93], v[156:159], v[196:199], v[90:93]
	v_mfma_f32_16x16x32_bf16 v[82:85], v[136:139], v[204:207], v[82:85]
	v_mfma_f32_16x16x32_bf16 v[74:77], v[156:159], v[204:207], v[74:77]
	v_mfma_f32_16x16x32_bf16 v[126:129], v[152:155], v[184:187], v[126:129]
	v_mfma_f32_16x16x32_bf16 v[122:125], v[160:163], v[184:187], v[122:125]
	v_mfma_f32_16x16x32_bf16 v[118:121], v[152:155], v[192:195], v[118:121]
	v_mfma_f32_16x16x32_bf16 v[114:117], v[160:163], v[192:195], v[114:117]
	v_mfma_f32_16x16x32_bf16 v[110:113], v[152:155], v[200:203], v[110:113]
	v_mfma_f32_16x16x32_bf16 v[90:93], v[160:163], v[200:203], v[90:93]
	v_mfma_f32_16x16x32_bf16 v[82:85], v[152:155], v[208:211], v[82:85]
	v_mfma_f32_16x16x32_bf16 v[74:77], v[160:163], v[208:211], v[74:77]
	s_setprio 0
	s_setprio 1
	v_mfma_f32_16x16x32_bf16 v[106:109], v[164:167], v[180:183], v[106:109]
	v_mfma_f32_16x16x32_bf16 v[102:105], v[172:175], v[180:183], v[102:105]
	v_mfma_f32_16x16x32_bf16 v[98:101], v[164:167], v[188:191], v[98:101]
	v_mfma_f32_16x16x32_bf16 v[94:97], v[172:175], v[188:191], v[94:97]
	v_mfma_f32_16x16x32_bf16 v[86:89], v[164:167], v[196:199], v[86:89]
	v_mfma_f32_16x16x32_bf16 v[78:81], v[172:175], v[196:199], v[78:81]
	v_mfma_f32_16x16x32_bf16 v[70:73], v[164:167], v[204:207], v[70:73]
	v_mfma_f32_16x16x32_bf16 v[66:69], v[172:175], v[204:207], v[66:69]
	v_mfma_f32_16x16x32_bf16 v[106:109], v[168:171], v[184:187], v[106:109]
	v_mfma_f32_16x16x32_bf16 v[102:105], v[176:179], v[184:187], v[102:105]
	v_mfma_f32_16x16x32_bf16 v[98:101], v[168:171], v[192:195], v[98:101]
	v_mfma_f32_16x16x32_bf16 v[94:97], v[176:179], v[192:195], v[94:97]
	v_mfma_f32_16x16x32_bf16 v[86:89], v[168:171], v[200:203], v[86:89]
	v_mfma_f32_16x16x32_bf16 v[78:81], v[176:179], v[200:203], v[78:81]
	v_mfma_f32_16x16x32_bf16 v[70:73], v[168:171], v[208:211], v[70:73]
	v_mfma_f32_16x16x32_bf16 v[66:69], v[176:179], v[208:211], v[66:69]
	s_setprio 0
	s_barrier
; #define PG8_BAR __builtin_amdgcn_s_barrier()
; template <class Epi, bool GATHER, bool EXPERT, bool FP8>
; DI void gemm_phase(LAS unsigned char* lds, const Gemm g, const StaticOrder& S, const Epi& E) {
;     ...
;         for (int t = 0; t < nt; t += 2) {
;             const bool last = (t == nt - 2);
;             const char* a1 = cA + (size_t)(t + 1) * kstep;
;             const char* a2 = last ? nA : cA + (size_t)(t + 2) * kstep; const char* b2 = last ? nB : cB + (size_t)(t + 2) * kstep;
;             const char* a3 = a2 + kstep; const char* b3 = b2 + kstep;
;             unsigned o00 = coffA[0][0], o01 = coffA[0][1], o10 = coffA[1][0], o11 = coffA[1][1];
;             if (GATHER && last && has_next) {
;                 o00 = sp[0] * (unsigned)(K * 2) + (unsigned)C0x2; o01 = sp[512] * (unsigned)(K * 2) + (unsigned)C1x2;
;                 o10 = sp[1024] * (unsigned)(K * 2) + (unsigned)C0x2; o11 = sp[1536] * (unsigned)(K * 2) + (unsigned)C1x2; }
;             PG8_TRIP(a1, a2, b2, a3, b3, o00, o01, o10, o11);
;             if (last) { coffA[0][0] = o00; coffA[0][1] = o01; coffA[1][0] = o10; coffA[1][1] = o11; }
;         }
;         if (wr == 0) PG8_BAR;
	v_mov_b32_e32 v130, v1
	ds_read_b128 v[180:183], v150 offset:49152
	ds_read_b128 v[184:187], v150 offset:50176
	ds_read_b128 v[188:191], v150 offset:51200
	ds_read_b128 v[192:195], v150 offset:52224
	ds_read_b128 v[196:199], v150 offset:53248
	ds_read_b128 v[200:203], v150 offset:54272
	ds_read_b128 v[204:207], v150 offset:55296
	ds_read_b128 v[208:211], v150 offset:56320
	s_add_i32 s56, s56, s40
	v_lshl_add_u64 v[140:141], s[0:1], 0, v[130:131]
	v_lshl_add_u64 v[140:141], v[140:141], 0, s[68:69]
	s_mov_b32 m0, s56
	v_mov_b32_e32 v130, v142
	global_load_lds_dwordx4 v[140:141], off
	s_add_i32 m0, s56, 0x2000
	s_nop 0
	v_lshl_add_u64 v[140:141], s[0:1], 0, v[130:131]
	s_add_u32 s0, s0, 0x80080
	v_lshl_add_u64 v[140:141], v[140:141], 0, s[68:69]
	s_addc_u32 s1, s1, 0
	v_mov_b32_e32 v130, v1
	s_add_i32 s56, s57, s40
	global_load_lds_dwordx4 v[140:141], off
	s_mov_b32 m0, s56
	s_nop 0
	global_load_lds_dwordx4 v130, s[0:1]
	v_mov_b32_e32 v130, v142
	s_add_i32 m0, s56, 0x2000
	s_nop 0
	global_load_lds_dwordx4 v130, s[0:1]
	v_mov_b32_e32 v130, v143
	s_mov_b32 m0, s47
	v_lshl_add_u64 v[140:141], s[34:35], 0, v[130:131]
	v_lshl_add_u64 v[140:141], v[140:141], 0, s[68:69]
	v_mov_b32_e32 v130, v145
	global_load_lds_dwordx4 v[140:141], off
	s_mov_b32 m0, s48
	v_lshl_add_u64 v[140:141], s[34:35], 0, v[130:131]
	v_lshl_add_u64 v[140:141], v[140:141], 0, s[68:69]
	global_load_lds_dwordx4 v[140:141], off
	s_waitcnt vmcnt(8)
	s_waitcnt lgkmcnt(0)
	s_barrier
	s_setprio 1
	s_waitcnt lgkmcnt(0)
	v_mfma_f32_16x16x32_bf16 v[62:65], v[136:139], v[180:183], v[62:65]
	v_mfma_f32_16x16x32_bf16 v[58:61], v[156:159], v[180:183], v[58:61]
	v_mfma_f32_16x16x32_bf16 v[54:57], v[136:139], v[188:191], v[54:57]
	v_mfma_f32_16x16x32_bf16 v[50:53], v[156:159], v[188:191], v[50:53]
	v_mfma_f32_16x16x32_bf16 v[42:45], v[136:139], v[196:199], v[42:45]
	v_mfma_f32_16x16x32_bf16 v[34:37], v[156:159], v[196:199], v[34:37]
	v_mfma_f32_16x16x32_bf16 v[22:25], v[136:139], v[204:207], v[22:25]
	v_mfma_f32_16x16x32_bf16 v[10:13], v[156:159], v[204:207], v[10:13]
	v_mfma_f32_16x16x32_bf16 v[62:65], v[152:155], v[184:187], v[62:65]
	v_mfma_f32_16x16x32_bf16 v[58:61], v[160:163], v[184:187], v[58:61]
	v_mfma_f32_16x16x32_bf16 v[54:57], v[152:155], v[192:195], v[54:57]
	v_mfma_f32_16x16x32_bf16 v[50:53], v[160:163], v[192:195], v[50:53]
	v_mfma_f32_16x16x32_bf16 v[42:45], v[152:155], v[200:203], v[42:45]
	v_mfma_f32_16x16x32_bf16 v[34:37], v[160:163], v[200:203], v[34:37]
	v_mfma_f32_16x16x32_bf16 v[22:25], v[152:155], v[208:211], v[22:25]
	v_mfma_f32_16x16x32_bf16 v[10:13], v[160:163], v[208:211], v[10:13]
	s_setprio 0
	s_setprio 1
	v_mfma_f32_16x16x32_bf16 v[46:49], v[164:167], v[180:183], v[46:49]
	v_mfma_f32_16x16x32_bf16 v[38:41], v[172:175], v[180:183], v[38:41]
	v_mfma_f32_16x16x32_bf16 v[30:33], v[164:167], v[188:191], v[30:33]
	v_mfma_f32_16x16x32_bf16 v[26:29], v[172:175], v[188:191], v[26:29]
	v_mfma_f32_16x16x32_bf16 v[18:21], v[164:167], v[196:199], v[18:21]
	v_mfma_f32_16x16x32_bf16 v[14:17], v[172:175], v[196:199], v[14:17]
	v_mfma_f32_16x16x32_bf16 v[6:9], v[164:167], v[204:207], v[6:9]
	v_mfma_f32_16x16x32_bf16 v[2:5], v[172:175], v[204:207], v[2:5]
	v_mfma_f32_16x16x32_bf16 v[46:49], v[168:171], v[184:187], v[46:49]
	v_mfma_f32_16x16x32_bf16 v[38:41], v[176:179], v[184:187], v[38:41]
	v_mfma_f32_16x16x32_bf16 v[30:33], v[168:171], v[192:195], v[30:33]
	v_mfma_f32_16x16x32_bf16 v[26:29], v[176:179], v[192:195], v[26:29]
	v_mfma_f32_16x16x32_bf16 v[18:21], v[168:171], v[200:203], v[18:21]
	v_mfma_f32_16x16x32_bf16 v[14:17], v[176:179], v[200:203], v[14:17]
	v_mfma_f32_16x16x32_bf16 v[6:9], v[168:171], v[208:211], v[6:9]
	v_mfma_f32_16x16x32_bf16 v[2:5], v[176:179], v[208:211], v[2:5]
	s_setprio 0
	s_barrier
	s_add_i32 s55, s55, 2
	s_add_u32 s21, s21, 0x100
	s_addc_u32 s23, s23, 0
	s_add_u32 s30, s30, 0x100
	s_addc_u32 s31, s31, 0
	s_cmp_gt_u32 s55, 29
	s_cbranch_scc0 .LBB0_793
	s_and_b64 vcc, exec, s[72:73]
	s_cbranch_vccz .LBB0_796
	s_barrier

; #define LAS __attribute__((address_space(3)))
; template <class Epi, bool GATHER, bool EXPERT, bool FP8>
; DI void gemm_phase(LAS unsigned char* lds, const Gemm g, const StaticOrder& S, const Epi& E) {
;     ...
;         if (GATHER) { int t2_ = threadIdx.x; asm volatile("" : "+v"(t2_)); int R0_, C0_, R1_, C1_; stage_rc(t2_ * 16, R0_, C0_); stage_rc(t2_ * 16 + 8192, R1_, C1_); C0x2 = C0_ * 2; C1x2 = C1_ * 2;
;             sp = (const LAS unsigned*)(stash + (t2_ & 63) * 4); }
;     ...
; #pragma unroll
;         for (int a = 0; a < 2; ++a)
; #pragma unroll
;             for (int b = 0; b < 2; ++b)
; #pragma unroll
;                 for (int m = 0; m < 4; ++m)
; #pragma unroll
;                     for (int n = 0; n < 2; ++n) acc[a][b][m][n] = (f32x4){0.f, 0.f, 0.f, 0.f};
.LBB0_1083:
	v_mov_b32_e32 v2, v0
	s_add_u32 s25, s36, 0x100
	v_bfe_i32 v5, v2, 27, 1
	v_lshlrev_b32_e32 v3, 4, v2
	v_lshrrev_b32_e32 v5, 22, v5
	v_add_u32_e32 v5, v3, v5
	v_and_b32_e32 v5, 0xfffffc00, v5
	v_sub_u32_e32 v5, v3, v5
	v_lshrrev_b32_e32 v6, 4, v5
	v_bitop3_b32 v6, v6, v5, 32 bitop3:0x6c
	v_ashrrev_i32_e32 v5, 31, v5
	v_lshrrev_b32_e32 v5, 26, v5
	v_add_u32_e32 v5, v6, v5
	v_and_b32_e32 v5, 0xc0, v5
	v_add_u32_e32 v3, 0x2000, v3
	v_sub_u32_e32 v5, v6, v5
	v_ashrrev_i32_e32 v6, 31, v3
	v_lshrrev_b32_e32 v6, 22, v6
	v_add_u32_e32 v6, v3, v6
	v_ashrrev_i32_e32 v6, 10, v6
	v_mul_i32_i24_e32 v7, 0x400, v6
	v_sub_u32_e32 v3, v3, v7
	v_lshrrev_b32_e32 v7, 4, v3
	v_bitop3_b32 v7, v7, v3, 32 bitop3:0x6c
	v_ashrrev_i32_e32 v3, 31, v3
	v_lshrrev_b32_e32 v3, 26, v3
	v_add_u32_e32 v3, v7, v3
	v_ashrrev_i32_e32 v4, 31, v2
	v_and_b32_e32 v3, 0xc0, v3
	v_lshrrev_b32_e32 v4, 26, v4
	v_sub_u32_e32 v3, v7, v3
	v_add_u32_e32 v4, v2, v4
	v_lshlrev_b32_e32 v6, 5, v6
	v_ashrrev_i16_sdwa v3, v1, sext(v3) dst_sel:DWORD dst_unused:UNUSED_PAD src0_sel:DWORD src1_sel:BYTE_0
	v_lshrrev_b32_e32 v4, 1, v4
	v_ashrrev_i16_sdwa v5, v1, sext(v5) dst_sel:DWORD dst_unused:UNUSED_PAD src0_sel:DWORD src1_sel:BYTE_0
	v_and_b32_e32 v6, 32, v6
	v_bfe_i32 v3, v3, 0, 16
	v_lshlrev_b32_e32 v2, 2, v2
	.p2align 8
	s_addc_u32 s72, s37, 0
	v_and_b32_e32 v4, 32, v4
	v_bfe_i32 v5, v5, 0, 16
	v_add_lshl_u32 v131, v6, v3, 1
	v_and_b32_e32 v3, 0xfc, v2
	s_add_u32 s36, s0, 0x80
	v_mov_b32_e32 v2, 0
	v_add_lshl_u32 v130, v4, v5, 1
	s_addc_u32 s37, s1, 0
	s_mov_b32 s0, -2
	v_add_u32_e32 v132, s57, v3
	v_mov_b32_e32 v3, v2
	v_mov_b32_e32 v4, v2
	v_mov_b32_e32 v5, v2
	v_mov_b32_e32 v10, v2
	v_mov_b32_e32 v11, v2
	v_mov_b32_e32 v12, v2
	v_mov_b32_e32 v13, v2
	v_mov_b32_e32 v18, v2
	v_mov_b32_e32 v19, v2
	v_mov_b32_e32 v20, v2
	v_mov_b32_e32 v21, v2
	v_mov_b32_e32 v26, v2
	v_mov_b32_e32 v27, v2
	v_mov_b32_e32 v28, v2
	v_mov_b32_e32 v29, v2
	v_mov_b32_e32 v34, v2
	v_mov_b32_e32 v35, v2
	v_mov_b32_e32 v36, v2
	v_mov_b32_e32 v37, v2
	v_mov_b32_e32 v42, v2
	v_mov_b32_e32 v43, v2
	v_mov_b32_e32 v44, v2
	v_mov_b32_e32 v45, v2
	v_mov_b32_e32 v50, v2
	v_mov_b32_e32 v51, v2
	v_mov_b32_e32 v52, v2
	v_mov_b32_e32 v53, v2
	v_mov_b32_e32 v58, v2
	v_mov_b32_e32 v59, v2
	v_mov_b32_e32 v60, v2
	v_mov_b32_e32 v61, v2
	v_mov_b32_e32 v6, v2
	v_mov_b32_e32 v7, v2
	v_mov_b32_e32 v8, v2
	v_mov_b32_e32 v9, v2
	v_mov_b32_e32 v14, v2
	v_mov_b32_e32 v15, v2
	v_mov_b32_e32 v16, v2
	v_mov_b32_e32 v17, v2
	v_mov_b32_e32 v22, v2
	v_mov_b32_e32 v23, v2
	v_mov_b32_e32 v24, v2
	v_mov_b32_e32 v25, v2
	v_mov_b32_e32 v30, v2
	v_mov_b32_e32 v31, v2
	v_mov_b32_e32 v32, v2
	v_mov_b32_e32 v33, v2
	v_mov_b32_e32 v38, v2
	v_mov_b32_e32 v39, v2
	v_mov_b32_e32 v40, v2
	v_mov_b32_e32 v41, v2
	v_mov_b32_e32 v46, v2
	v_mov_b32_e32 v47, v2
	v_mov_b32_e32 v48, v2
	v_mov_b32_e32 v49, v2
	v_mov_b32_e32 v54, v2
	v_mov_b32_e32 v55, v2
	v_mov_b32_e32 v56, v2
	v_mov_b32_e32 v57, v2
	v_mov_b32_e32 v62, v2
	v_mov_b32_e32 v63, v2
	v_mov_b32_e32 v64, v2
	v_mov_b32_e32 v65, v2
	v_mov_b32_e32 v66, v2
	v_mov_b32_e32 v67, v2
	v_mov_b32_e32 v68, v2
	v_mov_b32_e32 v69, v2
	v_mov_b32_e32 v74, v2
	v_mov_b32_e32 v75, v2
	v_mov_b32_e32 v76, v2
	v_mov_b32_e32 v77, v2
	v_mov_b32_e32 v82, v2
	v_mov_b32_e32 v83, v2
	v_mov_b32_e32 v84, v2
	v_mov_b32_e32 v85, v2
	v_mov_b32_e32 v90, v2
	v_mov_b32_e32 v91, v2
	v_mov_b32_e32 v92, v2
	v_mov_b32_e32 v93, v2
	v_mov_b32_e32 v98, v2
	v_mov_b32_e32 v99, v2
	v_mov_b32_e32 v100, v2
	v_mov_b32_e32 v101, v2
	v_mov_b32_e32 v106, v2
	v_mov_b32_e32 v107, v2
	v_mov_b32_e32 v108, v2
	v_mov_b32_e32 v109, v2
	v_mov_b32_e32 v122, v2
	v_mov_b32_e32 v123, v2
	v_mov_b32_e32 v124, v2
	v_mov_b32_e32 v125, v2
	v_mov_b32_e32 v138, v2
	v_mov_b32_e32 v139, v2
	v_mov_b32_e32 v140, v2
	v_mov_b32_e32 v141, v2
	v_mov_b32_e32 v70, v2
	v_mov_b32_e32 v71, v2
	v_mov_b32_e32 v72, v2
	v_mov_b32_e32 v73, v2
	v_mov_b32_e32 v78, v2
	v_mov_b32_e32 v79, v2
	v_mov_b32_e32 v80, v2
	v_mov_b32_e32 v81, v2
	v_mov_b32_e32 v86, v2
	v_mov_b32_e32 v87, v2
	v_mov_b32_e32 v88, v2
	v_mov_b32_e32 v89, v2
	v_mov_b32_e32 v94, v2
	v_mov_b32_e32 v95, v2
	v_mov_b32_e32 v96, v2
	v_mov_b32_e32 v97, v2
	v_mov_b32_e32 v102, v2
	v_mov_b32_e32 v103, v2
	v_mov_b32_e32 v104, v2
	v_mov_b32_e32 v105, v2
	v_mov_b32_e32 v114, v2
	v_mov_b32_e32 v115, v2
	v_mov_b32_e32 v116, v2
	v_mov_b32_e32 v117, v2
	v_mov_b32_e32 v134, v2
	v_mov_b32_e32 v135, v2
	v_mov_b32_e32 v136, v2
	v_mov_b32_e32 v137, v2
	v_mov_b32_e32 v142, v2
	v_mov_b32_e32 v143, v2
	v_mov_b32_e32 v144, v2
	v_mov_b32_e32 v145, v2
	s_cmp_gt_u32 s56, 1
	s_cselect_b32 s32, -2, 1
	s_branch .LBB0_1085

.LBB0_1087:
	v_add_u32_e32 v110, s67, v164
	ds_read_b128 v[168:171], v110
	ds_read_b128 v[172:175], v110 offset:1024
	ds_read_b128 v[176:179], v110 offset:2048
	ds_read_b128 v[180:183], v110 offset:3072
	v_add_u32_e32 v110, s68, v164
	ds_read_b128 v[184:187], v110
	ds_read_b128 v[188:191], v110 offset:1024
	ds_read_b128 v[192:195], v110 offset:2048
	ds_read_b128 v[196:199], v110 offset:3072
	s_add_u32 s1, s36, 0x80
	s_addc_u32 s42, s37, 0
	s_and_b64 s[40:41], s[38:39], exec
	s_cselect_b32 s41, s79, s42
	s_cselect_b32 s40, s78, s1
	s_cselect_b32 s43, s83, s72
	s_cselect_b32 s42, s82, s25
	v_mov_b32_e32 v110, v160
	ds_read_b128 v[200:203], v165
	ds_read_b128 v[204:207], v165 offset:1024
	ds_read_b128 v[208:211], v165 offset:2048
	ds_read_b128 v[212:215], v165 offset:3072
	ds_read_b128 v[216:219], v165 offset:4096
	ds_read_b128 v[220:223], v165 offset:5120
	ds_read_b128 v[226:229], v165 offset:6144
	ds_read_b128 v[230:233], v165 offset:7168
	s_add_i32 m0, s52, 0xc000
	s_nop 0
	global_load_lds_dwordx4 v110, s[36:37]
	v_mov_b32_e32 v110, v161
	s_add_i32 m0, s52, 0xe000
	s_nop 0
	global_load_lds_dwordx4 v110, s[36:37]
	s_cmp_eq_u32 s0, s32
	s_cbranch_scc1 .Lskipw_p9_0
	s_waitcnt vmcnt(8)
.Lskipw_p9_0:
	s_waitcnt lgkmcnt(0)
	s_barrier
	s_setprio 1
	s_waitcnt lgkmcnt(0)
	v_mfma_scale_f32_16x16x128_f8f6f4 v[114:117], v[168:175], v[208:215], v[114:117], v166, v166 op_sel_hi:[0,0,0]
	v_mfma_scale_f32_16x16x128_f8f6f4 v[102:105], v[176:183], v[208:215], v[102:105], v166, v166 op_sel_hi:[0,0,0]
	v_mfma_scale_f32_16x16x128_f8f6f4 v[94:97], v[168:175], v[216:223], v[94:97], v166, v166 op_sel_hi:[0,0,0]
	v_mfma_scale_f32_16x16x128_f8f6f4 v[86:89], v[176:183], v[216:223], v[86:89], v166, v166 op_sel_hi:[0,0,0]
	v_mfma_scale_f32_16x16x128_f8f6f4 v[78:81], v[168:175], v[226:233], v[78:81], v166, v166 op_sel_hi:[0,0,0]
	v_mfma_scale_f32_16x16x128_f8f6f4 v[70:73], v[176:183], v[226:233], v[70:73], v166, v166 op_sel_hi:[0,0,0]
	v_mfma_scale_f32_16x16x128_f8f6f4 v[110:113], v[168:175], v[200:207], v[142:145], v166, v166 op_sel_hi:[0,0,0]
	v_mfma_scale_f32_16x16x128_f8f6f4 v[118:121], v[176:183], v[200:207], v[134:137], v166, v166 op_sel_hi:[0,0,0]
	s_setprio 0
	s_setprio 1
	v_mfma_scale_f32_16x16x128_f8f6f4 v[122:125], v[192:199], v[200:207], v[122:125], v166, v166 op_sel_hi:[0,0,0]
	v_mfma_scale_f32_16x16x128_f8f6f4 v[106:109], v[184:191], v[208:215], v[106:109], v166, v166 op_sel_hi:[0,0,0]
	v_mfma_scale_f32_16x16x128_f8f6f4 v[98:101], v[192:199], v[208:215], v[98:101], v166, v166 op_sel_hi:[0,0,0]
	v_mfma_scale_f32_16x16x128_f8f6f4 v[90:93], v[184:191], v[216:223], v[90:93], v166, v166 op_sel_hi:[0,0,0]
	v_mfma_scale_f32_16x16x128_f8f6f4 v[82:85], v[192:199], v[216:223], v[82:85], v166, v166 op_sel_hi:[0,0,0]
	v_mfma_scale_f32_16x16x128_f8f6f4 v[74:77], v[184:191], v[226:233], v[74:77], v166, v166 op_sel_hi:[0,0,0]
	v_mfma_scale_f32_16x16x128_f8f6f4 v[66:69], v[192:199], v[226:233], v[66:69], v166, v166 op_sel_hi:[0,0,0]
	v_mfma_scale_f32_16x16x128_f8f6f4 v[126:129], v[184:191], v[200:207], v[138:141], v166, v166 op_sel_hi:[0,0,0]
	s_setprio 0
	s_barrier
	v_mov_b32_e32 v142, v158
	s_add_i32 s1, s67, s45
	ds_read_b128 v[134:137], v165 offset:16384
	s_nop 1
	ds_read_b128 v[138:141], v165 offset:17408
	ds_read_b128 v[200:203], v165 offset:18432
	ds_read_b128 v[204:207], v165 offset:19456
	ds_read_b128 v[208:211], v165 offset:20480
	ds_read_b128 v[212:215], v165 offset:21504
	ds_read_b128 v[216:219], v165 offset:22528
	ds_read_b128 v[220:223], v165 offset:23552
	s_mov_b32 m0, s1
	s_nop 0
	global_load_lds_dwordx4 v142, s[42:43]
	v_mov_b32_e32 v142, v159
	s_add_i32 m0, s1, 0x2000
	s_add_u32 s74, s42, 0x40000
	global_load_lds_dwordx4 v142, s[42:43]
	s_addc_u32 s75, s43, 0
	v_mov_b32_e32 v142, v158
	s_add_i32 s1, s68, s45
	s_mov_b32 m0, s1
	s_nop 0
	global_load_lds_dwordx4 v142, s[74:75]
	v_mov_b32_e32 v142, v159
	s_add_i32 m0, s1, 0x2000
	s_nop 0
	global_load_lds_dwordx4 v142, s[74:75]
	v_mov_b32_e32 v142, v133
	s_mov_b32 m0, s52
	s_nop 0
	global_load_lds_dwordx4 v142, s[40:41]
	v_mov_b32_e32 v142, v150
	s_mov_b32 m0, s53
	s_nop 0
	global_load_lds_dwordx4 v142, s[40:41]
	s_cmp_eq_u32 s0, s32
	s_cbranch_scc1 .Lskipw_p9_1
	s_waitcnt vmcnt(8)
.Lskipw_p9_1:
	s_waitcnt lgkmcnt(0)
	s_barrier
	s_setprio 1
	s_waitcnt lgkmcnt(0)
	v_mfma_scale_f32_16x16x128_f8f6f4 v[62:65], v[168:175], v[134:141], v[62:65], v166, v166 op_sel_hi:[0,0,0]
	v_mfma_scale_f32_16x16x128_f8f6f4 v[54:57], v[176:183], v[134:141], v[54:57], v166, v166 op_sel_hi:[0,0,0]
	v_mfma_scale_f32_16x16x128_f8f6f4 v[46:49], v[168:175], v[200:207], v[46:49], v166, v166 op_sel_hi:[0,0,0]
	v_mfma_scale_f32_16x16x128_f8f6f4 v[38:41], v[176:183], v[200:207], v[38:41], v166, v166 op_sel_hi:[0,0,0]
	v_mfma_scale_f32_16x16x128_f8f6f4 v[30:33], v[168:175], v[208:215], v[30:33], v166, v166 op_sel_hi:[0,0,0]
	v_mfma_scale_f32_16x16x128_f8f6f4 v[22:25], v[176:183], v[208:215], v[22:25], v166, v166 op_sel_hi:[0,0,0]
	v_mfma_scale_f32_16x16x128_f8f6f4 v[14:17], v[168:175], v[216:223], v[14:17], v166, v166 op_sel_hi:[0,0,0]
	v_mfma_scale_f32_16x16x128_f8f6f4 v[6:9], v[176:183], v[216:223], v[6:9], v166, v166 op_sel_hi:[0,0,0]
	s_setprio 0
	s_setprio 1
	v_mfma_scale_f32_16x16x128_f8f6f4 v[58:61], v[184:191], v[134:141], v[58:61], v166, v166 op_sel_hi:[0,0,0]
	v_mfma_scale_f32_16x16x128_f8f6f4 v[50:53], v[192:199], v[134:141], v[50:53], v166, v166 op_sel_hi:[0,0,0]
	v_mfma_scale_f32_16x16x128_f8f6f4 v[42:45], v[184:191], v[200:207], v[42:45], v166, v166 op_sel_hi:[0,0,0]
	v_mfma_scale_f32_16x16x128_f8f6f4 v[34:37], v[192:199], v[200:207], v[34:37], v166, v166 op_sel_hi:[0,0,0]
	v_mfma_scale_f32_16x16x128_f8f6f4 v[26:29], v[184:191], v[208:215], v[26:29], v166, v166 op_sel_hi:[0,0,0]
	v_mfma_scale_f32_16x16x128_f8f6f4 v[18:21], v[192:199], v[208:215], v[18:21], v166, v166 op_sel_hi:[0,0,0]
	v_mfma_scale_f32_16x16x128_f8f6f4 v[10:13], v[184:191], v[216:223], v[10:13], v166, v166 op_sel_hi:[0,0,0]
	v_mfma_scale_f32_16x16x128_f8f6f4 v[2:5], v[192:199], v[216:223], v[2:5], v166, v166 op_sel_hi:[0,0,0]
	s_setprio 0
	s_barrier
; template <class Epi, bool GATHER, bool EXPERT, bool FP8>
; DI void gemm_phase(LAS unsigned char* lds, const Gemm g, const StaticOrder& S, const Epi& E) {
;     ...
;             if (GATHER && last && has_next) {
;                 o00 = sp[0] * (unsigned)(K * 2) + (unsigned)C0x2; o01 = sp[512] * (unsigned)(K * 2) + (unsigned)C1x2;
;                 o10 = sp[1024] * (unsigned)(K * 2) + (unsigned)C0x2; o11 = sp[1536] * (unsigned)(K * 2) + (unsigned)C1x2; }
;             PG8_TRIP(a1, a2, b2, a3, b3, o00, o01, o10, o11);
;             if (last) { coffA[0][0] = o00; coffA[0][1] = o01; coffA[1][0] = o10; coffA[1][1] = o11; }
	s_add_i32 s1, 0, 0x18000
	v_add_u32_e32 v134, s1, v164
	s_add_i32 s73, 0, 0x1c000
	ds_read_b128 v[168:171], v134
	ds_read_b128 v[172:175], v134 offset:1024
	ds_read_b128 v[176:179], v134 offset:2048
	ds_read_b128 v[180:183], v134 offset:3072
	v_add_u32_e32 v134, s73, v164
	ds_read_b128 v[184:187], v134
	ds_read_b128 v[188:191], v134 offset:1024
	ds_read_b128 v[192:195], v134 offset:2048
	ds_read_b128 v[196:199], v134 offset:3072
	v_mov_b32_e32 v134, v151
	s_mov_b32 m0, s54
	ds_read_b128 v[200:203], v165 offset:32768
	ds_read_b128 v[204:207], v165 offset:33792
	ds_read_b128 v[208:211], v165 offset:34816
	ds_read_b128 v[212:215], v165 offset:35840
	ds_read_b128 v[216:219], v165 offset:36864
	ds_read_b128 v[220:223], v165 offset:37888
	ds_read_b128 v[226:229], v165 offset:38912
	ds_read_b128 v[230:233], v165 offset:39936
	s_nop 0
	global_load_lds_dwordx4 v134, s[40:41]
	v_mov_b32_e32 v134, v152
	s_mov_b32 m0, s55
	s_nop 0
	global_load_lds_dwordx4 v134, s[40:41]
	s_waitcnt vmcnt(8)
	s_waitcnt lgkmcnt(0)
	s_barrier
	s_setprio 1
	s_waitcnt lgkmcnt(0)
	v_mfma_scale_f32_16x16x128_f8f6f4 v[142:145], v[168:175], v[200:207], v[110:113], v166, v166 op_sel_hi:[0,0,0]
	v_mfma_scale_f32_16x16x128_f8f6f4 v[134:137], v[176:183], v[200:207], v[118:121], v166, v166 op_sel_hi:[0,0,0]
	v_mfma_scale_f32_16x16x128_f8f6f4 v[114:117], v[168:175], v[208:215], v[114:117], v166, v166 op_sel_hi:[0,0,0]
	v_mfma_scale_f32_16x16x128_f8f6f4 v[102:105], v[176:183], v[208:215], v[102:105], v166, v166 op_sel_hi:[0,0,0]
	v_mfma_scale_f32_16x16x128_f8f6f4 v[94:97], v[168:175], v[216:223], v[94:97], v166, v166 op_sel_hi:[0,0,0]
	v_mfma_scale_f32_16x16x128_f8f6f4 v[86:89], v[176:183], v[216:223], v[86:89], v166, v166 op_sel_hi:[0,0,0]
	v_mfma_scale_f32_16x16x128_f8f6f4 v[78:81], v[168:175], v[226:233], v[78:81], v166, v166 op_sel_hi:[0,0,0]
	v_mfma_scale_f32_16x16x128_f8f6f4 v[70:73], v[176:183], v[226:233], v[70:73], v166, v166 op_sel_hi:[0,0,0]
	s_setprio 0
	s_setprio 1
	v_mfma_scale_f32_16x16x128_f8f6f4 v[138:141], v[184:191], v[200:207], v[126:129], v166, v166 op_sel_hi:[0,0,0]
	v_mfma_scale_f32_16x16x128_f8f6f4 v[122:125], v[192:199], v[200:207], v[122:125], v166, v166 op_sel_hi:[0,0,0]
	v_mfma_scale_f32_16x16x128_f8f6f4 v[106:109], v[184:191], v[208:215], v[106:109], v166, v166 op_sel_hi:[0,0,0]
	v_mfma_scale_f32_16x16x128_f8f6f4 v[98:101], v[192:199], v[208:215], v[98:101], v166, v166 op_sel_hi:[0,0,0]
	v_mfma_scale_f32_16x16x128_f8f6f4 v[90:93], v[184:191], v[216:223], v[90:93], v166, v166 op_sel_hi:[0,0,0]
	v_mfma_scale_f32_16x16x128_f8f6f4 v[82:85], v[192:199], v[216:223], v[82:85], v166, v166 op_sel_hi:[0,0,0]
	v_mfma_scale_f32_16x16x128_f8f6f4 v[74:77], v[184:191], v[226:233], v[74:77], v166, v166 op_sel_hi:[0,0,0]
	v_mfma_scale_f32_16x16x128_f8f6f4 v[66:69], v[192:199], v[226:233], v[66:69], v166, v166 op_sel_hi:[0,0,0]
	s_setprio 0
	s_barrier
	v_mov_b32_e32 v146, v158
	ds_read_b128 v[200:203], v165 offset:49152
	ds_read_b128 v[204:207], v165 offset:50176
	ds_read_b128 v[208:211], v165 offset:51200
	ds_read_b128 v[212:215], v165 offset:52224
	ds_read_b128 v[216:219], v165 offset:53248
	ds_read_b128 v[220:223], v165 offset:54272
	ds_read_b128 v[226:229], v165 offset:55296
	ds_read_b128 v[230:233], v165 offset:56320
	s_add_i32 s1, s1, s45
	v_lshl_add_u64 v[110:111], s[42:43], 0, v[146:147]
	v_lshl_add_u64 v[110:111], v[110:111], 0, s[88:89]
	s_mov_b32 m0, s1
	v_mov_b32_e32 v146, v159
	global_load_lds_dwordx4 v[110:111], off
	s_add_i32 m0, s1, 0x2000
	v_lshl_add_u64 v[110:111], s[42:43], 0, v[146:147]
	v_lshl_add_u64 v[110:111], v[110:111], 0, s[88:89]
	s_add_u32 s42, s42, 0x40080
	global_load_lds_dwordx4 v[110:111], off
	s_addc_u32 s43, s43, 0
	v_mov_b32_e32 v110, v158
	s_add_i32 s1, s73, s45
	s_mov_b32 m0, s1
	v_mov_b32_e32 v146, v133
	global_load_lds_dwordx4 v110, s[42:43]
	v_mov_b32_e32 v110, v159
	s_add_i32 m0, s1, 0x2000
	s_nop 0
	global_load_lds_dwordx4 v110, s[42:43]
	s_mov_b32 m0, s59
	v_lshl_add_u64 v[110:111], s[40:41], 0, v[146:147]
	v_lshl_add_u64 v[110:111], v[110:111], 0, s[88:89]
	v_mov_b32_e32 v146, v150
	global_load_lds_dwordx4 v[110:111], off
	s_mov_b32 m0, s60
	v_lshl_add_u64 v[110:111], s[40:41], 0, v[146:147]
	v_lshl_add_u64 v[110:111], v[110:111], 0, s[88:89]
	global_load_lds_dwordx4 v[110:111], off
	s_waitcnt vmcnt(8)
	s_waitcnt lgkmcnt(0)
	s_barrier
	s_setprio 1
	s_waitcnt lgkmcnt(0)
	v_mfma_scale_f32_16x16x128_f8f6f4 v[62:65], v[168:175], v[200:207], v[62:65], v166, v166 op_sel_hi:[0,0,0]
	v_mfma_scale_f32_16x16x128_f8f6f4 v[54:57], v[176:183], v[200:207], v[54:57], v166, v166 op_sel_hi:[0,0,0]
	v_mfma_scale_f32_16x16x128_f8f6f4 v[46:49], v[168:175], v[208:215], v[46:49], v166, v166 op_sel_hi:[0,0,0]
	v_mfma_scale_f32_16x16x128_f8f6f4 v[38:41], v[176:183], v[208:215], v[38:41], v166, v166 op_sel_hi:[0,0,0]
	v_mfma_scale_f32_16x16x128_f8f6f4 v[30:33], v[168:175], v[216:223], v[30:33], v166, v166 op_sel_hi:[0,0,0]
	v_mfma_scale_f32_16x16x128_f8f6f4 v[22:25], v[176:183], v[216:223], v[22:25], v166, v166 op_sel_hi:[0,0,0]
	v_mfma_scale_f32_16x16x128_f8f6f4 v[14:17], v[168:175], v[226:233], v[14:17], v166, v166 op_sel_hi:[0,0,0]
	v_mfma_scale_f32_16x16x128_f8f6f4 v[6:9], v[176:183], v[226:233], v[6:9], v166, v166 op_sel_hi:[0,0,0]
	s_setprio 0
	s_setprio 1
	v_mfma_scale_f32_16x16x128_f8f6f4 v[58:61], v[184:191], v[200:207], v[58:61], v166, v166 op_sel_hi:[0,0,0]
	v_mfma_scale_f32_16x16x128_f8f6f4 v[50:53], v[192:199], v[200:207], v[50:53], v166, v166 op_sel_hi:[0,0,0]
	v_mfma_scale_f32_16x16x128_f8f6f4 v[42:45], v[184:191], v[208:215], v[42:45], v166, v166 op_sel_hi:[0,0,0]
	v_mfma_scale_f32_16x16x128_f8f6f4 v[34:37], v[192:199], v[208:215], v[34:37], v166, v166 op_sel_hi:[0,0,0]
	v_mfma_scale_f32_16x16x128_f8f6f4 v[26:29], v[184:191], v[216:223], v[26:29], v166, v166 op_sel_hi:[0,0,0]
	v_mfma_scale_f32_16x16x128_f8f6f4 v[18:21], v[192:199], v[216:223], v[18:21], v166, v166 op_sel_hi:[0,0,0]
	v_mfma_scale_f32_16x16x128_f8f6f4 v[10:13], v[184:191], v[226:233], v[10:13], v166, v166 op_sel_hi:[0,0,0]
	v_mfma_scale_f32_16x16x128_f8f6f4 v[2:5], v[192:199], v[226:233], v[2:5], v166, v166 op_sel_hi:[0,0,0]
	s_setprio 0
	s_barrier
	s_andn2_b64 vcc, exec, s[38:39]
	s_cbranch_vccnz .LBB0_1084
	v_mov_b32_e32 v161, v152
	v_mov_b32_e32 v160, v151
	v_mov_b32_e32 v163, v150
	v_mov_b32_e32 v162, v133
	s_branch .LBB0_1084

; DI f32x2 swiglu4_2(f32x2 hg, f32x2 hl) {
;     f32x2 glu, lin, ex, sg;
;     glu[0] = fminf(hg[0], 7.0f); glu[1] = fminf(hg[1], 7.0f); lin[0] = __builtin_amdgcn_fmed3f(hl[0], -7.0f, 7.0f); lin[1] = __builtin_amdgcn_fmed3f(hl[1], -7.0f, 7.0f);
;     const f32x2 t = glu * (-1.702f * 1.4426950408889634f);
;     ex[0] = __builtin_amdgcn_exp2f(t[0]); ex[1] = __builtin_amdgcn_exp2f(t[1]);
;     const f32x2 den = ex + 1.0f;
;     DI void operator()(const f32x4 (&acc)[2][2][4][2], const Unit& u, int wr, int wc, int fr, int fq, const LAS unsigned char* st) const {
;         const int row0 = u.pm * BM + wr * 64 + fr, f0 = u.pn * HALF + wc * 32 + 8 * fq;
;         f32x2 bg[4], bl[4];
;         { const LAS float* sb = (const LAS float*)(st + 512 + fq * 64);
; #pragma unroll
;           for (int p = 0; p < 4; ++p) { bg[p][0] = sb[4 * p]; bg[p][1] = sb[4 * p + 2]; bl[p][0] = sb[4 * p + 1]; bl[p][1] = sb[4 * p + 3]; } }
; #pragma unroll
;         for (int ai = 0; ai < 2; ++ai)
; #pragma unroll
;             for (int mp = 0; mp < 2; ++mp) {
;                 u32x2 w2[2];
; #pragma unroll
;                 for (int mm = 0; mm < 2; ++mm) { const int m = 2 * mp + mm; const float ws = *(const LAS float*)(st + ai * 256 + (m * 16 + fr) * 4) * (1.0f / 32.0f);
;                     const f32x4 g0 = acc[ai][0][m][0], g1 = acc[ai][0][m][1], l0 = acc[ai][1][m][0], l1 = acc[ai][1][m][1];
;                     f32x2 ws2; ws2[0] = ws; ws2[1] = ws;
;                     const f32x2 a01 = swiglu4_2(__builtin_shufflevector(g0, g0, 0, 1) * ws2 + bg[0], __builtin_shufflevector(l0, l0, 0, 1) * ws2 + bl[0]);
;                     const f32x2 a23 = swiglu4_2(__builtin_shufflevector(g0, g0, 2, 3) * ws2 + bg[1], __builtin_shufflevector(l0, l0, 2, 3) * ws2 + bl[1]);
;                     const f32x2 a45 = swiglu4_2(__builtin_shufflevector(g1, g1, 0, 1) * ws2 + bg[2], __builtin_shufflevector(l1, l1, 0, 1) * ws2 + bl[2]);
;                     const f32x2 a67 = swiglu4_2(__builtin_shufflevector(g1, g1, 2, 3) * ws2 + bg[3], __builtin_shufflevector(l1, l1, 2, 3) * ws2 + bl[3]);
;                     w2[mm].x = pk4_fp8n(a01[0], a01[1], a23[0], a23[1]); w2[mm].y = pk4_fp8n(a45[0], a45[1], a67[0], a67[1]); }
;                 const u32x4 w = pair16(w2[0], w2[1]);
;                 *(u32x4*)(ACT + (size_t)(row0 + ai * HALF + (2 * mp + (fq & 1)) * 16) * FF + (f0 - 8 * (fq & 1))) = w; }
.LBB0_1091:
	v_mov_b32_e32 v110, v224
	s_lshl_b32 s1, s34, 7
	v_ashrrev_i32_e32 v168, 4, v110
	v_and_b32_e32 v146, 15, v110
	v_lshl_add_u32 v110, v168, 6, s35
	ds_read_b128 v[130:133], v110 offset:512
	ds_read_b128 v[126:129], v110 offset:528
	ds_read_b128 v[118:121], v110 offset:544
	ds_read_b128 v[110:113], v110 offset:560
	s_or_b32 s1, s1, s58
	s_lshl_b32 s0, s33, 8
	s_waitcnt lgkmcnt(0)
	v_mov_b32_e32 v154, v126
	v_lshl_add_u32 v126, v146, 2, s35
	v_mov_b32_e32 v156, v130
	v_mov_b32_e32 v157, v132
	v_mov_b32_e32 v132, v131
	ds_read2_b32 v[130:131], v126 offset1:16
	v_mov_b32_e32 v150, v110
	v_mov_b32_e32 v151, v112
	v_mov_b32_e32 v112, v111
	v_lshl_add_u32 v110, v168, 3, s1
	s_waitcnt lgkmcnt(0)
	v_mul_f32_e32 v130, 0x3d000000, v130
	v_pk_fma_f32 v[142:143], v[142:143], v[130:131], v[156:157] op_sel_hi:[1,0,1]
	v_and_b32_e32 v111, 1, v168
	v_min_f32_e32 v142, 0x40e00000, v142
	v_min_f32_e32 v143, 0x40e00000, v143
	v_pk_mul_f32 v[168:169], v[142:143], s[84:85] op_sel_hi:[1,0]
	v_mov_b32_e32 v155, v128
	v_exp_f32_e32 v168, v168
	v_exp_f32_e32 v169, v169
	v_pk_fma_f32 v[144:145], v[144:145], v[130:131], v[154:155] op_sel_hi:[1,0,1]
	v_pk_fma_f32 v[138:139], v[138:139], v[130:131], v[132:133] op_sel_hi:[1,0,1]
	v_min_f32_e32 v144, 0x40e00000, v144
	v_pk_add_f32 v[168:169], v[168:169], 1.0 op_sel_hi:[1,0]
	v_min_f32_e32 v145, 0x40e00000, v145
	v_rcp_f32_e32 v168, v168
	v_rcp_f32_e32 v169, v169
	v_pk_mul_f32 v[170:171], v[144:145], s[84:85] op_sel_hi:[1,0]
	v_med3_f32 v138, v138, s69, v167
	v_exp_f32_e32 v170, v170
	v_exp_f32_e32 v171, v171
	v_med3_f32 v139, v139, s69, v167
	v_pk_mul_f32 v[142:143], v[142:143], v[168:169]
	v_pk_fma_f32 v[138:139], v[138:139], 4.0, 4.0 op_sel_hi:[1,0,0]
	v_mov_b32_e32 v128, v127
	v_pk_mul_f32 v[138:139], v[138:139], v[142:143]
	v_pk_add_f32 v[142:143], v[170:171], 1.0 op_sel_hi:[1,0]
	v_mov_b32_e32 v152, v118
	v_rcp_f32_e32 v142, v142
	v_rcp_f32_e32 v143, v143
	v_mov_b32_e32 v153, v120
	v_pk_fma_f32 v[140:141], v[140:141], v[130:131], v[128:129] op_sel_hi:[1,0,1]
	v_pk_fma_f32 v[134:135], v[134:135], v[130:131], v[152:153] op_sel_hi:[1,0,1]
	v_med3_f32 v140, v140, s69, v167
	v_med3_f32 v141, v141, s69, v167
	v_pk_mul_f32 v[142:143], v[144:145], v[142:143]
	v_pk_fma_f32 v[140:141], v[140:141], 4.0, 4.0 op_sel_hi:[1,0,0]
	v_min_f32_e32 v134, 0x40e00000, v134
	v_min_f32_e32 v135, 0x40e00000, v135
	v_pk_mul_f32 v[140:141], v[140:141], v[142:143]
	v_pk_mul_f32 v[142:143], v[134:135], s[84:85] op_sel_hi:[1,0]
	v_pk_fma_f32 v[136:137], v[136:137], v[130:131], v[150:151] op_sel_hi:[1,0,1]
	v_exp_f32_e32 v142, v142
	v_exp_f32_e32 v143, v143
	v_min_f32_e32 v136, 0x40e00000, v136
	v_min_f32_e32 v137, 0x40e00000, v137
	v_pk_mul_f32 v[144:145], v[136:137], s[84:85] op_sel_hi:[1,0]
	v_pk_add_f32 v[142:143], v[142:143], 1.0 op_sel_hi:[1,0]
	v_mov_b32_e32 v120, v119
	v_rcp_f32_e32 v142, v142
	v_rcp_f32_e32 v143, v143
	v_exp_f32_e32 v144, v144
	v_exp_f32_e32 v145, v145
	v_pk_fma_f32 v[122:123], v[122:123], v[130:131], v[120:121] op_sel_hi:[1,0,1]
	v_pk_mul_f32 v[134:135], v[134:135], v[142:143]
	v_med3_f32 v122, v122, s69, v167
	v_med3_f32 v123, v123, s69, v167
	v_pk_fma_f32 v[122:123], v[122:123], 4.0, 4.0 op_sel_hi:[1,0,0]
	v_pk_fma_f32 v[124:125], v[124:125], v[130:131], v[112:113] op_sel_hi:[1,0,1]
	v_pk_mul_f32 v[134:135], v[122:123], v[134:135]
	v_pk_add_f32 v[122:123], v[144:145], 1.0 op_sel_hi:[1,0]
	v_med3_f32 v124, v124, s69, v167
	v_rcp_f32_e32 v122, v122
	v_rcp_f32_e32 v123, v123
	v_med3_f32 v125, v125, s69, v167
	v_pk_fma_f32 v[124:125], v[124:125], 4.0, 4.0 op_sel_hi:[1,0,0]
	s_add_i32 s0, s0, s47
	v_pk_mul_f32 v[136:137], v[136:137], v[122:123]
	v_mov_b32_e32 v123, v147
	v_cvt_pk_fp8_f32 v123, v134, v135
	v_pk_mul_f32 v[124:125], v[124:125], v[136:137]
	v_mov_b32_e32 v122, v147
	v_cvt_pk_fp8_f32 v122, v138, v139
	v_cvt_pk_fp8_f32 v123, v124, v125 op_sel:[0,0,1]
	v_mul_f32_e32 v124, 0x3d000000, v131
	v_pk_fma_f32 v[114:115], v[114:115], v[124:125], v[156:157] op_sel_hi:[1,0,1]
	v_pk_fma_f32 v[116:117], v[116:117], v[124:125], v[154:155] op_sel_hi:[1,0,1]
	v_min_f32_e32 v114, 0x40e00000, v114
	v_min_f32_e32 v115, 0x40e00000, v115
	v_pk_mul_f32 v[130:131], v[114:115], s[84:85] op_sel_hi:[1,0]
	v_min_f32_e32 v116, 0x40e00000, v116
	v_exp_f32_e32 v130, v130
	v_exp_f32_e32 v131, v131
	v_min_f32_e32 v117, 0x40e00000, v117
	v_pk_mul_f32 v[134:135], v[116:117], s[84:85] op_sel_hi:[1,0]
	v_pk_fma_f32 v[106:107], v[106:107], v[124:125], v[132:133] op_sel_hi:[1,0,1]
	v_pk_add_f32 v[130:131], v[130:131], 1.0 op_sel_hi:[1,0]
	v_exp_f32_e32 v134, v134
	v_rcp_f32_e32 v130, v130
	v_rcp_f32_e32 v131, v131
	v_exp_f32_e32 v135, v135
	v_med3_f32 v106, v106, s69, v167
	v_med3_f32 v107, v107, s69, v167
	v_pk_mul_f32 v[114:115], v[114:115], v[130:131]
	v_pk_fma_f32 v[106:107], v[106:107], 4.0, 4.0 op_sel_hi:[1,0,0]
	v_pk_fma_f32 v[108:109], v[108:109], v[124:125], v[128:129] op_sel_hi:[1,0,1]
	v_pk_mul_f32 v[106:107], v[106:107], v[114:115]
	v_pk_add_f32 v[114:115], v[134:135], 1.0 op_sel_hi:[1,0]
	v_med3_f32 v108, v108, s69, v167
	v_rcp_f32_e32 v114, v114
	v_rcp_f32_e32 v115, v115
	v_med3_f32 v109, v109, s69, v167
	v_pk_fma_f32 v[102:103], v[102:103], v[124:125], v[152:153] op_sel_hi:[1,0,1]
	v_pk_fma_f32 v[108:109], v[108:109], 4.0, 4.0 op_sel_hi:[1,0,0]
	v_pk_mul_f32 v[114:115], v[116:117], v[114:115]
	v_min_f32_e32 v102, 0x40e00000, v102
	v_min_f32_e32 v103, 0x40e00000, v103
	v_pk_mul_f32 v[108:109], v[108:109], v[114:115]
	v_pk_mul_f32 v[114:115], v[102:103], s[84:85] op_sel_hi:[1,0]
	v_pk_fma_f32 v[104:105], v[104:105], v[124:125], v[150:151] op_sel_hi:[1,0,1]
	v_exp_f32_e32 v114, v114
	v_exp_f32_e32 v115, v115
; DI f32x2 swiglu4_2(f32x2 hg, f32x2 hl) {
;     f32x2 glu, lin, ex, sg;
;     glu[0] = fminf(hg[0], 7.0f); glu[1] = fminf(hg[1], 7.0f); lin[0] = __builtin_amdgcn_fmed3f(hl[0], -7.0f, 7.0f); lin[1] = __builtin_amdgcn_fmed3f(hl[1], -7.0f, 7.0f);
;     const f32x2 t = glu * (-1.702f * 1.4426950408889634f);
;     ex[0] = __builtin_amdgcn_exp2f(t[0]); ex[1] = __builtin_amdgcn_exp2f(t[1]);
;     const f32x2 den = ex + 1.0f;
;     DI void operator()(const f32x4 (&acc)[2][2][4][2], const Unit& u, int wr, int wc, int fr, int fq, const LAS unsigned char* st) const {
;         const int row0 = u.pm * BM + wr * 64 + fr, f0 = u.pn * HALF + wc * 32 + 8 * fq;
;         f32x2 bg[4], bl[4];
;         { const LAS float* sb = (const LAS float*)(st + 512 + fq * 64);
; #pragma unroll
;           for (int p = 0; p < 4; ++p) { bg[p][0] = sb[4 * p]; bg[p][1] = sb[4 * p + 2]; bl[p][0] = sb[4 * p + 1]; bl[p][1] = sb[4 * p + 3]; } }
; #pragma unroll
;         for (int ai = 0; ai < 2; ++ai)
; #pragma unroll
;             for (int mp = 0; mp < 2; ++mp) {
;                 u32x2 w2[2];
; #pragma unroll
;                 for (int mm = 0; mm < 2; ++mm) { const int m = 2 * mp + mm; const float ws = *(const LAS float*)(st + ai * 256 + (m * 16 + fr) * 4) * (1.0f / 32.0f);
;                     const f32x4 g0 = acc[ai][0][m][0], g1 = acc[ai][0][m][1], l0 = acc[ai][1][m][0], l1 = acc[ai][1][m][1];
;                     f32x2 ws2; ws2[0] = ws; ws2[1] = ws;
;                     const f32x2 a01 = swiglu4_2(__builtin_shufflevector(g0, g0, 0, 1) * ws2 + bg[0], __builtin_shufflevector(l0, l0, 0, 1) * ws2 + bl[0]);
;                     const f32x2 a23 = swiglu4_2(__builtin_shufflevector(g0, g0, 2, 3) * ws2 + bg[1], __builtin_shufflevector(l0, l0, 2, 3) * ws2 + bl[1]);
;                     const f32x2 a45 = swiglu4_2(__builtin_shufflevector(g1, g1, 0, 1) * ws2 + bg[2], __builtin_shufflevector(l1, l1, 0, 1) * ws2 + bl[2]);
;                     const f32x2 a67 = swiglu4_2(__builtin_shufflevector(g1, g1, 2, 3) * ws2 + bg[3], __builtin_shufflevector(l1, l1, 2, 3) * ws2 + bl[3]);
;                     w2[mm].x = pk4_fp8n(a01[0], a01[1], a23[0], a23[1]); w2[mm].y = pk4_fp8n(a45[0], a45[1], a67[0], a67[1]); }
;                 const u32x4 w = pair16(w2[0], w2[1]);
;                 *(u32x4*)(ACT + (size_t)(row0 + ai * HALF + (2 * mp + (fq & 1)) * 16) * FF + (f0 - 8 * (fq & 1))) = w; }
	v_min_f32_e32 v104, 0x40e00000, v104
	v_min_f32_e32 v105, 0x40e00000, v105
	v_pk_mul_f32 v[116:117], v[104:105], s[84:85] op_sel_hi:[1,0]
	v_pk_add_f32 v[114:115], v[114:115], 1.0 op_sel_hi:[1,0]
	v_exp_f32_e32 v116, v116
	v_rcp_f32_e32 v114, v114
	v_rcp_f32_e32 v115, v115
	v_exp_f32_e32 v117, v117
	v_pk_fma_f32 v[98:99], v[98:99], v[124:125], v[120:121] op_sel_hi:[1,0,1]
	v_pk_fma_f32 v[100:101], v[100:101], v[124:125], v[112:113] op_sel_hi:[1,0,1]
	v_med3_f32 v98, v98, s69, v167
	v_med3_f32 v99, v99, s69, v167
	v_pk_mul_f32 v[102:103], v[102:103], v[114:115]
	v_pk_fma_f32 v[98:99], v[98:99], 4.0, 4.0 op_sel_hi:[1,0,0]
	v_mov_b32_e32 v125, v147
	v_pk_mul_f32 v[98:99], v[98:99], v[102:103]
	v_pk_add_f32 v[102:103], v[116:117], 1.0 op_sel_hi:[1,0]
	v_cvt_pk_fp8_f32 v125, v98, v99
	v_rcp_f32_e32 v102, v102
	v_rcp_f32_e32 v103, v103
	v_med3_f32 v100, v100, s69, v167
	v_med3_f32 v101, v101, s69, v167
	v_mov_b32_e32 v124, v147
	v_pk_mul_f32 v[102:103], v[104:105], v[102:103]
	v_pk_fma_f32 v[98:99], v[100:101], 4.0, 4.0 op_sel_hi:[1,0,0]
	v_cvt_pk_fp8_f32 v124, v106, v107
	v_pk_mul_f32 v[98:99], v[98:99], v[102:103]
	v_lshlrev_b32_e32 v118, 4, v111
	v_cvt_pk_fp8_f32 v125, v98, v99 op_sel:[0,0,1]
	ds_read2_b32 v[98:99], v126 offset0:32 offset1:48
	v_or3_b32 v118, v118, s0, v146
	v_cvt_pk_fp8_f32 v122, v140, v141 op_sel:[0,0,1]
	v_cvt_pk_fp8_f32 v124, v108, v109 op_sel:[0,0,1]
	v_lshlrev_b32_e32 v111, 3, v111
	v_ashrrev_i32_e32 v119, 31, v118
	v_sub_u32_e32 v110, v110, v111
	v_lshlrev_b64 v[100:101], 11, v[118:119]
	s_waitcnt lgkmcnt(0)
	v_mul_f32_e32 v98, 0x3d000000, v98
	v_ashrrev_i32_e32 v111, 31, v110
	v_lshl_add_u64 v[100:101], s[86:87], 0, v[100:101]
	v_pk_fma_f32 v[94:95], v[94:95], v[98:99], v[156:157] op_sel_hi:[1,0,1]
	v_permlane16_swap_b32_e32 v122, v124
	v_permlane16_swap_b32_e32 v123, v125
	v_lshl_add_u64 v[100:101], v[100:101], 0, v[110:111]
	v_min_f32_e32 v94, 0x40e00000, v94
	v_min_f32_e32 v95, 0x40e00000, v95
	global_store_dwordx4 v[100:101], v[122:125], off
	v_pk_mul_f32 v[100:101], v[94:95], s[84:85] op_sel_hi:[1,0]
	v_pk_fma_f32 v[96:97], v[96:97], v[98:99], v[154:155] op_sel_hi:[1,0,1]
	v_exp_f32_e32 v100, v100
	v_exp_f32_e32 v101, v101
	v_min_f32_e32 v96, 0x40e00000, v96
	v_min_f32_e32 v97, 0x40e00000, v97
	v_pk_mul_f32 v[102:103], v[96:97], s[84:85] op_sel_hi:[1,0]
	v_pk_add_f32 v[100:101], v[100:101], 1.0 op_sel_hi:[1,0]
	v_exp_f32_e32 v102, v102
	v_rcp_f32_e32 v100, v100
	v_rcp_f32_e32 v101, v101
	v_exp_f32_e32 v103, v103
	v_pk_fma_f32 v[90:91], v[90:91], v[98:99], v[132:133] op_sel_hi:[1,0,1]
	v_pk_fma_f32 v[92:93], v[92:93], v[98:99], v[128:129] op_sel_hi:[1,0,1]
	v_med3_f32 v90, v90, s69, v167
	v_med3_f32 v91, v91, s69, v167
	v_pk_mul_f32 v[94:95], v[94:95], v[100:101]
	v_pk_fma_f32 v[90:91], v[90:91], 4.0, 4.0 op_sel_hi:[1,0,0]
	v_med3_f32 v92, v92, s69, v167
	v_pk_mul_f32 v[90:91], v[90:91], v[94:95]
	v_pk_add_f32 v[94:95], v[102:103], 1.0 op_sel_hi:[1,0]
	v_med3_f32 v93, v93, s69, v167
	v_rcp_f32_e32 v94, v94
	v_rcp_f32_e32 v95, v95
	v_pk_fma_f32 v[86:87], v[86:87], v[98:99], v[152:153] op_sel_hi:[1,0,1]
	v_pk_fma_f32 v[92:93], v[92:93], 4.0, 4.0 op_sel_hi:[1,0,0]
	v_min_f32_e32 v86, 0x40e00000, v86
	v_pk_mul_f32 v[94:95], v[96:97], v[94:95]
	v_min_f32_e32 v87, 0x40e00000, v87
	v_pk_mul_f32 v[92:93], v[92:93], v[94:95]
	v_pk_mul_f32 v[94:95], v[86:87], s[84:85] op_sel_hi:[1,0]
	v_pk_fma_f32 v[88:89], v[88:89], v[98:99], v[150:151] op_sel_hi:[1,0,1]
	v_exp_f32_e32 v94, v94
	v_exp_f32_e32 v95, v95
	v_min_f32_e32 v88, 0x40e00000, v88
	v_min_f32_e32 v89, 0x40e00000, v89
	v_pk_mul_f32 v[96:97], v[88:89], s[84:85] op_sel_hi:[1,0]
	v_pk_add_f32 v[94:95], v[94:95], 1.0 op_sel_hi:[1,0]
	v_exp_f32_e32 v96, v96
	v_rcp_f32_e32 v94, v94
	v_rcp_f32_e32 v95, v95
	v_exp_f32_e32 v97, v97
	v_pk_fma_f32 v[82:83], v[82:83], v[98:99], v[120:121] op_sel_hi:[1,0,1]
	v_pk_fma_f32 v[84:85], v[84:85], v[98:99], v[112:113] op_sel_hi:[1,0,1]
	v_med3_f32 v82, v82, s69, v167
	v_med3_f32 v83, v83, s69, v167
	v_pk_mul_f32 v[86:87], v[86:87], v[94:95]
	v_pk_fma_f32 v[82:83], v[82:83], 4.0, 4.0 op_sel_hi:[1,0,0]
	v_med3_f32 v84, v84, s69, v167
	v_pk_mul_f32 v[86:87], v[82:83], v[86:87]
	v_pk_add_f32 v[82:83], v[96:97], 1.0 op_sel_hi:[1,0]
	v_med3_f32 v85, v85, s69, v167
	v_rcp_f32_e32 v82, v82
	v_rcp_f32_e32 v83, v83
	v_pk_fma_f32 v[84:85], v[84:85], 4.0, 4.0 op_sel_hi:[1,0,0]
	s_and_b64 vcc, exec, s[2:3]
	s_mov_b64 s[0:1], -1
	v_pk_mul_f32 v[88:89], v[88:89], v[82:83]
	v_mov_b32_e32 v83, v147
	v_cvt_pk_fp8_f32 v83, v86, v87
	v_pk_mul_f32 v[84:85], v[84:85], v[88:89]
	v_mov_b32_e32 v82, v147
	v_cvt_pk_fp8_f32 v82, v90, v91
	v_cvt_pk_fp8_f32 v83, v84, v85 op_sel:[0,0,1]
	v_mul_f32_e32 v84, 0x3d000000, v99
	v_pk_fma_f32 v[78:79], v[78:79], v[84:85], v[156:157] op_sel_hi:[1,0,1]
	v_pk_fma_f32 v[80:81], v[80:81], v[84:85], v[154:155] op_sel_hi:[1,0,1]
	v_min_f32_e32 v78, 0x40e00000, v78
	v_min_f32_e32 v79, 0x40e00000, v79
	v_pk_mul_f32 v[86:87], v[78:79], s[84:85] op_sel_hi:[1,0]
	v_min_f32_e32 v80, 0x40e00000, v80
	v_exp_f32_e32 v86, v86
	v_exp_f32_e32 v87, v87
	v_min_f32_e32 v81, 0x40e00000, v81
	v_pk_mul_f32 v[88:89], v[80:81], s[84:85] op_sel_hi:[1,0]
	v_pk_fma_f32 v[74:75], v[74:75], v[84:85], v[132:133] op_sel_hi:[1,0,1]
	v_pk_add_f32 v[86:87], v[86:87], 1.0 op_sel_hi:[1,0]
	v_exp_f32_e32 v88, v88
	v_rcp_f32_e32 v86, v86
	v_rcp_f32_e32 v87, v87
	v_exp_f32_e32 v89, v89
	v_med3_f32 v74, v74, s69, v167
	v_med3_f32 v75, v75, s69, v167
	v_pk_mul_f32 v[78:79], v[78:79], v[86:87]
	v_pk_fma_f32 v[74:75], v[74:75], 4.0, 4.0 op_sel_hi:[1,0,0]
	v_pk_fma_f32 v[76:77], v[76:77], v[84:85], v[128:129] op_sel_hi:[1,0,1]
	v_pk_mul_f32 v[74:75], v[74:75], v[78:79]
; DI f32x2 swiglu4_2(f32x2 hg, f32x2 hl) {
;     f32x2 glu, lin, ex, sg;
;     glu[0] = fminf(hg[0], 7.0f); glu[1] = fminf(hg[1], 7.0f); lin[0] = __builtin_amdgcn_fmed3f(hl[0], -7.0f, 7.0f); lin[1] = __builtin_amdgcn_fmed3f(hl[1], -7.0f, 7.0f);
;     const f32x2 t = glu * (-1.702f * 1.4426950408889634f);
;     ex[0] = __builtin_amdgcn_exp2f(t[0]); ex[1] = __builtin_amdgcn_exp2f(t[1]);
;     const f32x2 den = ex + 1.0f;
;     DI void operator()(const f32x4 (&acc)[2][2][4][2], const Unit& u, int wr, int wc, int fr, int fq, const LAS unsigned char* st) const {
;         const int row0 = u.pm * BM + wr * 64 + fr, f0 = u.pn * HALF + wc * 32 + 8 * fq;
;         f32x2 bg[4], bl[4];
;         { const LAS float* sb = (const LAS float*)(st + 512 + fq * 64);
; #pragma unroll
;           for (int p = 0; p < 4; ++p) { bg[p][0] = sb[4 * p]; bg[p][1] = sb[4 * p + 2]; bl[p][0] = sb[4 * p + 1]; bl[p][1] = sb[4 * p + 3]; } }
; #pragma unroll
;         for (int ai = 0; ai < 2; ++ai)
; #pragma unroll
;             for (int mp = 0; mp < 2; ++mp) {
;                 u32x2 w2[2];
; #pragma unroll
;                 for (int mm = 0; mm < 2; ++mm) { const int m = 2 * mp + mm; const float ws = *(const LAS float*)(st + ai * 256 + (m * 16 + fr) * 4) * (1.0f / 32.0f);
;                     const f32x4 g0 = acc[ai][0][m][0], g1 = acc[ai][0][m][1], l0 = acc[ai][1][m][0], l1 = acc[ai][1][m][1];
;                     f32x2 ws2; ws2[0] = ws; ws2[1] = ws;
;                     const f32x2 a01 = swiglu4_2(__builtin_shufflevector(g0, g0, 0, 1) * ws2 + bg[0], __builtin_shufflevector(l0, l0, 0, 1) * ws2 + bl[0]);
;                     const f32x2 a23 = swiglu4_2(__builtin_shufflevector(g0, g0, 2, 3) * ws2 + bg[1], __builtin_shufflevector(l0, l0, 2, 3) * ws2 + bl[1]);
;                     const f32x2 a45 = swiglu4_2(__builtin_shufflevector(g1, g1, 0, 1) * ws2 + bg[2], __builtin_shufflevector(l1, l1, 0, 1) * ws2 + bl[2]);
;                     const f32x2 a67 = swiglu4_2(__builtin_shufflevector(g1, g1, 2, 3) * ws2 + bg[3], __builtin_shufflevector(l1, l1, 2, 3) * ws2 + bl[3]);
;                     w2[mm].x = pk4_fp8n(a01[0], a01[1], a23[0], a23[1]); w2[mm].y = pk4_fp8n(a45[0], a45[1], a67[0], a67[1]); }
;                 const u32x4 w = pair16(w2[0], w2[1]);
;                 *(u32x4*)(ACT + (size_t)(row0 + ai * HALF + (2 * mp + (fq & 1)) * 16) * FF + (f0 - 8 * (fq & 1))) = w; }
	v_pk_add_f32 v[78:79], v[88:89], 1.0 op_sel_hi:[1,0]
	v_med3_f32 v76, v76, s69, v167
	v_rcp_f32_e32 v78, v78
	v_rcp_f32_e32 v79, v79
	v_med3_f32 v77, v77, s69, v167
	v_pk_fma_f32 v[70:71], v[70:71], v[84:85], v[152:153] op_sel_hi:[1,0,1]
	v_pk_fma_f32 v[76:77], v[76:77], 4.0, 4.0 op_sel_hi:[1,0,0]
	v_pk_mul_f32 v[78:79], v[80:81], v[78:79]
	v_min_f32_e32 v70, 0x40e00000, v70
	v_min_f32_e32 v71, 0x40e00000, v71
	v_pk_mul_f32 v[76:77], v[76:77], v[78:79]
	v_pk_mul_f32 v[78:79], v[70:71], s[84:85] op_sel_hi:[1,0]
	v_pk_fma_f32 v[72:73], v[72:73], v[84:85], v[150:151] op_sel_hi:[1,0,1]
	v_exp_f32_e32 v78, v78
	v_exp_f32_e32 v79, v79
	v_pk_fma_f32 v[66:67], v[66:67], v[84:85], v[120:121] op_sel_hi:[1,0,1]
	v_min_f32_e32 v72, 0x40e00000, v72
	v_min_f32_e32 v73, 0x40e00000, v73
	v_pk_add_f32 v[78:79], v[78:79], 1.0 op_sel_hi:[1,0]
	v_med3_f32 v66, v66, s69, v167
	v_rcp_f32_e32 v78, v78
	v_rcp_f32_e32 v79, v79
	v_med3_f32 v67, v67, s69, v167
	v_pk_mul_f32 v[80:81], v[72:73], s[84:85] op_sel_hi:[1,0]
	v_pk_fma_f32 v[66:67], v[66:67], 4.0, 4.0 op_sel_hi:[1,0,0]
	v_exp_f32_e32 v80, v80
	v_exp_f32_e32 v81, v81
	v_pk_mul_f32 v[70:71], v[70:71], v[78:79]
	v_pk_fma_f32 v[68:69], v[68:69], v[84:85], v[112:113] op_sel_hi:[1,0,1]
	v_pk_mul_f32 v[66:67], v[66:67], v[70:71]
	v_med3_f32 v68, v68, s69, v167
	v_med3_f32 v69, v69, s69, v167
	v_mov_b32_e32 v85, v147
	v_cvt_pk_fp8_f32 v85, v66, v67
	v_pk_fma_f32 v[66:67], v[68:69], 4.0, 4.0 op_sel_hi:[1,0,0]
	ds_read2_b32 v[68:69], v126 offset0:64 offset1:80
	v_pk_add_f32 v[70:71], v[80:81], 1.0 op_sel_hi:[1,0]
	v_mov_b32_e32 v84, v147
	v_rcp_f32_e32 v70, v70
	v_rcp_f32_e32 v71, v71
	s_waitcnt lgkmcnt(0)
	v_mul_f32_e32 v68, 0x3d000000, v68
	v_pk_fma_f32 v[62:63], v[62:63], v[68:69], v[156:157] op_sel_hi:[1,0,1]
	v_pk_fma_f32 v[64:65], v[64:65], v[68:69], v[154:155] op_sel_hi:[1,0,1]
	v_pk_mul_f32 v[70:71], v[72:73], v[70:71]
	v_min_f32_e32 v62, 0x40e00000, v62
	v_min_f32_e32 v63, 0x40e00000, v63
	v_pk_mul_f32 v[66:67], v[66:67], v[70:71]
	v_pk_mul_f32 v[70:71], v[62:63], s[84:85] op_sel_hi:[1,0]
	v_min_f32_e32 v64, 0x40e00000, v64
	v_exp_f32_e32 v70, v70
	v_exp_f32_e32 v71, v71
	v_min_f32_e32 v65, 0x40e00000, v65
	v_pk_mul_f32 v[72:73], v[64:65], s[84:85] op_sel_hi:[1,0]
	v_pk_fma_f32 v[58:59], v[58:59], v[68:69], v[132:133] op_sel_hi:[1,0,1]
	v_pk_add_f32 v[70:71], v[70:71], 1.0 op_sel_hi:[1,0]
	v_exp_f32_e32 v72, v72
	v_rcp_f32_e32 v70, v70
	v_rcp_f32_e32 v71, v71
	v_exp_f32_e32 v73, v73
	v_med3_f32 v58, v58, s69, v167
	v_med3_f32 v59, v59, s69, v167
	v_pk_mul_f32 v[62:63], v[62:63], v[70:71]
	v_pk_fma_f32 v[58:59], v[58:59], 4.0, 4.0 op_sel_hi:[1,0,0]
	v_pk_fma_f32 v[60:61], v[60:61], v[68:69], v[128:129] op_sel_hi:[1,0,1]
	v_pk_mul_f32 v[58:59], v[58:59], v[62:63]
	v_pk_add_f32 v[62:63], v[72:73], 1.0 op_sel_hi:[1,0]
	v_med3_f32 v60, v60, s69, v167
	v_rcp_f32_e32 v62, v62
	v_rcp_f32_e32 v63, v63
	v_med3_f32 v61, v61, s69, v167
	v_pk_fma_f32 v[54:55], v[54:55], v[68:69], v[152:153] op_sel_hi:[1,0,1]
	v_pk_fma_f32 v[60:61], v[60:61], 4.0, 4.0 op_sel_hi:[1,0,0]
	v_pk_mul_f32 v[62:63], v[64:65], v[62:63]
	v_min_f32_e32 v54, 0x40e00000, v54
	v_min_f32_e32 v55, 0x40e00000, v55
	v_pk_mul_f32 v[60:61], v[60:61], v[62:63]
	v_pk_mul_f32 v[62:63], v[54:55], s[84:85] op_sel_hi:[1,0]
	v_pk_fma_f32 v[56:57], v[56:57], v[68:69], v[150:151] op_sel_hi:[1,0,1]
	v_exp_f32_e32 v62, v62
	v_exp_f32_e32 v63, v63
	v_min_f32_e32 v56, 0x40e00000, v56
	v_min_f32_e32 v57, 0x40e00000, v57
	v_pk_mul_f32 v[64:65], v[56:57], s[84:85] op_sel_hi:[1,0]
	v_pk_add_f32 v[62:63], v[62:63], 1.0 op_sel_hi:[1,0]
	v_exp_f32_e32 v64, v64
	v_rcp_f32_e32 v62, v62
	v_rcp_f32_e32 v63, v63
	v_exp_f32_e32 v65, v65
	v_pk_fma_f32 v[50:51], v[50:51], v[68:69], v[120:121] op_sel_hi:[1,0,1]
	v_pk_fma_f32 v[52:53], v[52:53], v[68:69], v[112:113] op_sel_hi:[1,0,1]
	v_med3_f32 v50, v50, s69, v167
	v_med3_f32 v51, v51, s69, v167
	v_pk_mul_f32 v[54:55], v[54:55], v[62:63]
	v_pk_fma_f32 v[50:51], v[50:51], 4.0, 4.0 op_sel_hi:[1,0,0]
	v_med3_f32 v52, v52, s69, v167
	v_pk_mul_f32 v[54:55], v[50:51], v[54:55]
	v_pk_add_f32 v[50:51], v[64:65], 1.0 op_sel_hi:[1,0]
	v_med3_f32 v53, v53, s69, v167
	v_rcp_f32_e32 v50, v50
	v_rcp_f32_e32 v51, v51
	v_pk_fma_f32 v[52:53], v[52:53], 4.0, 4.0 op_sel_hi:[1,0,0]
	v_cvt_pk_fp8_f32 v84, v74, v75
	v_cvt_pk_fp8_f32 v82, v92, v93 op_sel:[0,0,1]
	v_pk_mul_f32 v[56:57], v[56:57], v[50:51]
	v_mov_b32_e32 v51, v147
	v_cvt_pk_fp8_f32 v51, v54, v55
	v_pk_mul_f32 v[52:53], v[52:53], v[56:57]
	v_cvt_pk_fp8_f32 v84, v76, v77 op_sel:[0,0,1]
	v_cvt_pk_fp8_f32 v85, v66, v67 op_sel:[0,0,1]
	v_cvt_pk_fp8_f32 v51, v52, v53 op_sel:[0,0,1]
	v_mul_f32_e32 v52, 0x3d000000, v69
	v_pk_fma_f32 v[46:47], v[46:47], v[52:53], v[156:157] op_sel_hi:[1,0,1]
	v_pk_fma_f32 v[48:49], v[48:49], v[52:53], v[154:155] op_sel_hi:[1,0,1]
	v_min_f32_e32 v46, 0x40e00000, v46
	v_min_f32_e32 v47, 0x40e00000, v47
	v_pk_mul_f32 v[54:55], v[46:47], s[84:85] op_sel_hi:[1,0]
	v_min_f32_e32 v48, 0x40e00000, v48
	v_exp_f32_e32 v54, v54
	v_exp_f32_e32 v55, v55
	v_min_f32_e32 v49, 0x40e00000, v49
	v_pk_mul_f32 v[56:57], v[48:49], s[84:85] op_sel_hi:[1,0]
	v_pk_fma_f32 v[42:43], v[42:43], v[52:53], v[132:133] op_sel_hi:[1,0,1]
	v_pk_add_f32 v[54:55], v[54:55], 1.0 op_sel_hi:[1,0]
	v_exp_f32_e32 v56, v56
	v_rcp_f32_e32 v54, v54
	v_rcp_f32_e32 v55, v55
	v_exp_f32_e32 v57, v57
	v_med3_f32 v42, v42, s69, v167
	v_med3_f32 v43, v43, s69, v167
	v_pk_mul_f32 v[46:47], v[46:47], v[54:55]
	v_pk_fma_f32 v[42:43], v[42:43], 4.0, 4.0 op_sel_hi:[1,0,0]
	v_pk_fma_f32 v[44:45], v[44:45], v[52:53], v[128:129] op_sel_hi:[1,0,1]
	v_pk_mul_f32 v[42:43], v[42:43], v[46:47]
	v_pk_add_f32 v[46:47], v[56:57], 1.0 op_sel_hi:[1,0]
; DI f32x2 swiglu4_2(f32x2 hg, f32x2 hl) {
;     f32x2 glu, lin, ex, sg;
;     glu[0] = fminf(hg[0], 7.0f); glu[1] = fminf(hg[1], 7.0f); lin[0] = __builtin_amdgcn_fmed3f(hl[0], -7.0f, 7.0f); lin[1] = __builtin_amdgcn_fmed3f(hl[1], -7.0f, 7.0f);
;     const f32x2 t = glu * (-1.702f * 1.4426950408889634f);
;     ex[0] = __builtin_amdgcn_exp2f(t[0]); ex[1] = __builtin_amdgcn_exp2f(t[1]);
;     const f32x2 den = ex + 1.0f;
;     DI void operator()(const f32x4 (&acc)[2][2][4][2], const Unit& u, int wr, int wc, int fr, int fq, const LAS unsigned char* st) const {
;         const int row0 = u.pm * BM + wr * 64 + fr, f0 = u.pn * HALF + wc * 32 + 8 * fq;
;         f32x2 bg[4], bl[4];
;         { const LAS float* sb = (const LAS float*)(st + 512 + fq * 64);
; #pragma unroll
;           for (int p = 0; p < 4; ++p) { bg[p][0] = sb[4 * p]; bg[p][1] = sb[4 * p + 2]; bl[p][0] = sb[4 * p + 1]; bl[p][1] = sb[4 * p + 3]; } }
; #pragma unroll
;         for (int ai = 0; ai < 2; ++ai)
; #pragma unroll
;             for (int mp = 0; mp < 2; ++mp) {
;                 u32x2 w2[2];
; #pragma unroll
;                 for (int mm = 0; mm < 2; ++mm) { const int m = 2 * mp + mm; const float ws = *(const LAS float*)(st + ai * 256 + (m * 16 + fr) * 4) * (1.0f / 32.0f);
;                     const f32x4 g0 = acc[ai][0][m][0], g1 = acc[ai][0][m][1], l0 = acc[ai][1][m][0], l1 = acc[ai][1][m][1];
;                     f32x2 ws2; ws2[0] = ws; ws2[1] = ws;
;                     const f32x2 a01 = swiglu4_2(__builtin_shufflevector(g0, g0, 0, 1) * ws2 + bg[0], __builtin_shufflevector(l0, l0, 0, 1) * ws2 + bl[0]);
;                     const f32x2 a23 = swiglu4_2(__builtin_shufflevector(g0, g0, 2, 3) * ws2 + bg[1], __builtin_shufflevector(l0, l0, 2, 3) * ws2 + bl[1]);
;                     const f32x2 a45 = swiglu4_2(__builtin_shufflevector(g1, g1, 0, 1) * ws2 + bg[2], __builtin_shufflevector(l1, l1, 0, 1) * ws2 + bl[2]);
;                     const f32x2 a67 = swiglu4_2(__builtin_shufflevector(g1, g1, 2, 3) * ws2 + bg[3], __builtin_shufflevector(l1, l1, 2, 3) * ws2 + bl[3]);
;                     w2[mm].x = pk4_fp8n(a01[0], a01[1], a23[0], a23[1]); w2[mm].y = pk4_fp8n(a45[0], a45[1], a67[0], a67[1]); }
;                 const u32x4 w = pair16(w2[0], w2[1]);
;                 *(u32x4*)(ACT + (size_t)(row0 + ai * HALF + (2 * mp + (fq & 1)) * 16) * FF + (f0 - 8 * (fq & 1))) = w; }
	v_med3_f32 v44, v44, s69, v167
	v_rcp_f32_e32 v46, v46
	v_rcp_f32_e32 v47, v47
	v_med3_f32 v45, v45, s69, v167
	v_pk_fma_f32 v[38:39], v[38:39], v[52:53], v[152:153] op_sel_hi:[1,0,1]
	v_pk_fma_f32 v[44:45], v[44:45], 4.0, 4.0 op_sel_hi:[1,0,0]
	v_pk_mul_f32 v[46:47], v[48:49], v[46:47]
	v_min_f32_e32 v38, 0x40e00000, v38
	v_min_f32_e32 v39, 0x40e00000, v39
	v_pk_mul_f32 v[44:45], v[44:45], v[46:47]
	v_pk_mul_f32 v[46:47], v[38:39], s[84:85] op_sel_hi:[1,0]
	v_pk_fma_f32 v[40:41], v[40:41], v[52:53], v[150:151] op_sel_hi:[1,0,1]
	v_exp_f32_e32 v46, v46
	v_exp_f32_e32 v47, v47
	v_min_f32_e32 v40, 0x40e00000, v40
	v_min_f32_e32 v41, 0x40e00000, v41
	v_pk_mul_f32 v[48:49], v[40:41], s[84:85] op_sel_hi:[1,0]
	v_pk_add_f32 v[46:47], v[46:47], 1.0 op_sel_hi:[1,0]
	v_exp_f32_e32 v48, v48
	v_rcp_f32_e32 v46, v46
	v_rcp_f32_e32 v47, v47
	v_exp_f32_e32 v49, v49
	v_pk_fma_f32 v[34:35], v[34:35], v[52:53], v[120:121] op_sel_hi:[1,0,1]
	v_pk_fma_f32 v[36:37], v[36:37], v[52:53], v[112:113] op_sel_hi:[1,0,1]
	v_med3_f32 v34, v34, s69, v167
	v_med3_f32 v35, v35, s69, v167
	v_pk_mul_f32 v[38:39], v[38:39], v[46:47]
	v_pk_fma_f32 v[34:35], v[34:35], 4.0, 4.0 op_sel_hi:[1,0,0]
	v_mov_b32_e32 v53, v147
	v_pk_mul_f32 v[34:35], v[34:35], v[38:39]
	v_pk_add_f32 v[38:39], v[48:49], 1.0 op_sel_hi:[1,0]
	v_cvt_pk_fp8_f32 v53, v34, v35
	v_rcp_f32_e32 v38, v38
	v_rcp_f32_e32 v39, v39
	v_med3_f32 v36, v36, s69, v167
	v_med3_f32 v37, v37, s69, v167
	v_or_b32_e32 v66, 32, v118
	v_mov_b32_e32 v50, v147
	v_pk_mul_f32 v[38:39], v[40:41], v[38:39]
	v_mov_b32_e32 v52, v147
	v_pk_fma_f32 v[34:35], v[36:37], 4.0, 4.0 op_sel_hi:[1,0,0]
	v_ashrrev_i32_e32 v67, 31, v66
	v_cvt_pk_fp8_f32 v50, v58, v59
	v_cvt_pk_fp8_f32 v52, v42, v43
	v_pk_mul_f32 v[34:35], v[34:35], v[38:39]
	v_lshlrev_b64 v[66:67], 11, v[66:67]
	v_cvt_pk_fp8_f32 v53, v34, v35 op_sel:[0,0,1]
	ds_read2_b32 v[34:35], v126 offset0:96 offset1:112
	v_lshl_add_u64 v[66:67], s[86:87], 0, v[66:67]
	v_permlane16_swap_b32_e32 v82, v84
	v_permlane16_swap_b32_e32 v83, v85
	v_lshl_add_u64 v[66:67], v[66:67], 0, v[110:111]
	global_store_dwordx4 v[66:67], v[82:85], off
	v_add_u32_e32 v66, 0x80, v118
	v_cvt_pk_fp8_f32 v50, v60, v61 op_sel:[0,0,1]
	v_cvt_pk_fp8_f32 v52, v44, v45 op_sel:[0,0,1]
	v_ashrrev_i32_e32 v67, 31, v66
	v_lshlrev_b64 v[36:37], 11, v[66:67]
	s_waitcnt lgkmcnt(0)
	v_mul_f32_e32 v34, 0x3d000000, v34
	v_lshl_add_u64 v[36:37], s[86:87], 0, v[36:37]
	v_pk_fma_f32 v[30:31], v[30:31], v[34:35], v[156:157] op_sel_hi:[1,0,1]
	v_permlane16_swap_b32_e32 v50, v52
	v_permlane16_swap_b32_e32 v51, v53
	v_lshl_add_u64 v[36:37], v[36:37], 0, v[110:111]
	v_min_f32_e32 v30, 0x40e00000, v30
	v_min_f32_e32 v31, 0x40e00000, v31
	global_store_dwordx4 v[36:37], v[50:53], off
	v_pk_mul_f32 v[36:37], v[30:31], s[84:85] op_sel_hi:[1,0]
	v_pk_fma_f32 v[32:33], v[32:33], v[34:35], v[154:155] op_sel_hi:[1,0,1]
	v_exp_f32_e32 v36, v36
	v_exp_f32_e32 v37, v37
	v_min_f32_e32 v32, 0x40e00000, v32
	v_min_f32_e32 v33, 0x40e00000, v33
	v_pk_mul_f32 v[38:39], v[32:33], s[84:85] op_sel_hi:[1,0]
	v_pk_add_f32 v[36:37], v[36:37], 1.0 op_sel_hi:[1,0]
	v_exp_f32_e32 v38, v38
	v_rcp_f32_e32 v36, v36
	v_rcp_f32_e32 v37, v37
	v_exp_f32_e32 v39, v39
	v_pk_fma_f32 v[26:27], v[26:27], v[34:35], v[132:133] op_sel_hi:[1,0,1]
	v_pk_fma_f32 v[28:29], v[28:29], v[34:35], v[128:129] op_sel_hi:[1,0,1]
	v_med3_f32 v26, v26, s69, v167
	v_med3_f32 v27, v27, s69, v167
	v_pk_mul_f32 v[30:31], v[30:31], v[36:37]
	v_pk_fma_f32 v[26:27], v[26:27], 4.0, 4.0 op_sel_hi:[1,0,0]
	v_med3_f32 v28, v28, s69, v167
	v_pk_mul_f32 v[26:27], v[26:27], v[30:31]
	v_pk_add_f32 v[30:31], v[38:39], 1.0 op_sel_hi:[1,0]
	v_med3_f32 v29, v29, s69, v167
	v_rcp_f32_e32 v30, v30
	v_rcp_f32_e32 v31, v31
	v_pk_fma_f32 v[22:23], v[22:23], v[34:35], v[152:153] op_sel_hi:[1,0,1]
	v_pk_fma_f32 v[28:29], v[28:29], 4.0, 4.0 op_sel_hi:[1,0,0]
	v_min_f32_e32 v22, 0x40e00000, v22
	v_pk_mul_f32 v[30:31], v[32:33], v[30:31]
	v_min_f32_e32 v23, 0x40e00000, v23
	v_pk_mul_f32 v[28:29], v[28:29], v[30:31]
	v_pk_mul_f32 v[30:31], v[22:23], s[84:85] op_sel_hi:[1,0]
	v_pk_fma_f32 v[24:25], v[24:25], v[34:35], v[150:151] op_sel_hi:[1,0,1]
	v_exp_f32_e32 v30, v30
	v_exp_f32_e32 v31, v31
	v_min_f32_e32 v24, 0x40e00000, v24
	v_min_f32_e32 v25, 0x40e00000, v25
	v_pk_mul_f32 v[32:33], v[24:25], s[84:85] op_sel_hi:[1,0]
	v_pk_add_f32 v[30:31], v[30:31], 1.0 op_sel_hi:[1,0]
	v_exp_f32_e32 v32, v32
	v_rcp_f32_e32 v30, v30
	v_rcp_f32_e32 v31, v31
	v_exp_f32_e32 v33, v33
	v_pk_fma_f32 v[18:19], v[18:19], v[34:35], v[120:121] op_sel_hi:[1,0,1]
	v_pk_fma_f32 v[20:21], v[20:21], v[34:35], v[112:113] op_sel_hi:[1,0,1]
	v_med3_f32 v18, v18, s69, v167
	v_med3_f32 v19, v19, s69, v167
	v_pk_mul_f32 v[22:23], v[22:23], v[30:31]
	v_pk_fma_f32 v[18:19], v[18:19], 4.0, 4.0 op_sel_hi:[1,0,0]
	v_med3_f32 v20, v20, s69, v167
	v_pk_mul_f32 v[22:23], v[18:19], v[22:23]
; #define LAS __attribute__((address_space(3)))
; DI unsigned pk4_fp8n(float a, float b, float c, float d) { int v = __builtin_amdgcn_cvt_pk_fp8_f32(a, b, 0, false); v = __builtin_amdgcn_cvt_pk_fp8_f32(c, d, v, true); return (unsigned)v; }
; #define PG8_DMA4(gp, lp) __builtin_amdgcn_global_load_lds((const unsigned*)(gp), (LAS unsigned*)(lp), 4, 0, 0)
;     DI void prefetch(const Unit& u, int wr, int wc, int lane, LAS unsigned char* st) const {
;         const float* rp = rows + u.pm * BM + wr * 64 + lane;
;         PG8_DMA4(rp, st); PG8_DMA4(rp + HALF, st + 256);
;         PG8_DMA4(b_up + (size_t)u.e * UPW + 2 * (u.pn * HALF + wc * 32) + lane, st + 512);
;     }
;     DI void operator()(const f32x4 (&acc)[2][2][4][2], const Unit& u, int wr, int wc, int fr, int fq, const LAS unsigned char* st) const {
;     ...
;                 for (int mm = 0; mm < 2; ++mm) { const int m = 2 * mp + mm; const float ws = *(const LAS float*)(st + ai * 256 + (m * 16 + fr) * 4) * (1.0f / 32.0f);
;                     const f32x4 g0 = acc[ai][0][m][0], g1 = acc[ai][0][m][1], l0 = acc[ai][1][m][0], l1 = acc[ai][1][m][1];
;                     f32x2 ws2; ws2[0] = ws; ws2[1] = ws;
;                     const f32x2 a01 = swiglu4_2(__builtin_shufflevector(g0, g0, 0, 1) * ws2 + bg[0], __builtin_shufflevector(l0, l0, 0, 1) * ws2 + bl[0]);
;                     const f32x2 a23 = swiglu4_2(__builtin_shufflevector(g0, g0, 2, 3) * ws2 + bg[1], __builtin_shufflevector(l0, l0, 2, 3) * ws2 + bl[1]);
;                     const f32x2 a45 = swiglu4_2(__builtin_shufflevector(g1, g1, 0, 1) * ws2 + bg[2], __builtin_shufflevector(l1, l1, 0, 1) * ws2 + bl[2]);
;                     const f32x2 a67 = swiglu4_2(__builtin_shufflevector(g1, g1, 2, 3) * ws2 + bg[3], __builtin_shufflevector(l1, l1, 2, 3) * ws2 + bl[3]);
;                     w2[mm].x = pk4_fp8n(a01[0], a01[1], a23[0], a23[1]); w2[mm].y = pk4_fp8n(a45[0], a45[1], a67[0], a67[1]); }
;                 const u32x4 w = pair16(w2[0], w2[1]);
;                 *(u32x4*)(ACT + (size_t)(row0 + ai * HALF + (2 * mp + (fq & 1)) * 16) * FF + (f0 - 8 * (fq & 1))) = w; }
	v_pk_add_f32 v[18:19], v[32:33], 1.0 op_sel_hi:[1,0]
	v_med3_f32 v21, v21, s69, v167
	v_rcp_f32_e32 v18, v18
	v_rcp_f32_e32 v19, v19
	v_pk_fma_f32 v[20:21], v[20:21], 4.0, 4.0 op_sel_hi:[1,0,0]
	v_pk_mul_f32 v[24:25], v[24:25], v[18:19]
	v_mov_b32_e32 v19, v147
	v_cvt_pk_fp8_f32 v19, v22, v23
	v_pk_mul_f32 v[20:21], v[20:21], v[24:25]
	v_mov_b32_e32 v18, v147
	v_cvt_pk_fp8_f32 v18, v26, v27
	v_cvt_pk_fp8_f32 v19, v20, v21 op_sel:[0,0,1]
	v_mul_f32_e32 v20, 0x3d000000, v35
	v_pk_fma_f32 v[14:15], v[14:15], v[20:21], v[156:157] op_sel_hi:[1,0,1]
	v_pk_fma_f32 v[16:17], v[16:17], v[20:21], v[154:155] op_sel_hi:[1,0,1]
	v_min_f32_e32 v14, 0x40e00000, v14
	v_min_f32_e32 v15, 0x40e00000, v15
	v_pk_mul_f32 v[22:23], v[14:15], s[84:85] op_sel_hi:[1,0]
	v_min_f32_e32 v16, 0x40e00000, v16
	v_exp_f32_e32 v22, v22
	v_exp_f32_e32 v23, v23
	v_min_f32_e32 v17, 0x40e00000, v17
	v_pk_mul_f32 v[24:25], v[16:17], s[84:85] op_sel_hi:[1,0]
	v_pk_fma_f32 v[10:11], v[10:11], v[20:21], v[132:133] op_sel_hi:[1,0,1]
	v_pk_add_f32 v[22:23], v[22:23], 1.0 op_sel_hi:[1,0]
	v_exp_f32_e32 v24, v24
	v_rcp_f32_e32 v22, v22
	v_rcp_f32_e32 v23, v23
	v_exp_f32_e32 v25, v25
	v_med3_f32 v10, v10, s69, v167
	v_med3_f32 v11, v11, s69, v167
	v_pk_mul_f32 v[14:15], v[14:15], v[22:23]
	v_pk_fma_f32 v[10:11], v[10:11], 4.0, 4.0 op_sel_hi:[1,0,0]
	v_pk_fma_f32 v[12:13], v[12:13], v[20:21], v[128:129] op_sel_hi:[1,0,1]
	v_pk_mul_f32 v[10:11], v[10:11], v[14:15]
	v_pk_add_f32 v[14:15], v[24:25], 1.0 op_sel_hi:[1,0]
	v_med3_f32 v12, v12, s69, v167
	v_rcp_f32_e32 v14, v14
	v_rcp_f32_e32 v15, v15
	v_med3_f32 v13, v13, s69, v167
	v_pk_fma_f32 v[6:7], v[6:7], v[20:21], v[152:153] op_sel_hi:[1,0,1]
	v_pk_fma_f32 v[12:13], v[12:13], 4.0, 4.0 op_sel_hi:[1,0,0]
	v_pk_mul_f32 v[14:15], v[16:17], v[14:15]
	v_min_f32_e32 v6, 0x40e00000, v6
	v_min_f32_e32 v7, 0x40e00000, v7
	v_pk_mul_f32 v[12:13], v[12:13], v[14:15]
	v_pk_mul_f32 v[14:15], v[6:7], s[84:85] op_sel_hi:[1,0]
	v_pk_fma_f32 v[8:9], v[8:9], v[20:21], v[150:151] op_sel_hi:[1,0,1]
	v_exp_f32_e32 v14, v14
	v_exp_f32_e32 v15, v15
	v_min_f32_e32 v8, 0x40e00000, v8
	v_min_f32_e32 v9, 0x40e00000, v9
	v_pk_mul_f32 v[16:17], v[8:9], s[84:85] op_sel_hi:[1,0]
	v_pk_add_f32 v[14:15], v[14:15], 1.0 op_sel_hi:[1,0]
	v_exp_f32_e32 v16, v16
	v_rcp_f32_e32 v14, v14
	v_rcp_f32_e32 v15, v15
	v_exp_f32_e32 v17, v17
	v_pk_fma_f32 v[2:3], v[2:3], v[20:21], v[120:121] op_sel_hi:[1,0,1]
	v_pk_fma_f32 v[4:5], v[4:5], v[20:21], v[112:113] op_sel_hi:[1,0,1]
	v_med3_f32 v2, v2, s69, v167
	v_med3_f32 v3, v3, s69, v167
	v_pk_mul_f32 v[6:7], v[6:7], v[14:15]
	v_pk_fma_f32 v[2:3], v[2:3], 4.0, 4.0 op_sel_hi:[1,0,0]
	v_mov_b32_e32 v20, v147
	v_pk_mul_f32 v[2:3], v[2:3], v[6:7]
	v_pk_add_f32 v[6:7], v[16:17], 1.0 op_sel_hi:[1,0]
	v_mov_b32_e32 v21, v147
	v_rcp_f32_e32 v6, v6
	v_rcp_f32_e32 v7, v7
	v_cvt_pk_fp8_f32 v20, v10, v11
	v_cvt_pk_fp8_f32 v21, v2, v3
	v_med3_f32 v4, v4, s69, v167
	v_med3_f32 v5, v5, s69, v167
	v_pk_mul_f32 v[6:7], v[8:9], v[6:7]
	v_pk_fma_f32 v[2:3], v[4:5], 4.0, 4.0 op_sel_hi:[1,0,0]
	v_cvt_pk_fp8_f32 v18, v28, v29 op_sel:[0,0,1]
	v_pk_mul_f32 v[2:3], v[2:3], v[6:7]
	v_cvt_pk_fp8_f32 v20, v12, v13 op_sel:[0,0,1]
	v_cvt_pk_fp8_f32 v21, v2, v3 op_sel:[0,0,1]
	v_add_u32_e32 v2, 0xa0, v118
	v_ashrrev_i32_e32 v3, 31, v2
	v_lshlrev_b64 v[2:3], 11, v[2:3]
	v_lshl_add_u64 v[2:3], s[86:87], 0, v[2:3]
	v_permlane16_swap_b32_e32 v18, v20
	v_permlane16_swap_b32_e32 v19, v21
	v_lshl_add_u64 v[2:3], v[2:3], 0, v[110:111]
	global_store_dwordx4 v[2:3], v[18:21], off
	s_waitcnt vmcnt(4)
	s_cbranch_vccnz .LBB0_1076
	s_lshl_b32 s0, s71, 8
	s_ashr_i32 s1, s0, 31
	v_mov_b32_e32 v2, v224
	s_lshl_b64 s[0:1], s[0:1], 2
	s_add_u32 s0, s62, s0
	v_ashrrev_i32_e32 v3, 31, v2
	s_addc_u32 s1, s63, s1
	v_lshlrev_b64 v[2:3], 2, v[2:3]
	s_mov_b32 m0, s35
	v_lshl_add_u64 v[4:5], s[0:1], 0, v[2:3]
	s_lshl_b64 s[0:1], s[30:31], 14
	v_readlane_b32 s16, v254, 25
	global_load_lds_dword v[4:5], off
	s_add_i32 m0, s35, 0x100
	v_readlane_b32 s30, v254, 39
	v_readlane_b32 s31, v254, 40
	s_add_u32 s2, s30, s0
	s_addc_u32 s3, s31, s1
	s_lshl_b32 s0, s76, 8
	s_or_b32 s0, s0, s51
	s_ashr_i32 s1, s0, 31
	s_lshl_b64 s[0:1], s[0:1], 2
	s_add_u32 s0, s2, s0
	v_lshl_add_u64 v[4:5], v[4:5], 0, s[12:13]
	s_addc_u32 s1, s3, s1
	global_load_lds_dword v[4:5], off
	v_lshl_add_u64 v[2:3], s[0:1], 0, v[2:3]
	s_mov_b32 m0, s70
	s_andn2_b64 vcc, exec, s[14:15]
	global_load_lds_dword v[2:3], off
	v_readlane_b32 s17, v254, 26
	v_readlane_b32 s18, v254, 27
	v_readlane_b32 s19, v254, 28
	v_readlane_b32 s20, v254, 29
	v_readlane_b32 s21, v254, 30
	v_readlane_b32 s22, v254, 31
	v_readlane_b32 s23, v254, 32
	v_readlane_b32 s24, v254, 33
	v_readlane_b32 s25, v254, 34
	v_readlane_b32 s26, v254, 35
	v_readlane_b32 s27, v254, 36
	v_readlane_b32 s28, v254, 37
	v_readlane_b32 s29, v254, 38
	s_cbranch_vccnz .LBB0_1075
	s_barrier
	s_branch .LBB0_1075

; DI const char* sptr(const char* p) { const unsigned long long v = (unsigned long long)p; const unsigned lo = __builtin_amdgcn_readfirstlane((unsigned)v), hi = __builtin_amdgcn_readfirstlane((unsigned)(v >> 32)); return (const char*)(((unsigned long long)hi << 32) | lo); }
; template <class Epi, bool GATHER, bool EXPERT, bool FP8>
; DI void gemm_phase(LAS unsigned char* lds, const Gemm g, const StaticOrder& S, const Epi& E) {
;     ...
;     for (;;) {
;         const bool has_next = S.next(ui + 1, nxt);
;         if (EXPERT) nxt.e = has_next ? __builtin_amdgcn_readfirstlane(g.tile_e[nxt.pm]) : 0;
;         const char* nA = sptr(has_next ? (const char*)g.A + (GATHER ? (size_t)0 : (size_t)nxt.pm * tstep) : cA);
;         const char* nB = sptr(has_next ? (const char*)g.Bt + (size_t)nxt.e * g.estride + (size_t)nxt.pn * tstep : cB);
;     ...
; #pragma unroll
;         for (int a = 0; a < 2; ++a)
; #pragma unroll
;             for (int b = 0; b < 2; ++b)
; #pragma unroll
;                 for (int m = 0; m < 4; ++m)
; #pragma unroll
;                     for (int n = 0; n < 2; ++n) acc[a][b][m][n] = (f32x4){0.f, 0.f, 0.f, 0.f};
;         cur = nxt; cA = nA; cB = nB; ++ui;
.LBB0_1160:
	s_ashr_i32 s23, s22, 31
	s_lshl_b64 s[0:1], s[22:23], 19
	s_add_u32 s21, s19, s0
	s_addc_u32 s23, s40, s1
	s_and_b64 s[0:1], s[4:5], exec
	s_cselect_b32 s24, s21, s34
	s_cselect_b32 s25, s23, s35
	s_lshl_b64 s[0:1], s[26:27], 22
	s_add_u32 s23, s41, s0
	s_addc_u32 s33, s42, s1
	s_ashr_i32 s21, s20, 31
	s_lshl_b64 s[0:1], s[20:21], 19
	s_add_u32 s21, s23, s0
	s_addc_u32 s23, s33, s1
	s_and_b64 s[0:1], s[4:5], exec
	s_cselect_b32 s4, s21, s36
	s_cselect_b32 s5, s23, s37
	s_add_u32 s0, s36, 0x100
	.p2align 8
	s_addc_u32 s1, s37, 0
	s_add_u32 s34, s34, 0x80
	v_mov_b32_e32 v0, 0
	s_addc_u32 s35, s35, 0
	s_mov_b32 s21, -2
	v_mov_b32_e32 v1, v0
	v_mov_b32_e32 v2, v0
	v_mov_b32_e32 v3, v0
	v_mov_b32_e32 v4, v0
	v_mov_b32_e32 v5, v0
	v_mov_b32_e32 v6, v0
	v_mov_b32_e32 v7, v0
	v_mov_b32_e32 v8, v0
	v_mov_b32_e32 v9, v0
	v_mov_b32_e32 v10, v0
	v_mov_b32_e32 v11, v0
	v_mov_b32_e32 v12, v0
	v_mov_b32_e32 v13, v0
	v_mov_b32_e32 v14, v0
	v_mov_b32_e32 v15, v0
	v_mov_b32_e32 v32, v0
	v_mov_b32_e32 v33, v0
	v_mov_b32_e32 v34, v0
	v_mov_b32_e32 v35, v0
	v_mov_b32_e32 v36, v0
	v_mov_b32_e32 v37, v0
	v_mov_b32_e32 v38, v0
	v_mov_b32_e32 v39, v0
	v_mov_b32_e32 v40, v0
	v_mov_b32_e32 v41, v0
	v_mov_b32_e32 v42, v0
	v_mov_b32_e32 v43, v0
	v_mov_b32_e32 v44, v0
	v_mov_b32_e32 v45, v0
	v_mov_b32_e32 v46, v0
	v_mov_b32_e32 v47, v0
	v_mov_b32_e32 v16, v0
	v_mov_b32_e32 v17, v0
	v_mov_b32_e32 v18, v0
	v_mov_b32_e32 v19, v0
	v_mov_b32_e32 v20, v0
	v_mov_b32_e32 v21, v0
	v_mov_b32_e32 v22, v0
	v_mov_b32_e32 v23, v0
	v_mov_b32_e32 v24, v0
	v_mov_b32_e32 v25, v0
	v_mov_b32_e32 v26, v0
	v_mov_b32_e32 v27, v0
	v_mov_b32_e32 v28, v0
	v_mov_b32_e32 v29, v0
	v_mov_b32_e32 v30, v0
	v_mov_b32_e32 v31, v0
	v_mov_b32_e32 v48, v0
	v_mov_b32_e32 v49, v0
	v_mov_b32_e32 v50, v0
	v_mov_b32_e32 v51, v0
	v_mov_b32_e32 v52, v0
	v_mov_b32_e32 v53, v0
	v_mov_b32_e32 v54, v0
	v_mov_b32_e32 v55, v0
	v_mov_b32_e32 v56, v0
	v_mov_b32_e32 v57, v0
	v_mov_b32_e32 v58, v0
	v_mov_b32_e32 v59, v0
	v_mov_b32_e32 v60, v0
	v_mov_b32_e32 v61, v0
	v_mov_b32_e32 v62, v0
	v_mov_b32_e32 v63, v0
	v_mov_b32_e32 v64, v0
	v_mov_b32_e32 v65, v0
	v_mov_b32_e32 v66, v0
	v_mov_b32_e32 v67, v0
	v_mov_b32_e32 v68, v0
	v_mov_b32_e32 v69, v0
	v_mov_b32_e32 v70, v0
	v_mov_b32_e32 v71, v0
	v_mov_b32_e32 v72, v0
	v_mov_b32_e32 v73, v0
	v_mov_b32_e32 v74, v0
	v_mov_b32_e32 v75, v0
	v_mov_b32_e32 v76, v0
	v_mov_b32_e32 v77, v0
	v_mov_b32_e32 v78, v0
	v_mov_b32_e32 v79, v0
	v_mov_b32_e32 v96, v0
	v_mov_b32_e32 v97, v0
	v_mov_b32_e32 v98, v0
	v_mov_b32_e32 v99, v0
	v_mov_b32_e32 v100, v0
	v_mov_b32_e32 v101, v0
	v_mov_b32_e32 v102, v0
	v_mov_b32_e32 v103, v0
	v_mov_b32_e32 v104, v0
	v_mov_b32_e32 v105, v0
	v_mov_b32_e32 v106, v0
	v_mov_b32_e32 v107, v0
	v_mov_b32_e32 v108, v0
	v_mov_b32_e32 v109, v0
	v_mov_b32_e32 v110, v0
	v_mov_b32_e32 v111, v0
	v_mov_b32_e32 v80, v0
	v_mov_b32_e32 v81, v0
	v_mov_b32_e32 v82, v0
	v_mov_b32_e32 v83, v0
	v_mov_b32_e32 v84, v0
	v_mov_b32_e32 v85, v0
	v_mov_b32_e32 v86, v0
	v_mov_b32_e32 v87, v0
	v_mov_b32_e32 v88, v0
	v_mov_b32_e32 v89, v0
	v_mov_b32_e32 v90, v0
	v_mov_b32_e32 v91, v0
	v_mov_b32_e32 v92, v0
	v_mov_b32_e32 v93, v0
	v_mov_b32_e32 v94, v0
	v_mov_b32_e32 v95, v0
	v_mov_b32_e32 v112, v0
	v_mov_b32_e32 v113, v0
	v_mov_b32_e32 v114, v0
	v_mov_b32_e32 v115, v0
	v_mov_b32_e32 v116, v0
	v_mov_b32_e32 v117, v0
	v_mov_b32_e32 v118, v0
	v_mov_b32_e32 v119, v0
	v_mov_b32_e32 v120, v0
	v_mov_b32_e32 v121, v0
	v_mov_b32_e32 v122, v0
	v_mov_b32_e32 v123, v0
	v_mov_b32_e32 v124, v0
	v_mov_b32_e32 v125, v0
	v_mov_b32_e32 v126, v0
	v_mov_b32_e32 v127, v0
	s_cmp_gt_u32 s61, 1
	s_cselect_b32 s32, -2, 1
.LBB0_1161:
	ds_read_b128 v[128:131], v157
	ds_read_b128 v[132:135], v157 offset:1024
	ds_read_b128 v[136:139], v157 offset:2048
	ds_read_b128 v[140:143], v157 offset:3072
	ds_read_b128 v[162:165], v158
	ds_read_b128 v[166:169], v158 offset:1024
	ds_read_b128 v[170:173], v158 offset:2048
	ds_read_b128 v[174:177], v158 offset:3072
	s_add_u32 s23, s34, 0x80
	s_addc_u32 s33, s35, 0
	s_cmp_eq_u32 s21, 12
	s_cselect_b32 s37, s25, s33
	s_cselect_b32 s36, s24, s23
	s_cselect_b32 s39, s5, s1
	s_cselect_b32 s38, s4, s0
	v_mov_b32_e32 v144, v153
	ds_read_b128 v[178:181], v159
	ds_read_b128 v[182:185], v159 offset:1024
	ds_read_b128 v[186:189], v159 offset:2048
	ds_read_b128 v[190:193], v159 offset:3072
	ds_read_b128 v[194:197], v159 offset:4096
	ds_read_b128 v[198:201], v159 offset:5120
	ds_read_b128 v[202:205], v159 offset:6144
	ds_read_b128 v[206:209], v159 offset:7168
	s_add_i32 m0, s31, 0xc000
	s_nop 0
	global_load_lds_dwordx4 v144, s[34:35]
	v_mov_b32_e32 v144, v155
	s_add_i32 m0, s31, 0xe000
	s_nop 0
	global_load_lds_dwordx4 v144, s[34:35]
	s_cmp_eq_u32 s21, s32
	s_cbranch_scc1 .Lskipw_p10_0
	s_waitcnt vmcnt(8)
.Lskipw_p10_0:
	s_waitcnt lgkmcnt(0)
	s_barrier
	s_setprio 1
	s_waitcnt lgkmcnt(0)
	v_mfma_scale_f32_16x16x128_f8f6f4 v[124:127], v[128:135], v[178:185], v[124:127], v160, v160 op_sel_hi:[0,0,0]
	v_mfma_scale_f32_16x16x128_f8f6f4 v[120:123], v[136:143], v[178:185], v[120:123], v160, v160 op_sel_hi:[0,0,0]
	v_mfma_scale_f32_16x16x128_f8f6f4 v[116:119], v[128:135], v[186:193], v[116:119], v160, v160 op_sel_hi:[0,0,0]
	v_mfma_scale_f32_16x16x128_f8f6f4 v[112:115], v[136:143], v[186:193], v[112:115], v160, v160 op_sel_hi:[0,0,0]
	v_mfma_scale_f32_16x16x128_f8f6f4 v[210:213], v[128:135], v[194:201], v[92:95], v160, v160 op_sel_hi:[0,0,0]
	v_mfma_scale_f32_16x16x128_f8f6f4 v[214:217], v[136:143], v[194:201], v[88:91], v160, v160 op_sel_hi:[0,0,0]
	v_mfma_scale_f32_16x16x128_f8f6f4 v[218:221], v[128:135], v[202:209], v[84:87], v160, v160 op_sel_hi:[0,0,0]
	v_mfma_scale_f32_16x16x128_f8f6f4 v[226:229], v[136:143], v[202:209], v[80:83], v160, v160 op_sel_hi:[0,0,0]
	s_setprio 0
	s_setprio 1
	v_mfma_scale_f32_16x16x128_f8f6f4 v[108:111], v[162:169], v[178:185], v[108:111], v160, v160 op_sel_hi:[0,0,0]
	v_mfma_scale_f32_16x16x128_f8f6f4 v[104:107], v[170:177], v[178:185], v[104:107], v160, v160 op_sel_hi:[0,0,0]
	v_mfma_scale_f32_16x16x128_f8f6f4 v[100:103], v[162:169], v[186:193], v[100:103], v160, v160 op_sel_hi:[0,0,0]
	v_mfma_scale_f32_16x16x128_f8f6f4 v[96:99], v[170:177], v[186:193], v[96:99], v160, v160 op_sel_hi:[0,0,0]
	v_mfma_scale_f32_16x16x128_f8f6f4 v[230:233], v[162:169], v[194:201], v[76:79], v160, v160 op_sel_hi:[0,0,0]
	v_mfma_scale_f32_16x16x128_f8f6f4 v[194:197], v[170:177], v[194:201], v[72:75], v160, v160 op_sel_hi:[0,0,0]
	v_mfma_scale_f32_16x16x128_f8f6f4 v[198:201], v[162:169], v[202:209], v[68:71], v160, v160 op_sel_hi:[0,0,0]
	v_mfma_scale_f32_16x16x128_f8f6f4 v[202:205], v[170:177], v[202:209], v[64:67], v160, v160 op_sel_hi:[0,0,0]
	s_setprio 0
	s_barrier
	v_mov_b32_e32 v144, v150
	s_add_i32 s23, s57, s43
	s_nop 2
	ds_read_b128 v[64:67], v159 offset:16384
	ds_read_b128 v[68:71], v159 offset:17408
	ds_read_b128 v[72:75], v159 offset:18432
	ds_read_b128 v[76:79], v159 offset:19456
	ds_read_b128 v[80:83], v159 offset:20480
	ds_read_b128 v[84:87], v159 offset:21504
	ds_read_b128 v[88:91], v159 offset:22528
	ds_read_b128 v[92:95], v159 offset:23552
	s_mov_b32 m0, s23
	s_nop 0
	global_load_lds_dwordx4 v144, s[38:39]
	v_mov_b32_e32 v144, v151
	s_add_i32 m0, s23, 0x2000
	s_add_u32 s62, s38, 0x40000
	global_load_lds_dwordx4 v144, s[38:39]
	s_addc_u32 s63, s39, 0
	v_mov_b32_e32 v144, v150
	s_add_i32 s23, s58, s43
	s_mov_b32 m0, s23
	s_nop 0
	global_load_lds_dwordx4 v144, s[62:63]
	v_mov_b32_e32 v144, v151
	s_add_i32 m0, s23, 0x2000
	s_nop 0
	global_load_lds_dwordx4 v144, s[62:63]
	v_mov_b32_e32 v144, v152
	s_mov_b32 m0, s31
	s_nop 0
	global_load_lds_dwordx4 v144, s[36:37]
	v_mov_b32_e32 v144, v154
	s_mov_b32 m0, s49
	s_nop 0
	global_load_lds_dwordx4 v144, s[36:37]
	s_cmp_eq_u32 s21, s32
	s_cbranch_scc1 .Lskipw_p10_1
	s_waitcnt vmcnt(8)
.Lskipw_p10_1:
	s_waitcnt lgkmcnt(0)
	s_barrier
	s_setprio 1
	s_waitcnt lgkmcnt(0)
	v_mfma_scale_f32_16x16x128_f8f6f4 v[60:63], v[128:135], v[64:71], v[60:63], v160, v160 op_sel_hi:[0,0,0]
	v_mfma_scale_f32_16x16x128_f8f6f4 v[56:59], v[136:143], v[64:71], v[56:59], v160, v160 op_sel_hi:[0,0,0]
	v_mfma_scale_f32_16x16x128_f8f6f4 v[52:55], v[128:135], v[72:79], v[52:55], v160, v160 op_sel_hi:[0,0,0]
	v_mfma_scale_f32_16x16x128_f8f6f4 v[48:51], v[136:143], v[72:79], v[48:51], v160, v160 op_sel_hi:[0,0,0]
	v_mfma_scale_f32_16x16x128_f8f6f4 v[28:31], v[128:135], v[80:87], v[28:31], v160, v160 op_sel_hi:[0,0,0]
	v_mfma_scale_f32_16x16x128_f8f6f4 v[24:27], v[136:143], v[80:87], v[24:27], v160, v160 op_sel_hi:[0,0,0]
	v_mfma_scale_f32_16x16x128_f8f6f4 v[20:23], v[128:135], v[88:95], v[20:23], v160, v160 op_sel_hi:[0,0,0]
	v_mfma_scale_f32_16x16x128_f8f6f4 v[16:19], v[136:143], v[88:95], v[16:19], v160, v160 op_sel_hi:[0,0,0]
	s_setprio 0
	s_setprio 1
	v_mfma_scale_f32_16x16x128_f8f6f4 v[44:47], v[162:169], v[64:71], v[44:47], v160, v160 op_sel_hi:[0,0,0]
	v_mfma_scale_f32_16x16x128_f8f6f4 v[40:43], v[170:177], v[64:71], v[40:43], v160, v160 op_sel_hi:[0,0,0]
	v_mfma_scale_f32_16x16x128_f8f6f4 v[36:39], v[162:169], v[72:79], v[36:39], v160, v160 op_sel_hi:[0,0,0]
	v_mfma_scale_f32_16x16x128_f8f6f4 v[32:35], v[170:177], v[72:79], v[32:35], v160, v160 op_sel_hi:[0,0,0]
	v_mfma_scale_f32_16x16x128_f8f6f4 v[12:15], v[162:169], v[80:87], v[12:15], v160, v160 op_sel_hi:[0,0,0]
	v_mfma_scale_f32_16x16x128_f8f6f4 v[8:11], v[170:177], v[80:87], v[8:11], v160, v160 op_sel_hi:[0,0,0]
	v_mfma_scale_f32_16x16x128_f8f6f4 v[4:7], v[162:169], v[88:95], v[4:7], v160, v160 op_sel_hi:[0,0,0]
	v_mfma_scale_f32_16x16x128_f8f6f4 v[0:3], v[170:177], v[88:95], v[0:3], v160, v160 op_sel_hi:[0,0,0]
	s_setprio 0
	s_barrier
	s_add_i32 s23, 0, 0x18000
	v_add_u32_e32 v64, s23, v156
	s_add_i32 s33, 0, 0x1c000
	ds_read_b128 v[128:131], v64
	ds_read_b128 v[132:135], v64 offset:1024
	ds_read_b128 v[136:139], v64 offset:2048
	ds_read_b128 v[140:143], v64 offset:3072
	v_add_u32_e32 v64, s33, v156
	ds_read_b128 v[162:165], v64
	ds_read_b128 v[166:169], v64 offset:1024
	ds_read_b128 v[170:173], v64 offset:2048
	ds_read_b128 v[174:177], v64 offset:3072
	v_mov_b32_e32 v80, v153
	s_mov_b32 m0, s50
	ds_read_b128 v[64:67], v159 offset:32768
	ds_read_b128 v[68:71], v159 offset:33792
	ds_read_b128 v[72:75], v159 offset:34816
	ds_read_b128 v[76:79], v159 offset:35840
	ds_read_b128 v[178:181], v159 offset:36864
	ds_read_b128 v[182:185], v159 offset:37888
	ds_read_b128 v[186:189], v159 offset:38912
	ds_read_b128 v[190:193], v159 offset:39936
	s_nop 0
	global_load_lds_dwordx4 v80, s[36:37]
	v_mov_b32_e32 v80, v155
	s_mov_b32 m0, s51
	s_nop 0
	global_load_lds_dwordx4 v80, s[36:37]
	s_waitcnt vmcnt(8)
	s_waitcnt lgkmcnt(0)
	s_barrier
	s_setprio 1
	s_waitcnt lgkmcnt(0)
	v_mfma_scale_f32_16x16x128_f8f6f4 v[124:127], v[128:135], v[64:71], v[124:127], v160, v160 op_sel_hi:[0,0,0]
	v_mfma_scale_f32_16x16x128_f8f6f4 v[120:123], v[136:143], v[64:71], v[120:123], v160, v160 op_sel_hi:[0,0,0]
	v_mfma_scale_f32_16x16x128_f8f6f4 v[116:119], v[128:135], v[72:79], v[116:119], v160, v160 op_sel_hi:[0,0,0]
	v_mfma_scale_f32_16x16x128_f8f6f4 v[112:115], v[136:143], v[72:79], v[112:115], v160, v160 op_sel_hi:[0,0,0]
	v_mfma_scale_f32_16x16x128_f8f6f4 v[92:95], v[128:135], v[178:185], v[210:213], v160, v160 op_sel_hi:[0,0,0]
	v_mfma_scale_f32_16x16x128_f8f6f4 v[88:91], v[136:143], v[178:185], v[214:217], v160, v160 op_sel_hi:[0,0,0]
	v_mfma_scale_f32_16x16x128_f8f6f4 v[84:87], v[128:135], v[186:193], v[218:221], v160, v160 op_sel_hi:[0,0,0]
	v_mfma_scale_f32_16x16x128_f8f6f4 v[80:83], v[136:143], v[186:193], v[226:229], v160, v160 op_sel_hi:[0,0,0]
	s_setprio 0
	s_setprio 1
	v_mfma_scale_f32_16x16x128_f8f6f4 v[108:111], v[162:169], v[64:71], v[108:111], v160, v160 op_sel_hi:[0,0,0]
	v_mfma_scale_f32_16x16x128_f8f6f4 v[104:107], v[170:177], v[64:71], v[104:107], v160, v160 op_sel_hi:[0,0,0]
	v_mfma_scale_f32_16x16x128_f8f6f4 v[100:103], v[162:169], v[72:79], v[100:103], v160, v160 op_sel_hi:[0,0,0]
	v_mfma_scale_f32_16x16x128_f8f6f4 v[96:99], v[170:177], v[72:79], v[96:99], v160, v160 op_sel_hi:[0,0,0]
	v_mfma_scale_f32_16x16x128_f8f6f4 v[76:79], v[162:169], v[178:185], v[230:233], v160, v160 op_sel_hi:[0,0,0]
	v_mfma_scale_f32_16x16x128_f8f6f4 v[72:75], v[170:177], v[178:185], v[194:197], v160, v160 op_sel_hi:[0,0,0]
	v_mfma_scale_f32_16x16x128_f8f6f4 v[68:71], v[162:169], v[186:193], v[198:201], v160, v160 op_sel_hi:[0,0,0]
	v_mfma_scale_f32_16x16x128_f8f6f4 v[64:67], v[170:177], v[186:193], v[202:205], v160, v160 op_sel_hi:[0,0,0]
	s_setprio 0
	s_barrier
	v_mov_b32_e32 v144, v150
	ds_read_b128 v[178:181], v159 offset:49152
	ds_read_b128 v[182:185], v159 offset:50176
	ds_read_b128 v[186:189], v159 offset:51200
	ds_read_b128 v[190:193], v159 offset:52224
	ds_read_b128 v[194:197], v159 offset:53248
	ds_read_b128 v[198:201], v159 offset:54272
	ds_read_b128 v[202:205], v159 offset:55296
	ds_read_b128 v[206:209], v159 offset:56320
	s_add_i32 s23, s23, s43
	v_lshl_add_u64 v[148:149], s[38:39], 0, v[144:145]
	v_lshl_add_u64 v[148:149], v[148:149], 0, s[14:15]
	s_mov_b32 m0, s23
	v_mov_b32_e32 v144, v151
	global_load_lds_dwordx4 v[148:149], off
	s_add_i32 m0, s23, 0x2000
	s_nop 0
	v_lshl_add_u64 v[148:149], s[38:39], 0, v[144:145]
	s_add_u32 s38, s38, 0x40080
	v_lshl_add_u64 v[148:149], v[148:149], 0, s[14:15]
	s_addc_u32 s39, s39, 0
	v_mov_b32_e32 v144, v150
	s_add_i32 s23, s33, s43
	global_load_lds_dwordx4 v[148:149], off
	s_mov_b32 m0, s23
	s_nop 0
	global_load_lds_dwordx4 v144, s[38:39]
	v_mov_b32_e32 v144, v151
	s_add_i32 m0, s23, 0x2000
	s_nop 0
	global_load_lds_dwordx4 v144, s[38:39]
	v_mov_b32_e32 v144, v152
	s_mov_b32 m0, s52
	v_lshl_add_u64 v[148:149], s[36:37], 0, v[144:145]
	v_lshl_add_u64 v[148:149], v[148:149], 0, s[14:15]
	v_mov_b32_e32 v144, v154
	global_load_lds_dwordx4 v[148:149], off
	s_mov_b32 m0, s53
	v_lshl_add_u64 v[148:149], s[36:37], 0, v[144:145]
	v_lshl_add_u64 v[148:149], v[148:149], 0, s[14:15]
	global_load_lds_dwordx4 v[148:149], off
	s_waitcnt vmcnt(8)
	s_waitcnt lgkmcnt(0)
	s_barrier
	s_setprio 1
	s_waitcnt lgkmcnt(0)
	v_mfma_scale_f32_16x16x128_f8f6f4 v[60:63], v[128:135], v[178:185], v[60:63], v160, v160 op_sel_hi:[0,0,0]
	v_mfma_scale_f32_16x16x128_f8f6f4 v[56:59], v[136:143], v[178:185], v[56:59], v160, v160 op_sel_hi:[0,0,0]
	v_mfma_scale_f32_16x16x128_f8f6f4 v[52:55], v[128:135], v[186:193], v[52:55], v160, v160 op_sel_hi:[0,0,0]
	v_mfma_scale_f32_16x16x128_f8f6f4 v[48:51], v[136:143], v[186:193], v[48:51], v160, v160 op_sel_hi:[0,0,0]
	v_mfma_scale_f32_16x16x128_f8f6f4 v[28:31], v[128:135], v[194:201], v[28:31], v160, v160 op_sel_hi:[0,0,0]
	v_mfma_scale_f32_16x16x128_f8f6f4 v[24:27], v[136:143], v[194:201], v[24:27], v160, v160 op_sel_hi:[0,0,0]
	v_mfma_scale_f32_16x16x128_f8f6f4 v[20:23], v[128:135], v[202:209], v[20:23], v160, v160 op_sel_hi:[0,0,0]
	v_mfma_scale_f32_16x16x128_f8f6f4 v[16:19], v[136:143], v[202:209], v[16:19], v160, v160 op_sel_hi:[0,0,0]
	s_setprio 0
	s_setprio 1
	v_mfma_scale_f32_16x16x128_f8f6f4 v[44:47], v[162:169], v[178:185], v[44:47], v160, v160 op_sel_hi:[0,0,0]
	v_mfma_scale_f32_16x16x128_f8f6f4 v[40:43], v[170:177], v[178:185], v[40:43], v160, v160 op_sel_hi:[0,0,0]
	v_mfma_scale_f32_16x16x128_f8f6f4 v[36:39], v[162:169], v[186:193], v[36:39], v160, v160 op_sel_hi:[0,0,0]
	v_mfma_scale_f32_16x16x128_f8f6f4 v[32:35], v[170:177], v[186:193], v[32:35], v160, v160 op_sel_hi:[0,0,0]
	v_mfma_scale_f32_16x16x128_f8f6f4 v[12:15], v[162:169], v[194:201], v[12:15], v160, v160 op_sel_hi:[0,0,0]
	v_mfma_scale_f32_16x16x128_f8f6f4 v[8:11], v[170:177], v[194:201], v[8:11], v160, v160 op_sel_hi:[0,0,0]
	v_mfma_scale_f32_16x16x128_f8f6f4 v[4:7], v[162:169], v[202:209], v[4:7], v160, v160 op_sel_hi:[0,0,0]
	v_mfma_scale_f32_16x16x128_f8f6f4 v[0:3], v[170:177], v[202:209], v[0:3], v160, v160 op_sel_hi:[0,0,0]
	s_setprio 0
	s_barrier
	s_add_i32 s21, s21, 2
	s_add_u32 s0, s0, 0x100
	s_addc_u32 s1, s1, 0
	s_add_u32 s34, s34, 0x100
	s_addc_u32 s35, s35, 0
	s_cmp_gt_u32 s21, 13
	s_cbranch_scc0 .LBB0_1161
	s_and_b64 vcc, exec, s[16:17]
	s_cbranch_vccz .LBB0_1164
	s_barrier
; #define LAS __attribute__((address_space(3)))
;     DI void operator()(const f32x4 (&acc)[2][2][4][2], const Unit& u, int wr, int wc, int fr, int fq, const LAS unsigned char* st) const {
;         const int row0 = u.pm * BM + wr * 64 + fr, col0 = u.pn * BM + wc * 32 + 8 * fq;
;         f32x4 bv[2][2];
; #pragma unroll
;         for (int bj = 0; bj < 2; ++bj)
; #pragma unroll
;             for (int n = 0; n < 2; ++n) bv[bj][n] = *(const LAS f32x4*)(st + 512 + bj * 128 + fq * 32 + 16 * n);
; #pragma unroll
;         for (int ai = 0; ai < 2; ++ai)
; #pragma unroll
;             for (int mp = 0; mp < 2; ++mp) {
;                 const float wA = *(const LAS float*)(st + ai * 256 + ((2 * mp) * 16 + fr) * 4) * 16.0f, wB = *(const LAS float*)(st + ai * 256 + ((2 * mp + 1) * 16 + fr) * 4) * 16.0f;
;                 unsigned char* rowp = YB + (size_t)(row0 + ai * HALF + (2 * mp + (fq & 1)) * 16) * DM + (col0 - 8 * (fq & 1));
; #pragma unroll
;                 for (int bj = 0; bj < 2; ++bj) { u32x2 w2[2];
; #pragma unroll
;                     for (int mm = 0; mm < 2; ++mm) { const int m = 2 * mp + mm; const float w8 = mm ? wB : wA;
;                         const f32x4 v0 = (acc[ai][bj][m][0] * (1.0f / 128.0f) + bv[bj][0]) * w8, v1 = (acc[ai][bj][m][1] * (1.0f / 128.0f) + bv[bj][1]) * w8;
;                         w2[mm].x = pk4_fp8m(v0[0], v0[1], v0[2], v0[3]); w2[mm].y = pk4_fp8m(v1[0], v1[1], v1[2], v1[3]); }
;                     *(u32x4*)(rowp + bj * HALF) = pair16(w2[0], w2[1]); } }
.LBB0_1164:
	v_mov_b32_e32 v128, v224
	s_lshl_b32 s0, s30, 8
	v_and_b32_e32 v144, 15, v128
	v_ashrrev_i32_e32 v148, 4, v128
	v_lshl_add_u32 v128, v148, 5, s29
	v_lshl_add_u32 v169, v144, 2, s29
	ds_read_b128 v[140:143], v128 offset:512
	ds_read_b128 v[136:139], v128 offset:528
	ds_read_b128 v[132:135], v128 offset:640
	ds_read_b128 v[128:131], v128 offset:656
	ds_read2_b32 v[162:163], v169 offset1:16
	s_add_i32 s0, s0, s44
	v_or_b32_e32 v168, s0, v144
	s_lshl_b32 s0, s28, 8
	s_or_b32 s0, s0, s45
	v_and_b32_e32 v144, 1, v148
	v_lshl_add_u32 v149, v148, 3, s0
	v_lshlrev_b32_e32 v148, 3, v144
	v_lshlrev_b32_e32 v170, 4, v144
	s_waitcnt lgkmcnt(0)
	v_mul_f32_e32 v144, 0x41800000, v162
	v_pk_fma_f32 v[124:125], v[124:125], s[18:19], v[140:141] op_sel_hi:[1,0,1]
	v_pk_fma_f32 v[126:127], v[126:127], s[18:19], v[142:143] op_sel_hi:[1,0,1]
	v_pk_mul_f32 v[124:125], v[124:125], v[144:145] op_sel_hi:[1,0]
	v_pk_fma_f32 v[120:121], v[120:121], s[18:19], v[136:137] op_sel_hi:[1,0,1]
	v_pk_mul_f32 v[126:127], v[126:127], v[144:145] op_sel_hi:[1,0]
	v_pk_mul_f32 v[166:167], v[120:121], v[144:145] op_sel_hi:[1,0]
	v_med3_f32 v121, v124, s59, v161
	v_med3_f32 v124, v125, s59, v161
	v_mov_b32_e32 v120, v145
	v_med3_f32 v125, v126, s59, v161
	v_med3_f32 v126, v127, s59, v161
	v_cvt_pk_fp8_f32 v120, v121, v124
	v_med3_f32 v124, v166, s59, v161
	v_med3_f32 v127, v167, s59, v161
	v_mov_b32_e32 v121, v145
	v_cvt_pk_fp8_f32 v121, v124, v127
	v_pk_fma_f32 v[122:123], v[122:123], s[18:19], v[138:139] op_sel_hi:[1,0,1]
	v_mul_f32_e32 v124, 0x41800000, v163
	v_pk_mul_f32 v[122:123], v[122:123], v[144:145] op_sel_hi:[1,0]
	v_pk_fma_f32 v[112:113], v[112:113], s[18:19], v[136:137] op_sel_hi:[1,0,1]
	v_med3_f32 v122, v122, s59, v161
	v_med3_f32 v123, v123, s59, v161
	v_pk_mul_f32 v[112:113], v[112:113], v[124:125] op_sel_hi:[1,0]
	v_cvt_pk_fp8_f32 v121, v122, v123 op_sel:[0,0,1]
	v_med3_f32 v112, v112, s59, v161
	v_med3_f32 v113, v113, s59, v161
	v_mov_b32_e32 v123, v145
	v_cvt_pk_fp8_f32 v123, v112, v113
	v_pk_fma_f32 v[114:115], v[114:115], s[18:19], v[138:139] op_sel_hi:[1,0,1]
	v_pk_fma_f32 v[108:109], v[108:109], s[18:19], v[132:133] op_sel_hi:[1,0,1]
	v_pk_mul_f32 v[114:115], v[114:115], v[124:125] op_sel_hi:[1,0]
	v_pk_fma_f32 v[110:111], v[110:111], s[18:19], v[134:135] op_sel_hi:[1,0,1]
	v_med3_f32 v112, v114, s59, v161
	v_med3_f32 v113, v115, s59, v161
	v_pk_mul_f32 v[108:109], v[108:109], v[144:145] op_sel_hi:[1,0]
	v_pk_fma_f32 v[104:105], v[104:105], s[18:19], v[128:129] op_sel_hi:[1,0,1]
	v_cvt_pk_fp8_f32 v123, v112, v113 op_sel:[0,0,1]
	v_pk_mul_f32 v[110:111], v[110:111], v[144:145] op_sel_hi:[1,0]
	v_pk_mul_f32 v[112:113], v[104:105], v[144:145] op_sel_hi:[1,0]
	v_med3_f32 v105, v108, s59, v161
	v_med3_f32 v108, v109, s59, v161
	v_mov_b32_e32 v104, v145
	v_med3_f32 v109, v110, s59, v161
	v_med3_f32 v110, v111, s59, v161
	v_cvt_pk_fp8_f32 v104, v105, v108
	v_med3_f32 v108, v112, s59, v161
	v_med3_f32 v111, v113, s59, v161
	v_mov_b32_e32 v105, v145
	v_cvt_pk_fp8_f32 v105, v108, v111
	v_pk_fma_f32 v[106:107], v[106:107], s[18:19], v[130:131] op_sel_hi:[1,0,1]
	v_pk_fma_f32 v[96:97], v[96:97], s[18:19], v[128:129] op_sel_hi:[1,0,1]
	v_pk_mul_f32 v[106:107], v[106:107], v[144:145] op_sel_hi:[1,0]
	v_pk_mul_f32 v[96:97], v[96:97], v[124:125] op_sel_hi:[1,0]
	v_med3_f32 v106, v106, s59, v161
	v_med3_f32 v107, v107, s59, v161
	v_cvt_pk_fp8_f32 v105, v106, v107 op_sel:[0,0,1]
	v_med3_f32 v96, v96, s59, v161
	v_med3_f32 v97, v97, s59, v161
	v_mov_b32_e32 v107, v145
	v_cvt_pk_fp8_f32 v107, v96, v97
	v_pk_fma_f32 v[98:99], v[98:99], s[18:19], v[130:131] op_sel_hi:[1,0,1]
	v_pk_fma_f32 v[100:101], v[100:101], s[18:19], v[132:133] op_sel_hi:[1,0,1]
	v_pk_mul_f32 v[98:99], v[98:99], v[124:125] op_sel_hi:[1,0]
	v_pk_mul_f32 v[100:101], v[100:101], v[124:125] op_sel_hi:[1,0]
	v_med3_f32 v96, v98, s59, v161
	v_med3_f32 v97, v99, s59, v161
	v_cvt_pk_fp8_f32 v107, v96, v97 op_sel:[0,0,1]
	ds_read2_b32 v[96:97], v169 offset0:32 offset1:48
	v_pk_fma_f32 v[92:93], v[92:93], s[18:19], v[140:141] op_sel_hi:[1,0,1]
	v_med3_f32 v100, v100, s59, v161
	v_med3_f32 v101, v101, s59, v161
	v_mov_b32_e32 v106, v145
	s_waitcnt lgkmcnt(0)
	v_mul_f32_e32 v96, 0x41800000, v96
	v_pk_fma_f32 v[94:95], v[94:95], s[18:19], v[142:143] op_sel_hi:[1,0,1]
	v_pk_mul_f32 v[92:93], v[92:93], v[96:97] op_sel_hi:[1,0]
	v_pk_fma_f32 v[88:89], v[88:89], s[18:19], v[136:137] op_sel_hi:[1,0,1]
	v_cvt_pk_fp8_f32 v106, v100, v101
	v_pk_mul_f32 v[94:95], v[94:95], v[96:97] op_sel_hi:[1,0]
	v_pk_mul_f32 v[100:101], v[88:89], v[96:97] op_sel_hi:[1,0]
	v_med3_f32 v89, v92, s59, v161
	v_med3_f32 v92, v93, s59, v161
	v_mov_b32_e32 v88, v145
	v_med3_f32 v93, v94, s59, v161
	v_med3_f32 v94, v95, s59, v161
	v_cvt_pk_fp8_f32 v88, v89, v92
	v_med3_f32 v92, v100, s59, v161
	v_med3_f32 v95, v101, s59, v161
	v_mov_b32_e32 v89, v145
	v_cvt_pk_fp8_f32 v89, v92, v95
	v_pk_fma_f32 v[90:91], v[90:91], s[18:19], v[138:139] op_sel_hi:[1,0,1]
	v_mul_f32_e32 v92, 0x41800000, v97
	v_pk_mul_f32 v[90:91], v[90:91], v[96:97] op_sel_hi:[1,0]
	v_pk_fma_f32 v[80:81], v[80:81], s[18:19], v[136:137] op_sel_hi:[1,0,1]
	v_med3_f32 v90, v90, s59, v161
	v_med3_f32 v91, v91, s59, v161
	v_pk_mul_f32 v[80:81], v[80:81], v[92:93] op_sel_hi:[1,0]
	v_cvt_pk_fp8_f32 v89, v90, v91 op_sel:[0,0,1]
	v_med3_f32 v80, v80, s59, v161
	v_med3_f32 v81, v81, s59, v161
	v_mov_b32_e32 v91, v145
	v_cvt_pk_fp8_f32 v91, v80, v81
	v_pk_fma_f32 v[82:83], v[82:83], s[18:19], v[138:139] op_sel_hi:[1,0,1]
	v_pk_fma_f32 v[76:77], v[76:77], s[18:19], v[132:133] op_sel_hi:[1,0,1]
	v_pk_mul_f32 v[82:83], v[82:83], v[92:93] op_sel_hi:[1,0]
; #define LAS __attribute__((address_space(3)))
;     DI void operator()(const f32x4 (&acc)[2][2][4][2], const Unit& u, int wr, int wc, int fr, int fq, const LAS unsigned char* st) const {
;     ...
;             for (int mp = 0; mp < 2; ++mp) {
;                 const float wA = *(const LAS float*)(st + ai * 256 + ((2 * mp) * 16 + fr) * 4) * 16.0f, wB = *(const LAS float*)(st + ai * 256 + ((2 * mp + 1) * 16 + fr) * 4) * 16.0f;
;                 unsigned char* rowp = YB + (size_t)(row0 + ai * HALF + (2 * mp + (fq & 1)) * 16) * DM + (col0 - 8 * (fq & 1));
; #pragma unroll
;                 for (int bj = 0; bj < 2; ++bj) { u32x2 w2[2];
; #pragma unroll
;                     for (int mm = 0; mm < 2; ++mm) { const int m = 2 * mp + mm; const float w8 = mm ? wB : wA;
;                         const f32x4 v0 = (acc[ai][bj][m][0] * (1.0f / 128.0f) + bv[bj][0]) * w8, v1 = (acc[ai][bj][m][1] * (1.0f / 128.0f) + bv[bj][1]) * w8;
;                         w2[mm].x = pk4_fp8m(v0[0], v0[1], v0[2], v0[3]); w2[mm].y = pk4_fp8m(v1[0], v1[1], v1[2], v1[3]); }
;                     *(u32x4*)(rowp + bj * HALF) = pair16(w2[0], w2[1]); } }
	v_pk_fma_f32 v[78:79], v[78:79], s[18:19], v[134:135] op_sel_hi:[1,0,1]
	v_med3_f32 v80, v82, s59, v161
	v_med3_f32 v81, v83, s59, v161
	v_pk_mul_f32 v[76:77], v[76:77], v[96:97] op_sel_hi:[1,0]
	v_pk_fma_f32 v[72:73], v[72:73], s[18:19], v[128:129] op_sel_hi:[1,0,1]
	v_cvt_pk_fp8_f32 v91, v80, v81 op_sel:[0,0,1]
	v_pk_mul_f32 v[78:79], v[78:79], v[96:97] op_sel_hi:[1,0]
	v_pk_mul_f32 v[80:81], v[72:73], v[96:97] op_sel_hi:[1,0]
	v_med3_f32 v73, v76, s59, v161
	v_med3_f32 v76, v77, s59, v161
	v_mov_b32_e32 v72, v145
	v_med3_f32 v77, v78, s59, v161
	v_med3_f32 v78, v79, s59, v161
	v_cvt_pk_fp8_f32 v72, v73, v76
	v_med3_f32 v76, v80, s59, v161
	v_med3_f32 v79, v81, s59, v161
	v_mov_b32_e32 v73, v145
	v_cvt_pk_fp8_f32 v73, v76, v79
	v_pk_fma_f32 v[74:75], v[74:75], s[18:19], v[130:131] op_sel_hi:[1,0,1]
	v_pk_fma_f32 v[64:65], v[64:65], s[18:19], v[128:129] op_sel_hi:[1,0,1]
	v_pk_mul_f32 v[74:75], v[74:75], v[96:97] op_sel_hi:[1,0]
	v_pk_mul_f32 v[64:65], v[64:65], v[92:93] op_sel_hi:[1,0]
	v_med3_f32 v74, v74, s59, v161
	v_med3_f32 v75, v75, s59, v161
	v_cvt_pk_fp8_f32 v73, v74, v75 op_sel:[0,0,1]
	v_med3_f32 v64, v64, s59, v161
	v_med3_f32 v65, v65, s59, v161
	v_mov_b32_e32 v75, v145
	v_cvt_pk_fp8_f32 v75, v64, v65
	v_pk_fma_f32 v[66:67], v[66:67], s[18:19], v[130:131] op_sel_hi:[1,0,1]
	v_pk_fma_f32 v[68:69], v[68:69], s[18:19], v[132:133] op_sel_hi:[1,0,1]
	v_pk_mul_f32 v[66:67], v[66:67], v[92:93] op_sel_hi:[1,0]
	v_pk_mul_f32 v[68:69], v[68:69], v[92:93] op_sel_hi:[1,0]
	v_med3_f32 v64, v66, s59, v161
	v_med3_f32 v65, v67, s59, v161
	v_cvt_pk_fp8_f32 v75, v64, v65 op_sel:[0,0,1]
	ds_read2_b32 v[64:65], v169 offset0:64 offset1:80
	v_pk_fma_f32 v[60:61], v[60:61], s[18:19], v[140:141] op_sel_hi:[1,0,1]
	v_med3_f32 v68, v68, s59, v161
	v_med3_f32 v69, v69, s59, v161
	v_mov_b32_e32 v74, v145
	s_waitcnt lgkmcnt(0)
	v_mul_f32_e32 v64, 0x41800000, v64
	v_pk_fma_f32 v[62:63], v[62:63], s[18:19], v[142:143] op_sel_hi:[1,0,1]
	v_pk_mul_f32 v[60:61], v[60:61], v[64:65] op_sel_hi:[1,0]
	v_pk_fma_f32 v[56:57], v[56:57], s[18:19], v[136:137] op_sel_hi:[1,0,1]
	v_cvt_pk_fp8_f32 v74, v68, v69
	v_pk_mul_f32 v[62:63], v[62:63], v[64:65] op_sel_hi:[1,0]
	v_pk_mul_f32 v[68:69], v[56:57], v[64:65] op_sel_hi:[1,0]
	v_med3_f32 v57, v60, s59, v161
	v_med3_f32 v60, v61, s59, v161
	v_mov_b32_e32 v56, v145
	v_med3_f32 v61, v62, s59, v161
	v_med3_f32 v62, v63, s59, v161
	v_cvt_pk_fp8_f32 v56, v57, v60
	v_med3_f32 v60, v68, s59, v161
	v_med3_f32 v63, v69, s59, v161
	v_mov_b32_e32 v57, v145
	v_cvt_pk_fp8_f32 v57, v60, v63
	v_pk_fma_f32 v[58:59], v[58:59], s[18:19], v[138:139] op_sel_hi:[1,0,1]
	v_mul_f32_e32 v60, 0x41800000, v65
	v_pk_mul_f32 v[58:59], v[58:59], v[64:65] op_sel_hi:[1,0]
	v_pk_fma_f32 v[48:49], v[48:49], s[18:19], v[136:137] op_sel_hi:[1,0,1]
	v_med3_f32 v58, v58, s59, v161
	v_med3_f32 v59, v59, s59, v161
	v_pk_mul_f32 v[48:49], v[48:49], v[60:61] op_sel_hi:[1,0]
	v_cvt_pk_fp8_f32 v57, v58, v59 op_sel:[0,0,1]
	v_med3_f32 v48, v48, s59, v161
	v_med3_f32 v49, v49, s59, v161
	v_mov_b32_e32 v59, v145
	v_cvt_pk_fp8_f32 v59, v48, v49
	v_pk_fma_f32 v[50:51], v[50:51], s[18:19], v[138:139] op_sel_hi:[1,0,1]
	v_pk_fma_f32 v[44:45], v[44:45], s[18:19], v[132:133] op_sel_hi:[1,0,1]
	v_pk_mul_f32 v[50:51], v[50:51], v[60:61] op_sel_hi:[1,0]
	v_pk_fma_f32 v[46:47], v[46:47], s[18:19], v[134:135] op_sel_hi:[1,0,1]
	v_med3_f32 v48, v50, s59, v161
	v_med3_f32 v49, v51, s59, v161
	v_pk_mul_f32 v[44:45], v[44:45], v[64:65] op_sel_hi:[1,0]
	v_pk_fma_f32 v[40:41], v[40:41], s[18:19], v[128:129] op_sel_hi:[1,0,1]
	v_cvt_pk_fp8_f32 v59, v48, v49 op_sel:[0,0,1]
	v_pk_mul_f32 v[46:47], v[46:47], v[64:65] op_sel_hi:[1,0]
	v_pk_mul_f32 v[48:49], v[40:41], v[64:65] op_sel_hi:[1,0]
	v_med3_f32 v41, v44, s59, v161
	v_med3_f32 v44, v45, s59, v161
	v_mov_b32_e32 v40, v145
	v_med3_f32 v45, v46, s59, v161
	v_med3_f32 v46, v47, s59, v161
	v_cvt_pk_fp8_f32 v40, v41, v44
	v_med3_f32 v44, v48, s59, v161
	v_med3_f32 v47, v49, s59, v161
	v_mov_b32_e32 v41, v145
	v_cvt_pk_fp8_f32 v41, v44, v47
	v_pk_fma_f32 v[42:43], v[42:43], s[18:19], v[130:131] op_sel_hi:[1,0,1]
	v_pk_fma_f32 v[32:33], v[32:33], s[18:19], v[128:129] op_sel_hi:[1,0,1]
	v_pk_mul_f32 v[42:43], v[42:43], v[64:65] op_sel_hi:[1,0]
	v_pk_mul_f32 v[32:33], v[32:33], v[60:61] op_sel_hi:[1,0]
	v_med3_f32 v42, v42, s59, v161
	v_med3_f32 v43, v43, s59, v161
	v_cvt_pk_fp8_f32 v41, v42, v43 op_sel:[0,0,1]
	v_med3_f32 v32, v32, s59, v161
	v_med3_f32 v33, v33, s59, v161
	v_mov_b32_e32 v43, v145
	v_cvt_pk_fp8_f32 v43, v32, v33
	v_pk_fma_f32 v[34:35], v[34:35], s[18:19], v[130:131] op_sel_hi:[1,0,1]
	v_pk_fma_f32 v[36:37], v[36:37], s[18:19], v[132:133] op_sel_hi:[1,0,1]
	v_pk_mul_f32 v[34:35], v[34:35], v[60:61] op_sel_hi:[1,0]
	v_pk_mul_f32 v[36:37], v[36:37], v[60:61] op_sel_hi:[1,0]
	v_med3_f32 v32, v34, s59, v161
	v_med3_f32 v33, v35, s59, v161
	v_cvt_pk_fp8_f32 v43, v32, v33 op_sel:[0,0,1]
	ds_read2_b32 v[32:33], v169 offset0:96 offset1:112
	v_pk_fma_f32 v[28:29], v[28:29], s[18:19], v[140:141] op_sel_hi:[1,0,1]
	v_med3_f32 v36, v36, s59, v161
	v_med3_f32 v37, v37, s59, v161
	v_mov_b32_e32 v42, v145
	s_waitcnt lgkmcnt(0)
; #define LAS __attribute__((address_space(3)))
;     DI void operator()(const f32x4 (&acc)[2][2][4][2], const Unit& u, int wr, int wc, int fr, int fq, const LAS unsigned char* st) const {
;     ...
;             for (int mp = 0; mp < 2; ++mp) {
;                 const float wA = *(const LAS float*)(st + ai * 256 + ((2 * mp) * 16 + fr) * 4) * 16.0f, wB = *(const LAS float*)(st + ai * 256 + ((2 * mp + 1) * 16 + fr) * 4) * 16.0f;
;                 unsigned char* rowp = YB + (size_t)(row0 + ai * HALF + (2 * mp + (fq & 1)) * 16) * DM + (col0 - 8 * (fq & 1));
; #pragma unroll
;                 for (int bj = 0; bj < 2; ++bj) { u32x2 w2[2];
; #pragma unroll
;                     for (int mm = 0; mm < 2; ++mm) { const int m = 2 * mp + mm; const float w8 = mm ? wB : wA;
;                         const f32x4 v0 = (acc[ai][bj][m][0] * (1.0f / 128.0f) + bv[bj][0]) * w8, v1 = (acc[ai][bj][m][1] * (1.0f / 128.0f) + bv[bj][1]) * w8;
;                         w2[mm].x = pk4_fp8m(v0[0], v0[1], v0[2], v0[3]); w2[mm].y = pk4_fp8m(v1[0], v1[1], v1[2], v1[3]); }
;                     *(u32x4*)(rowp + bj * HALF) = pair16(w2[0], w2[1]); } }
	v_mul_f32_e32 v32, 0x41800000, v32
	v_pk_fma_f32 v[30:31], v[30:31], s[18:19], v[142:143] op_sel_hi:[1,0,1]
	v_pk_mul_f32 v[28:29], v[28:29], v[32:33] op_sel_hi:[1,0]
	v_pk_fma_f32 v[24:25], v[24:25], s[18:19], v[136:137] op_sel_hi:[1,0,1]
	v_cvt_pk_fp8_f32 v42, v36, v37
	v_pk_mul_f32 v[30:31], v[30:31], v[32:33] op_sel_hi:[1,0]
	v_pk_mul_f32 v[36:37], v[24:25], v[32:33] op_sel_hi:[1,0]
	v_med3_f32 v25, v28, s59, v161
	v_med3_f32 v28, v29, s59, v161
	v_mov_b32_e32 v24, v145
	v_med3_f32 v29, v30, s59, v161
	v_med3_f32 v30, v31, s59, v161
	v_cvt_pk_fp8_f32 v24, v25, v28
	v_med3_f32 v28, v36, s59, v161
	v_med3_f32 v31, v37, s59, v161
	v_mov_b32_e32 v25, v145
	v_cvt_pk_fp8_f32 v25, v28, v31
	v_pk_fma_f32 v[26:27], v[26:27], s[18:19], v[138:139] op_sel_hi:[1,0,1]
	v_mul_f32_e32 v28, 0x41800000, v33
	v_pk_mul_f32 v[26:27], v[26:27], v[32:33] op_sel_hi:[1,0]
	v_pk_fma_f32 v[16:17], v[16:17], s[18:19], v[136:137] op_sel_hi:[1,0,1]
	v_med3_f32 v26, v26, s59, v161
	v_med3_f32 v27, v27, s59, v161
	v_pk_mul_f32 v[16:17], v[16:17], v[28:29] op_sel_hi:[1,0]
	v_cvt_pk_fp8_f32 v25, v26, v27 op_sel:[0,0,1]
	v_med3_f32 v16, v16, s59, v161
	v_med3_f32 v17, v17, s59, v161
	v_mov_b32_e32 v27, v145
	v_cvt_pk_fp8_f32 v27, v16, v17
	v_pk_fma_f32 v[18:19], v[18:19], s[18:19], v[138:139] op_sel_hi:[1,0,1]
	v_pk_fma_f32 v[12:13], v[12:13], s[18:19], v[132:133] op_sel_hi:[1,0,1]
	v_pk_mul_f32 v[18:19], v[18:19], v[28:29] op_sel_hi:[1,0]
	v_pk_fma_f32 v[14:15], v[14:15], s[18:19], v[134:135] op_sel_hi:[1,0,1]
	v_med3_f32 v16, v18, s59, v161
	v_med3_f32 v17, v19, s59, v161
	v_pk_mul_f32 v[12:13], v[12:13], v[32:33] op_sel_hi:[1,0]
	v_pk_fma_f32 v[8:9], v[8:9], s[18:19], v[128:129] op_sel_hi:[1,0,1]
	v_cvt_pk_fp8_f32 v27, v16, v17 op_sel:[0,0,1]
	v_pk_mul_f32 v[14:15], v[14:15], v[32:33] op_sel_hi:[1,0]
	v_pk_mul_f32 v[16:17], v[8:9], v[32:33] op_sel_hi:[1,0]
	v_med3_f32 v9, v12, s59, v161
	v_med3_f32 v12, v13, s59, v161
	v_mov_b32_e32 v8, v145
	v_med3_f32 v13, v14, s59, v161
	v_med3_f32 v14, v15, s59, v161
	v_cvt_pk_fp8_f32 v8, v9, v12
	v_med3_f32 v12, v16, s59, v161
	v_med3_f32 v15, v17, s59, v161
	v_mov_b32_e32 v9, v145
	v_cvt_pk_fp8_f32 v9, v12, v15
	v_pk_fma_f32 v[10:11], v[10:11], s[18:19], v[130:131] op_sel_hi:[1,0,1]
	v_pk_fma_f32 v[116:117], v[116:117], s[18:19], v[140:141] op_sel_hi:[1,0,1]
	v_pk_fma_f32 v[84:85], v[84:85], s[18:19], v[140:141] op_sel_hi:[1,0,1]
	v_pk_fma_f32 v[52:53], v[52:53], s[18:19], v[140:141] op_sel_hi:[1,0,1]
	v_pk_fma_f32 v[20:21], v[20:21], s[18:19], v[140:141] op_sel_hi:[1,0,1]
	v_pk_mul_f32 v[10:11], v[10:11], v[32:33] op_sel_hi:[1,0]
	v_pk_fma_f32 v[4:5], v[4:5], s[18:19], v[132:133] op_sel_hi:[1,0,1]
	v_pk_fma_f32 v[0:1], v[0:1], s[18:19], v[128:129] op_sel_hi:[1,0,1]
	v_pk_mul_f32 v[116:117], v[116:117], v[124:125] op_sel_hi:[1,0]
	v_pk_mul_f32 v[84:85], v[84:85], v[92:93] op_sel_hi:[1,0]
	v_pk_mul_f32 v[52:53], v[52:53], v[60:61] op_sel_hi:[1,0]
	v_pk_mul_f32 v[20:21], v[20:21], v[28:29] op_sel_hi:[1,0]
	v_med3_f32 v10, v10, s59, v161
	v_med3_f32 v11, v11, s59, v161
	v_pk_mul_f32 v[4:5], v[4:5], v[28:29] op_sel_hi:[1,0]
	v_pk_mul_f32 v[0:1], v[0:1], v[28:29] op_sel_hi:[1,0]
	v_med3_f32 v116, v116, s59, v161
	v_med3_f32 v117, v117, s59, v161
	v_mov_b32_e32 v122, v145
	v_med3_f32 v84, v84, s59, v161
	v_med3_f32 v85, v85, s59, v161
	v_mov_b32_e32 v90, v145
	v_med3_f32 v52, v52, s59, v161
	v_med3_f32 v53, v53, s59, v161
	v_mov_b32_e32 v58, v145
	v_med3_f32 v20, v20, s59, v161
	v_med3_f32 v21, v21, s59, v161
	v_mov_b32_e32 v26, v145
	v_cvt_pk_fp8_f32 v9, v10, v11 op_sel:[0,0,1]
	v_med3_f32 v4, v4, s59, v161
	v_med3_f32 v5, v5, s59, v161
	v_mov_b32_e32 v10, v145
	v_med3_f32 v0, v0, s59, v161
	v_med3_f32 v1, v1, s59, v161
	v_mov_b32_e32 v11, v145
	v_cvt_pk_fp8_f32 v122, v116, v117
	v_pk_fma_f32 v[102:103], v[102:103], s[18:19], v[134:135] op_sel_hi:[1,0,1]
	v_cvt_pk_fp8_f32 v90, v84, v85
	v_pk_fma_f32 v[70:71], v[70:71], s[18:19], v[134:135] op_sel_hi:[1,0,1]
	v_cvt_pk_fp8_f32 v58, v52, v53
	v_cvt_pk_fp8_f32 v26, v20, v21
	v_cvt_pk_fp8_f32 v10, v4, v5
	v_cvt_pk_fp8_f32 v11, v0, v1
	v_pk_fma_f32 v[118:119], v[118:119], s[18:19], v[142:143] op_sel_hi:[1,0,1]
	v_pk_mul_f32 v[102:103], v[102:103], v[124:125] op_sel_hi:[1,0]
	v_pk_fma_f32 v[86:87], v[86:87], s[18:19], v[142:143] op_sel_hi:[1,0,1]
	v_pk_mul_f32 v[70:71], v[70:71], v[92:93] op_sel_hi:[1,0]
	v_pk_fma_f32 v[54:55], v[54:55], s[18:19], v[142:143] op_sel_hi:[1,0,1]
	v_pk_fma_f32 v[38:39], v[38:39], s[18:19], v[134:135] op_sel_hi:[1,0,1]
	v_pk_fma_f32 v[22:23], v[22:23], s[18:19], v[142:143] op_sel_hi:[1,0,1]
	v_pk_fma_f32 v[6:7], v[6:7], s[18:19], v[134:135] op_sel_hi:[1,0,1]
	v_pk_fma_f32 v[2:3], v[2:3], s[18:19], v[130:131] op_sel_hi:[1,0,1]
	v_pk_mul_f32 v[118:119], v[118:119], v[124:125] op_sel_hi:[1,0]
; #define LAS __attribute__((address_space(3)))
; #define PG8_DMA4(gp, lp) __builtin_amdgcn_global_load_lds((const unsigned*)(gp), (LAS unsigned*)(lp), 4, 0, 0)
;     DI void prefetch(const Unit& u, int wr, int wc, int lane, LAS unsigned char* st) const {
;         const float* rp = roww + u.pm * BM + wr * 64 + lane;
;         PG8_DMA4(rp, st); PG8_DMA4(rp + HALF, st + 256);
;         PG8_DMA4(b_down + (size_t)u.e * DM + u.pn * BM + (lane >> 5) * HALF + wc * 32 + (lane & 31), st + 512);
;     }
;     DI void operator()(const f32x4 (&acc)[2][2][4][2], const Unit& u, int wr, int wc, int fr, int fq, const LAS unsigned char* st) const {
;     ...
;             for (int mp = 0; mp < 2; ++mp) {
;                 const float wA = *(const LAS float*)(st + ai * 256 + ((2 * mp) * 16 + fr) * 4) * 16.0f, wB = *(const LAS float*)(st + ai * 256 + ((2 * mp + 1) * 16 + fr) * 4) * 16.0f;
;                 unsigned char* rowp = YB + (size_t)(row0 + ai * HALF + (2 * mp + (fq & 1)) * 16) * DM + (col0 - 8 * (fq & 1));
; #pragma unroll
;                 for (int bj = 0; bj < 2; ++bj) { u32x2 w2[2];
; #pragma unroll
;                     for (int mm = 0; mm < 2; ++mm) { const int m = 2 * mp + mm; const float w8 = mm ? wB : wA;
;                         const f32x4 v0 = (acc[ai][bj][m][0] * (1.0f / 128.0f) + bv[bj][0]) * w8, v1 = (acc[ai][bj][m][1] * (1.0f / 128.0f) + bv[bj][1]) * w8;
;                         w2[mm].x = pk4_fp8m(v0[0], v0[1], v0[2], v0[3]); w2[mm].y = pk4_fp8m(v1[0], v1[1], v1[2], v1[3]); }
;                     *(u32x4*)(rowp + bj * HALF) = pair16(w2[0], w2[1]); } }
	v_med3_f32 v102, v102, s59, v161
	v_med3_f32 v103, v103, s59, v161
	v_pk_mul_f32 v[86:87], v[86:87], v[92:93] op_sel_hi:[1,0]
	v_med3_f32 v70, v70, s59, v161
	v_med3_f32 v71, v71, s59, v161
	v_pk_mul_f32 v[54:55], v[54:55], v[60:61] op_sel_hi:[1,0]
	v_pk_mul_f32 v[38:39], v[38:39], v[60:61] op_sel_hi:[1,0]
	v_pk_mul_f32 v[22:23], v[22:23], v[28:29] op_sel_hi:[1,0]
	v_pk_mul_f32 v[6:7], v[6:7], v[28:29] op_sel_hi:[1,0]
	v_pk_mul_f32 v[2:3], v[2:3], v[28:29] op_sel_hi:[1,0]
	v_med3_f32 v118, v118, s59, v161
	v_med3_f32 v119, v119, s59, v161
	v_cvt_pk_fp8_f32 v106, v102, v103 op_sel:[0,0,1]
	v_or_b32_e32 v102, 32, v170
	v_med3_f32 v86, v86, s59, v161
	v_med3_f32 v87, v87, s59, v161
	v_cvt_pk_fp8_f32 v74, v70, v71 op_sel:[0,0,1]
	v_add_u32_e32 v70, 0x80, v168
	v_med3_f32 v54, v54, s59, v161
	v_med3_f32 v55, v55, s59, v161
	v_med3_f32 v38, v38, s59, v161
	v_med3_f32 v39, v39, s59, v161
	v_med3_f32 v22, v22, s59, v161
	v_med3_f32 v23, v23, s59, v161
	v_med3_f32 v6, v6, s59, v161
	v_med3_f32 v7, v7, s59, v161
	v_med3_f32 v0, v2, s59, v161
	v_med3_f32 v1, v3, s59, v161
	v_or_b32_e32 v164, v170, v168
	v_cvt_pk_fp8_f32 v120, v125, v126 op_sel:[0,0,1]
	v_cvt_pk_fp8_f32 v122, v118, v119 op_sel:[0,0,1]
	v_cvt_pk_fp8_f32 v104, v109, v110 op_sel:[0,0,1]
	v_or_b32_e32 v98, v102, v168
	v_cvt_pk_fp8_f32 v88, v93, v94 op_sel:[0,0,1]
	v_cvt_pk_fp8_f32 v90, v86, v87 op_sel:[0,0,1]
	v_cvt_pk_fp8_f32 v72, v77, v78 op_sel:[0,0,1]
	v_or_b32_e32 v66, v170, v70
	v_cvt_pk_fp8_f32 v56, v61, v62 op_sel:[0,0,1]
	v_cvt_pk_fp8_f32 v58, v54, v55 op_sel:[0,0,1]
	v_cvt_pk_fp8_f32 v40, v45, v46 op_sel:[0,0,1]
	v_cvt_pk_fp8_f32 v42, v38, v39 op_sel:[0,0,1]
	v_or_b32_e32 v34, v102, v70
	v_cvt_pk_fp8_f32 v24, v29, v30 op_sel:[0,0,1]
	v_cvt_pk_fp8_f32 v26, v22, v23 op_sel:[0,0,1]
	v_cvt_pk_fp8_f32 v8, v13, v14 op_sel:[0,0,1]
	v_cvt_pk_fp8_f32 v10, v6, v7 op_sel:[0,0,1]
	v_cvt_pk_fp8_f32 v11, v0, v1 op_sel:[0,0,1]
	v_ashrrev_i32_e32 v165, 31, v164
	v_ashrrev_i32_e32 v99, 31, v98
	v_ashrrev_i32_e32 v67, 31, v66
	v_ashrrev_i32_e32 v35, 31, v34
	v_sub_u32_e32 v148, v149, v148
	v_lshlrev_b64 v[164:165], 11, v[164:165]
	v_lshlrev_b64 v[98:99], 11, v[98:99]
	v_lshlrev_b64 v[66:67], 11, v[66:67]
	v_lshlrev_b64 v[34:35], 11, v[34:35]
	v_ashrrev_i32_e32 v149, 31, v148
	v_lshl_add_u64 v[164:165], s[12:13], 0, v[164:165]
	v_lshl_add_u64 v[98:99], s[12:13], 0, v[98:99]
	v_lshl_add_u64 v[66:67], s[12:13], 0, v[66:67]
	v_lshl_add_u64 v[34:35], s[12:13], 0, v[34:35]
	v_lshl_add_u64 v[164:165], v[164:165], 0, v[148:149]
	v_permlane16_swap_b32_e32 v120, v122
	v_permlane16_swap_b32_e32 v121, v123
	v_permlane16_swap_b32_e32 v104, v106
	v_permlane16_swap_b32_e32 v105, v107
	v_lshl_add_u64 v[98:99], v[98:99], 0, v[148:149]
	v_permlane16_swap_b32_e32 v88, v90
	v_permlane16_swap_b32_e32 v89, v91
	v_permlane16_swap_b32_e32 v72, v74
	v_permlane16_swap_b32_e32 v73, v75
	v_lshl_add_u64 v[66:67], v[66:67], 0, v[148:149]
	v_permlane16_swap_b32_e32 v56, v58
	v_permlane16_swap_b32_e32 v57, v59
	v_permlane16_swap_b32_e32 v40, v42
	v_permlane16_swap_b32_e32 v41, v43
	v_lshl_add_u64 v[34:35], v[34:35], 0, v[148:149]
	v_permlane16_swap_b32_e32 v24, v26
	v_permlane16_swap_b32_e32 v25, v27
	v_permlane16_swap_b32_e32 v8, v10
	v_permlane16_swap_b32_e32 v9, v11
	s_and_b64 vcc, exec, s[2:3]
	s_mov_b64 s[0:1], -1
	global_store_dwordx4 v[164:165], v[120:123], off
	global_store_dwordx4 v[164:165], v[104:107], off offset:128
	global_store_dwordx4 v[98:99], v[88:91], off
	global_store_dwordx4 v[98:99], v[72:75], off offset:128
	global_store_dwordx4 v[66:67], v[56:59], off
	global_store_dwordx4 v[66:67], v[40:43], off offset:128
	global_store_dwordx4 v[34:35], v[24:27], off
	global_store_dwordx4 v[34:35], v[8:11], off offset:128
	s_waitcnt vmcnt(8)
	s_cbranch_vccnz .LBB0_1155
	s_lshl_b32 s0, s22, 8
	s_ashr_i32 s1, s0, 31
	s_lshl_b64 s[0:1], s[0:1], 2
	v_mov_b32_e32 v0, v224
	s_add_u32 s0, s55, s0
	s_addc_u32 s1, s56, s1
	v_ashrrev_i32_e32 v1, 31, v0
	s_mov_b32 m0, s29
	v_lshl_add_u64 v[2:3], v[0:1], 2, s[0:1]
	global_load_lds_dword v[2:3], off
	s_add_i32 m0, s29, 0x100
	s_lshl_b64 s[0:1], s[26:27], 13
	s_add_u32 s2, s90, s0
	s_addc_u32 s3, s91, s1
	s_lshl_b32 s0, s20, 8
	s_ashr_i32 s1, s0, 31
	v_lshl_add_u64 v[2:3], v[2:3], 0, s[8:9]
	s_lshl_b64 s[0:1], s[0:1], 2
	v_lshlrev_b32_e32 v1, 2, v0
	global_load_lds_dword v[2:3], off
	s_add_u32 s0, s2, s0
	v_and_b32_e32 v2, 0xffffff80, v1
	s_addc_u32 s1, s3, s1
	v_ashrrev_i32_e32 v3, 31, v2
	v_lshl_add_u64 v[2:3], v[2:3], 2, s[0:1]
	v_and_b32_e32 v0, 31, v0
	v_lshl_add_u64 v[2:3], v[2:3], 0, s[6:7]
	v_lshlrev_b32_e32 v144, 2, v0
	v_lshl_add_u64 v[0:1], v[2:3], 0, v[144:145]
	s_mov_b32 m0, s60
	s_andn2_b64 vcc, exec, s[10:11]
	global_load_lds_dword v[0:1], off
	s_cbranch_vccnz .LBB0_1154
	s_barrier
	s_branch .LBB0_1154
